# sc1 write-through on all 16-byte global stores (less dirty L2 at grid barriers)
# speedup vs baseline: 1.0086x; 1.0086x over previous
.LBB0_14:
	v_add_u32_e32 v28, s33, v71
	v_add_u32_e32 v4, 0x41, v28
	v_ashrrev_i32_e32 v29, 31, v28
	v_ashrrev_i32_e32 v5, 31, v4
	v_lshlrev_b64 v[0:1], 12, v[28:29]
	v_lshlrev_b64 v[4:5], 12, v[4:5]
	v_lshl_add_u64 v[0:1], v[72:73], 0, v[0:1]
	v_lshl_add_u64 v[4:5], v[72:73], 0, v[4:5]
	global_load_dwordx4 v[32:35], v[0:1], off nt
	global_load_dwordx4 v[8:11], v[4:5], off nt
	v_or_b32_e32 v0, 1, v28
	v_add_u32_e32 v4, 0x42, v28
	v_ashrrev_i32_e32 v1, 31, v0
	v_ashrrev_i32_e32 v5, 31, v4
	v_lshlrev_b64 v[0:1], 12, v[0:1]
	v_lshlrev_b64 v[4:5], 12, v[4:5]
	v_lshl_add_u64 v[0:1], v[72:73], 0, v[0:1]
	v_lshl_add_u64 v[4:5], v[72:73], 0, v[4:5]
	global_load_dwordx4 v[36:39], v[0:1], off nt
	global_load_dwordx4 v[16:19], v[4:5], off nt
	v_or_b32_e32 v0, 2, v28
	v_add_u32_e32 v4, 0x43, v28
	v_ashrrev_i32_e32 v1, 31, v0
	v_ashrrev_i32_e32 v5, 31, v4
	v_lshlrev_b64 v[0:1], 12, v[0:1]
	v_lshlrev_b64 v[4:5], 12, v[4:5]
	v_lshl_add_u64 v[0:1], v[72:73], 0, v[0:1]
	v_lshl_add_u64 v[4:5], v[72:73], 0, v[4:5]
	global_load_dwordx4 v[44:47], v[0:1], off nt
	global_load_dwordx4 v[24:27], v[4:5], off nt
	v_or_b32_e32 v0, 3, v28
	v_add_u32_e32 v4, 0x44, v28
	v_ashrrev_i32_e32 v1, 31, v0
	v_ashrrev_i32_e32 v5, 31, v4
	v_lshlrev_b64 v[0:1], 12, v[0:1]
	v_lshlrev_b64 v[4:5], 12, v[4:5]
	v_lshl_add_u64 v[0:1], v[72:73], 0, v[0:1]
	v_lshl_add_u64 v[4:5], v[72:73], 0, v[4:5]
	global_load_dwordx4 v[52:55], v[0:1], off nt
	v_add_u32_e32 v12, 0x45, v28
	global_load_dwordx4 v[4:7], v[4:5], off nt
	v_or_b32_e32 v0, 4, v28
	v_ashrrev_i32_e32 v1, 31, v0
	v_ashrrev_i32_e32 v13, 31, v12
	v_lshlrev_b64 v[0:1], 12, v[0:1]
	v_lshlrev_b64 v[12:13], 12, v[12:13]
	v_lshl_add_u64 v[0:1], v[72:73], 0, v[0:1]
	v_lshl_add_u64 v[12:13], v[72:73], 0, v[12:13]
	global_load_dwordx4 v[40:43], v[0:1], off nt
	v_add_u32_e32 v20, 0x46, v28
	global_load_dwordx4 v[12:15], v[12:13], off nt
	v_or_b32_e32 v0, 5, v28
	v_ashrrev_i32_e32 v1, 31, v0
	v_ashrrev_i32_e32 v21, 31, v20
	v_lshlrev_b64 v[0:1], 12, v[0:1]
	v_lshlrev_b64 v[20:21], 12, v[20:21]
	v_lshl_add_u64 v[0:1], v[72:73], 0, v[0:1]
	v_lshl_add_u64 v[20:21], v[72:73], 0, v[20:21]
	global_load_dwordx4 v[48:51], v[0:1], off nt
	v_mov_b32_e32 v128, 0
	global_load_dwordx4 v[20:23], v[20:21], off nt
	v_or_b32_e32 v0, 6, v28
	v_ashrrev_i32_e32 v1, 31, v0
	v_lshlrev_b64 v[0:1], 12, v[0:1]
	v_lshl_add_u64 v[0:1], v[72:73], 0, v[0:1]
	global_load_dwordx4 v[56:59], v[0:1], off nt
	v_or_b32_e32 v0, 7, v28
	v_ashrrev_i32_e32 v1, 31, v0
	v_lshlrev_b64 v[0:1], 12, v[0:1]
	v_lshl_add_u64 v[0:1], v[72:73], 0, v[0:1]
	global_load_dwordx4 v[60:63], v[0:1], off nt
	v_add_u32_e32 v0, 64, v28
	v_ashrrev_i32_e32 v1, 31, v0
	v_lshlrev_b64 v[0:1], 12, v[0:1]
	v_lshl_add_u64 v[0:1], v[72:73], 0, v[0:1]
	global_load_dwordx4 v[0:3], v[0:1], off nt
	v_add_u32_e32 v28, 0x47, v28
	v_ashrrev_i32_e32 v29, 31, v28
	v_lshlrev_b64 v[28:29], 12, v[28:29]
	v_lshl_add_u64 v[28:29], v[72:73], 0, v[28:29]
	global_load_dwordx4 v[28:31], v[28:29], off nt
	v_mov_b32_e32 v129, 0
	s_and_b64 vcc, exec, s[16:17]
	s_mov_b64 s[16:17], 0
	s_waitcnt vmcnt(15)
	v_mul_f32_e32 v32, 0x42000000, v32
	v_mul_f32_e32 v33, 0x42000000, v33
	v_mul_f32_e32 v34, 0x42000000, v34
	v_mul_f32_e32 v35, 0x42000000, v35
	s_waitcnt vmcnt(14)
	v_mul_f32_e32 v8, 0x42000000, v8
	s_waitcnt vmcnt(13)
	v_mul_f32_e32 v36, 0x42000000, v36
	v_cvt_pk_fp8_f32 v128, v32, v36
	s_waitcnt vmcnt(12)
	v_mul_f32_e32 v16, 0x42000000, v16
	s_waitcnt vmcnt(11)
	v_mul_f32_e32 v44, 0x42000000, v44
	s_waitcnt vmcnt(10)
	v_mul_f32_e32 v24, 0x42000000, v24
	s_waitcnt vmcnt(9)
	v_mul_f32_e32 v52, 0x42000000, v52
	v_cvt_pk_fp8_f32 v128, v44, v52 op_sel:[0,0,1]
	s_waitcnt vmcnt(7)
	v_mul_f32_e32 v32, 0x42000000, v40
	s_waitcnt vmcnt(5)
	v_mul_f32_e32 v36, 0x42000000, v48
	v_cvt_pk_fp8_f32 v129, v32, v36
	v_mul_f32_e32 v36, 0x42000000, v37
	v_mov_b32_e32 v32, 0
	v_cvt_pk_fp8_f32 v32, v33, v36
	v_mul_f32_e32 v37, 0x42000000, v45
	v_mul_f32_e32 v36, 0x42000000, v41
	s_waitcnt vmcnt(3)
	v_mul_f32_e32 v40, 0x42000000, v56
	v_mov_b32_e32 v33, 0
	v_mul_f32_e32 v41, 0x42000000, v57
	s_waitcnt vmcnt(2)
	v_mul_f32_e32 v44, 0x42000000, v60
	v_cvt_pk_fp8_f32 v129, v40, v44 op_sel:[0,0,1]
	v_mul_f32_e32 v44, 0x42000000, v53
	v_cvt_pk_fp8_f32 v32, v37, v44 op_sel:[0,0,1]
	v_mul_f32_e32 v37, 0x42000000, v49
	v_cvt_pk_fp8_f32 v33, v36, v37
	v_mul_f32_e32 v37, 0x42000000, v38
	v_mov_b32_e32 v36, 0
	v_cvt_pk_fp8_f32 v36, v34, v37
	v_mul_f32_e32 v44, 0x42000000, v61
	v_cvt_pk_fp8_f32 v33, v41, v44 op_sel:[0,0,1]
	v_mul_f32_e32 v38, 0x42000000, v46
	v_mul_f32_e32 v41, 0x42000000, v54
	v_cvt_pk_fp8_f32 v36, v38, v41 op_sel:[0,0,1]
	v_mul_f32_e32 v34, 0x42000000, v42
	v_mul_f32_e32 v38, 0x42000000, v50
	v_mov_b32_e32 v37, 0
	v_cvt_pk_fp8_f32 v37, v34, v38
	v_mul_f32_e32 v38, 0x42000000, v39
	v_mov_b32_e32 v34, 0
	v_cvt_pk_fp8_f32 v34, v35, v38
	v_mul_f32_e32 v41, 0x42000000, v58
	v_mul_f32_e32 v42, 0x42000000, v62
	v_cvt_pk_fp8_f32 v37, v41, v42 op_sel:[0,0,1]
	v_mul_f32_e32 v39, 0x42000000, v47
	v_mul_f32_e32 v41, 0x42000000, v55
	v_cvt_pk_fp8_f32 v34, v39, v41 op_sel:[0,0,1]
	v_mul_f32_e32 v38, 0x42000000, v43
	v_mul_f32_e32 v39, 0x42000000, v51
	v_mov_b32_e32 v35, 0
	v_cvt_pk_fp8_f32 v35, v38, v39
	s_waitcnt vmcnt(1)
	v_mul_f32_e32 v0, 0x42000000, v0
	v_mov_b32_e32 v38, 0
	v_cvt_pk_fp8_f32 v38, v0, v8
	v_mul_f32_e32 v0, 0x42000000, v4
	v_mul_f32_e32 v4, 0x42000000, v12
	v_mov_b32_e32 v39, 0
	v_cvt_pk_fp8_f32 v39, v0, v4
	v_mul_f32_e32 v1, 0x42000000, v1
	v_mul_f32_e32 v4, 0x42000000, v9
	v_mov_b32_e32 v0, 0
	v_cvt_pk_fp8_f32 v0, v1, v4
	v_mul_f32_e32 v4, 0x42000000, v5
	v_mul_f32_e32 v5, 0x42000000, v13
	v_mov_b32_e32 v1, 0
	v_cvt_pk_fp8_f32 v1, v4, v5
	v_mul_f32_e32 v8, 0x42000000, v20
	s_waitcnt vmcnt(0)
	v_mul_f32_e32 v12, 0x42000000, v28
	v_cvt_pk_fp8_f32 v39, v8, v12 op_sel:[0,0,1]
	v_mul_f32_e32 v8, 0x42000000, v17
	v_mul_f32_e32 v9, 0x42000000, v25
	v_cvt_pk_fp8_f32 v0, v8, v9 op_sel:[0,0,1]
	v_mul_f32_e32 v8, 0x42000000, v21
	v_mul_f32_e32 v9, 0x42000000, v29
	v_cvt_pk_fp8_f32 v1, v8, v9 op_sel:[0,0,1]
	v_add_u32_e32 v40, s33, v125
	v_mul_f32_e32 v4, 0x42000000, v18
	v_mul_f32_e32 v5, 0x42000000, v26
	ds_write2_b64 v40, v[32:33], v[0:1] offset0:34 offset1:42
	v_mul_f32_e32 v1, 0x42000000, v2
	v_mul_f32_e32 v2, 0x42000000, v10
	v_mov_b32_e32 v0, 0
	v_cvt_pk_fp8_f32 v0, v1, v2
	v_mul_f32_e32 v2, 0x42000000, v6
	v_mov_b32_e32 v1, 0
	v_mul_f32_e32 v6, 0x42000000, v30
	v_cvt_pk_fp8_f32 v0, v4, v5 op_sel:[0,0,1]
	v_mul_f32_e32 v4, 0x42000000, v14
	v_cvt_pk_fp8_f32 v1, v2, v4
	v_mul_f32_e32 v5, 0x42000000, v22
	v_mul_f32_e32 v2, 0x42000000, v11
	v_mul_f32_e32 v4, 0x42000000, v27
	v_cvt_pk_fp8_f32 v1, v5, v6 op_sel:[0,0,1]
	v_mul_f32_e32 v41, 0x42000000, v59
	v_mul_f32_e32 v42, 0x42000000, v63
	v_mul_f32_e32 v5, 0x42000000, v31
	ds_write2_b64 v40, v[36:37], v[0:1] offset0:68 offset1:76
	v_mul_f32_e32 v1, 0x42000000, v3
	v_mov_b32_e32 v0, 0
	v_cvt_pk_fp8_f32 v0, v1, v2
	v_mul_f32_e32 v3, 0x42000000, v19
	v_mul_f32_e32 v2, 0x42000000, v7
	v_mov_b32_e32 v1, 0
	v_cvt_pk_fp8_f32 v0, v3, v4 op_sel:[0,0,1]
	v_mul_f32_e32 v3, 0x42000000, v15
	v_cvt_pk_fp8_f32 v1, v2, v3
	v_mul_f32_e32 v4, 0x42000000, v23
	v_cvt_pk_fp8_f32 v35, v41, v42 op_sel:[0,0,1]
	v_cvt_pk_fp8_f32 v38, v16, v24 op_sel:[0,0,1]
	v_cvt_pk_fp8_f32 v1, v4, v5 op_sel:[0,0,1]
	s_movk_i32 s33, 0x80
	ds_write2_b64 v40, v[128:129], v[38:39] offset1:8
	ds_write2_b64 v40, v[34:35], v[0:1] offset0:102 offset1:110
	s_cbranch_vccnz .LBB0_14
	s_add_u32 s14, s18, s14
	s_waitcnt lgkmcnt(0)
	s_barrier
	v_add_u32_e32 v0, v77, v66
	s_addc_u32 s15, s19, s15
	ds_read_b128 v[0:3], v0
	v_add_u32_e32 v4, s2, v76
	s_add_u32 s14, s14, s31
	v_ashrrev_i32_e32 v5, 31, v4
	s_addc_u32 s15, s15, 0
	v_lshlrev_b64 v[4:5], 10, v[4:5]
	v_lshl_add_u64 v[4:5], s[14:15], 0, v[4:5]
	v_lshl_add_u64 v[8:9], v[4:5], 0, v[66:67]
	v_add_u32_e32 v4, v79, v66
	ds_read_b128 v[4:7], v4
	s_waitcnt lgkmcnt(1)
	global_store_dwordx4 v[8:9], v[0:3], off sc1
	s_nop 1
	v_add_u32_e32 v0, s2, v78
	v_ashrrev_i32_e32 v1, 31, v0
	v_lshlrev_b64 v[0:1], 10, v[0:1]
	v_lshl_add_u64 v[0:1], s[14:15], 0, v[0:1]
	v_lshl_add_u64 v[0:1], v[0:1], 0, v[66:67]
	s_waitcnt lgkmcnt(0)
	global_store_dwordx4 v[0:1], v[4:7], off sc1
	v_add_u32_e32 v0, v81, v66
	ds_read_b128 v[0:3], v0
	v_add_u32_e32 v4, s2, v80
	v_ashrrev_i32_e32 v5, 31, v4
	v_lshlrev_b64 v[4:5], 10, v[4:5]
	v_lshl_add_u64 v[4:5], s[14:15], 0, v[4:5]
	v_lshl_add_u64 v[8:9], v[4:5], 0, v[66:67]
	v_add_u32_e32 v4, v83, v66
	ds_read_b128 v[4:7], v4
	s_waitcnt lgkmcnt(1)
	global_store_dwordx4 v[8:9], v[0:3], off sc1
	s_nop 1
	v_add_u32_e32 v0, s2, v82
	v_ashrrev_i32_e32 v1, 31, v0
	v_lshlrev_b64 v[0:1], 10, v[0:1]
	v_lshl_add_u64 v[0:1], s[14:15], 0, v[0:1]
	v_lshl_add_u64 v[0:1], v[0:1], 0, v[66:67]
	s_waitcnt lgkmcnt(0)
	global_store_dwordx4 v[0:1], v[4:7], off sc1
	v_add_u32_e32 v0, v85, v66
	ds_read_b128 v[0:3], v0
	v_add_u32_e32 v4, s2, v84
	v_ashrrev_i32_e32 v5, 31, v4
	v_lshlrev_b64 v[4:5], 10, v[4:5]
	v_lshl_add_u64 v[4:5], s[14:15], 0, v[4:5]
	v_lshl_add_u64 v[8:9], v[4:5], 0, v[66:67]
	v_add_u32_e32 v4, v87, v66
	ds_read_b128 v[4:7], v4
	s_waitcnt lgkmcnt(1)
	global_store_dwordx4 v[8:9], v[0:3], off sc1
	s_nop 1
	v_add_u32_e32 v0, s2, v86
	v_ashrrev_i32_e32 v1, 31, v0
	v_lshlrev_b64 v[0:1], 10, v[0:1]
	v_lshl_add_u64 v[0:1], s[14:15], 0, v[0:1]
	v_lshl_add_u64 v[0:1], v[0:1], 0, v[66:67]
	s_waitcnt lgkmcnt(0)
	global_store_dwordx4 v[0:1], v[4:7], off sc1
	v_add_u32_e32 v0, v89, v66
	ds_read_b128 v[0:3], v0
	v_add_u32_e32 v4, s2, v88
	v_ashrrev_i32_e32 v5, 31, v4
	v_lshlrev_b64 v[4:5], 10, v[4:5]
	v_lshl_add_u64 v[4:5], s[14:15], 0, v[4:5]
	v_lshl_add_u64 v[8:9], v[4:5], 0, v[66:67]
	v_add_u32_e32 v4, v124, v66
	ds_read_b128 v[4:7], v4
	s_waitcnt lgkmcnt(1)
	global_store_dwordx4 v[8:9], v[0:3], off sc1
	s_nop 1
	v_add_u32_e32 v0, s2, v90
	v_ashrrev_i32_e32 v1, 31, v0
	v_lshlrev_b64 v[0:1], 10, v[0:1]
	v_lshl_add_u64 v[0:1], s[14:15], 0, v[0:1]
	v_lshl_add_u64 v[0:1], v[0:1], 0, v[66:67]
	s_waitcnt lgkmcnt(0)
	global_store_dwordx4 v[0:1], v[4:7], off sc1
	s_waitcnt lgkmcnt(0)
	s_barrier

.LBB0_20:
	v_add_u32_e32 v28, s31, v71
	v_add_u32_e32 v4, 0x41, v28
	v_ashrrev_i32_e32 v29, 31, v28
	v_ashrrev_i32_e32 v5, 31, v4
	v_lshlrev_b64 v[0:1], 13, v[28:29]
	v_lshlrev_b64 v[4:5], 13, v[4:5]
	v_lshl_add_u64 v[0:1], v[72:73], 0, v[0:1]
	v_lshl_add_u64 v[4:5], v[72:73], 0, v[4:5]
	global_load_dwordx4 v[32:35], v[0:1], off nt
	global_load_dwordx4 v[8:11], v[4:5], off nt
	v_or_b32_e32 v0, 1, v28
	v_add_u32_e32 v4, 0x42, v28
	v_ashrrev_i32_e32 v1, 31, v0
	v_ashrrev_i32_e32 v5, 31, v4
	v_lshlrev_b64 v[0:1], 13, v[0:1]
	v_lshlrev_b64 v[4:5], 13, v[4:5]
	v_lshl_add_u64 v[0:1], v[72:73], 0, v[0:1]
	v_lshl_add_u64 v[4:5], v[72:73], 0, v[4:5]
	global_load_dwordx4 v[36:39], v[0:1], off nt
	global_load_dwordx4 v[16:19], v[4:5], off nt
	v_or_b32_e32 v0, 2, v28
	v_add_u32_e32 v4, 0x43, v28
	v_ashrrev_i32_e32 v1, 31, v0
	v_ashrrev_i32_e32 v5, 31, v4
	v_lshlrev_b64 v[0:1], 13, v[0:1]
	v_lshlrev_b64 v[4:5], 13, v[4:5]
	v_lshl_add_u64 v[0:1], v[72:73], 0, v[0:1]
	v_lshl_add_u64 v[4:5], v[72:73], 0, v[4:5]
	global_load_dwordx4 v[44:47], v[0:1], off nt
	global_load_dwordx4 v[24:27], v[4:5], off nt
	v_or_b32_e32 v0, 3, v28
	v_add_u32_e32 v4, 0x44, v28
	v_ashrrev_i32_e32 v1, 31, v0
	v_ashrrev_i32_e32 v5, 31, v4
	v_lshlrev_b64 v[0:1], 13, v[0:1]
	v_lshlrev_b64 v[4:5], 13, v[4:5]
	v_lshl_add_u64 v[0:1], v[72:73], 0, v[0:1]
	v_lshl_add_u64 v[4:5], v[72:73], 0, v[4:5]
	global_load_dwordx4 v[52:55], v[0:1], off nt
	v_add_u32_e32 v12, 0x45, v28
	global_load_dwordx4 v[4:7], v[4:5], off nt
	v_or_b32_e32 v0, 4, v28
	v_ashrrev_i32_e32 v1, 31, v0
	v_ashrrev_i32_e32 v13, 31, v12
	v_lshlrev_b64 v[0:1], 13, v[0:1]
	v_lshlrev_b64 v[12:13], 13, v[12:13]
	v_lshl_add_u64 v[0:1], v[72:73], 0, v[0:1]
	v_lshl_add_u64 v[12:13], v[72:73], 0, v[12:13]
	global_load_dwordx4 v[40:43], v[0:1], off nt
	v_add_u32_e32 v20, 0x46, v28
	global_load_dwordx4 v[12:15], v[12:13], off nt
	v_or_b32_e32 v0, 5, v28
	v_ashrrev_i32_e32 v1, 31, v0
	v_ashrrev_i32_e32 v21, 31, v20
	v_lshlrev_b64 v[0:1], 13, v[0:1]
	v_lshlrev_b64 v[20:21], 13, v[20:21]
	v_lshl_add_u64 v[0:1], v[72:73], 0, v[0:1]
	v_lshl_add_u64 v[20:21], v[72:73], 0, v[20:21]
	global_load_dwordx4 v[48:51], v[0:1], off nt
	v_mov_b32_e32 v128, 0
	global_load_dwordx4 v[20:23], v[20:21], off nt
	v_or_b32_e32 v0, 6, v28
	v_ashrrev_i32_e32 v1, 31, v0
	v_lshlrev_b64 v[0:1], 13, v[0:1]
	v_lshl_add_u64 v[0:1], v[72:73], 0, v[0:1]
	global_load_dwordx4 v[56:59], v[0:1], off nt
	v_or_b32_e32 v0, 7, v28
	v_ashrrev_i32_e32 v1, 31, v0
	v_lshlrev_b64 v[0:1], 13, v[0:1]
	v_lshl_add_u64 v[0:1], v[72:73], 0, v[0:1]
	global_load_dwordx4 v[60:63], v[0:1], off nt
	v_add_u32_e32 v0, 64, v28
	v_ashrrev_i32_e32 v1, 31, v0
	v_lshlrev_b64 v[0:1], 13, v[0:1]
	v_lshl_add_u64 v[0:1], v[72:73], 0, v[0:1]
	global_load_dwordx4 v[0:3], v[0:1], off nt
	v_add_u32_e32 v28, 0x47, v28
	v_ashrrev_i32_e32 v29, 31, v28
	v_lshlrev_b64 v[28:29], 13, v[28:29]
	v_lshl_add_u64 v[28:29], v[72:73], 0, v[28:29]
	global_load_dwordx4 v[28:31], v[28:29], off nt
	v_mov_b32_e32 v129, 0
	s_and_b64 vcc, exec, s[14:15]
	s_mov_b64 s[14:15], 0
	s_waitcnt vmcnt(15)
	v_mul_f32_e32 v32, 0x42000000, v32
	v_mul_f32_e32 v33, 0x42000000, v33
	v_mul_f32_e32 v34, 0x42000000, v34
	v_mul_f32_e32 v35, 0x42000000, v35
	s_waitcnt vmcnt(14)
	v_mul_f32_e32 v8, 0x42000000, v8
	s_waitcnt vmcnt(13)
	v_mul_f32_e32 v36, 0x42000000, v36
	v_cvt_pk_fp8_f32 v128, v32, v36
	s_waitcnt vmcnt(12)
	v_mul_f32_e32 v16, 0x42000000, v16
	s_waitcnt vmcnt(11)
	v_mul_f32_e32 v44, 0x42000000, v44
	s_waitcnt vmcnt(10)
	v_mul_f32_e32 v24, 0x42000000, v24
	s_waitcnt vmcnt(9)
	v_mul_f32_e32 v52, 0x42000000, v52
	v_cvt_pk_fp8_f32 v128, v44, v52 op_sel:[0,0,1]
	s_waitcnt vmcnt(7)
	v_mul_f32_e32 v32, 0x42000000, v40
	s_waitcnt vmcnt(5)
	v_mul_f32_e32 v36, 0x42000000, v48
	v_cvt_pk_fp8_f32 v129, v32, v36
	v_mul_f32_e32 v36, 0x42000000, v37
	v_mov_b32_e32 v32, 0
	v_cvt_pk_fp8_f32 v32, v33, v36
	v_mul_f32_e32 v37, 0x42000000, v45
	v_mul_f32_e32 v36, 0x42000000, v41
	s_waitcnt vmcnt(3)
	v_mul_f32_e32 v40, 0x42000000, v56
	v_mov_b32_e32 v33, 0
	v_mul_f32_e32 v41, 0x42000000, v57
	s_waitcnt vmcnt(2)
	v_mul_f32_e32 v44, 0x42000000, v60
	v_cvt_pk_fp8_f32 v129, v40, v44 op_sel:[0,0,1]
	v_mul_f32_e32 v44, 0x42000000, v53
	v_cvt_pk_fp8_f32 v32, v37, v44 op_sel:[0,0,1]
	v_mul_f32_e32 v37, 0x42000000, v49
	v_cvt_pk_fp8_f32 v33, v36, v37
	v_mul_f32_e32 v37, 0x42000000, v38
	v_mov_b32_e32 v36, 0
	v_cvt_pk_fp8_f32 v36, v34, v37
	v_mul_f32_e32 v44, 0x42000000, v61
	v_cvt_pk_fp8_f32 v33, v41, v44 op_sel:[0,0,1]
	v_mul_f32_e32 v38, 0x42000000, v46
	v_mul_f32_e32 v41, 0x42000000, v54
	v_cvt_pk_fp8_f32 v36, v38, v41 op_sel:[0,0,1]
	v_mul_f32_e32 v34, 0x42000000, v42
	v_mul_f32_e32 v38, 0x42000000, v50
	v_mov_b32_e32 v37, 0
	v_cvt_pk_fp8_f32 v37, v34, v38
	v_mul_f32_e32 v38, 0x42000000, v39
	v_mov_b32_e32 v34, 0
	v_cvt_pk_fp8_f32 v34, v35, v38
	v_mul_f32_e32 v41, 0x42000000, v58
	v_mul_f32_e32 v42, 0x42000000, v62
	v_cvt_pk_fp8_f32 v37, v41, v42 op_sel:[0,0,1]
	v_mul_f32_e32 v39, 0x42000000, v47
	v_mul_f32_e32 v41, 0x42000000, v55
	v_cvt_pk_fp8_f32 v34, v39, v41 op_sel:[0,0,1]
	v_mul_f32_e32 v38, 0x42000000, v43
	v_mul_f32_e32 v39, 0x42000000, v51
	v_mov_b32_e32 v35, 0
	v_cvt_pk_fp8_f32 v35, v38, v39
	s_waitcnt vmcnt(1)
	v_mul_f32_e32 v0, 0x42000000, v0
	v_mov_b32_e32 v38, 0
	v_cvt_pk_fp8_f32 v38, v0, v8
	v_mul_f32_e32 v0, 0x42000000, v4
	v_mul_f32_e32 v4, 0x42000000, v12
	v_mov_b32_e32 v39, 0
	v_cvt_pk_fp8_f32 v39, v0, v4
	v_mul_f32_e32 v1, 0x42000000, v1
	v_mul_f32_e32 v4, 0x42000000, v9
	v_mov_b32_e32 v0, 0
	v_cvt_pk_fp8_f32 v0, v1, v4
	v_mul_f32_e32 v4, 0x42000000, v5
	v_mul_f32_e32 v5, 0x42000000, v13
	v_mov_b32_e32 v1, 0
	v_cvt_pk_fp8_f32 v1, v4, v5
	v_mul_f32_e32 v8, 0x42000000, v20
	s_waitcnt vmcnt(0)
	v_mul_f32_e32 v12, 0x42000000, v28
	v_cvt_pk_fp8_f32 v39, v8, v12 op_sel:[0,0,1]
	v_mul_f32_e32 v8, 0x42000000, v17
	v_mul_f32_e32 v9, 0x42000000, v25
	v_cvt_pk_fp8_f32 v0, v8, v9 op_sel:[0,0,1]
	v_mul_f32_e32 v8, 0x42000000, v21
	v_mul_f32_e32 v9, 0x42000000, v29
	v_cvt_pk_fp8_f32 v1, v8, v9 op_sel:[0,0,1]
	v_add_u32_e32 v40, s31, v125
	v_mul_f32_e32 v4, 0x42000000, v18
	v_mul_f32_e32 v5, 0x42000000, v26
	ds_write2_b64 v40, v[32:33], v[0:1] offset0:34 offset1:42
	v_mul_f32_e32 v1, 0x42000000, v2
	v_mul_f32_e32 v2, 0x42000000, v10
	v_mov_b32_e32 v0, 0
	v_cvt_pk_fp8_f32 v0, v1, v2
	v_mul_f32_e32 v2, 0x42000000, v6
	v_mov_b32_e32 v1, 0
	v_mul_f32_e32 v6, 0x42000000, v30
	v_cvt_pk_fp8_f32 v0, v4, v5 op_sel:[0,0,1]
	v_mul_f32_e32 v4, 0x42000000, v14
	v_cvt_pk_fp8_f32 v1, v2, v4
	v_mul_f32_e32 v5, 0x42000000, v22
	v_mul_f32_e32 v2, 0x42000000, v11
	v_mul_f32_e32 v4, 0x42000000, v27
	v_cvt_pk_fp8_f32 v1, v5, v6 op_sel:[0,0,1]
	v_mul_f32_e32 v41, 0x42000000, v59
	v_mul_f32_e32 v42, 0x42000000, v63
	v_mul_f32_e32 v5, 0x42000000, v31
	ds_write2_b64 v40, v[36:37], v[0:1] offset0:68 offset1:76
	v_mul_f32_e32 v1, 0x42000000, v3
	v_mov_b32_e32 v0, 0
	v_cvt_pk_fp8_f32 v0, v1, v2
	v_mul_f32_e32 v3, 0x42000000, v19
	v_mul_f32_e32 v2, 0x42000000, v7
	v_mov_b32_e32 v1, 0
	v_cvt_pk_fp8_f32 v0, v3, v4 op_sel:[0,0,1]
	v_mul_f32_e32 v3, 0x42000000, v15
	v_cvt_pk_fp8_f32 v1, v2, v3
	v_mul_f32_e32 v4, 0x42000000, v23
	v_cvt_pk_fp8_f32 v35, v41, v42 op_sel:[0,0,1]
	v_cvt_pk_fp8_f32 v38, v16, v24 op_sel:[0,0,1]
	v_cvt_pk_fp8_f32 v1, v4, v5 op_sel:[0,0,1]
	s_movk_i32 s31, 0x80
	ds_write2_b64 v40, v[128:129], v[38:39] offset1:8
	ds_write2_b64 v40, v[34:35], v[0:1] offset0:102 offset1:110
	s_cbranch_vccnz .LBB0_20
	s_lshl_b64 s[14:15], s[2:3], 21
	s_add_u32 s2, s21, s14
	s_waitcnt lgkmcnt(0)
	s_barrier
	v_add_u32_e32 v0, v77, v66
	s_addc_u32 s15, s22, s15
	ds_read_b128 v[0:3], v0
	v_add_u32_e32 v4, s16, v76
	s_add_u32 s14, s2, s17
	v_ashrrev_i32_e32 v5, 31, v4
	s_addc_u32 s15, s15, 0
	v_lshlrev_b64 v[4:5], 10, v[4:5]
	v_lshl_add_u64 v[4:5], s[14:15], 0, v[4:5]
	v_lshl_add_u64 v[8:9], v[4:5], 0, v[66:67]
	v_add_u32_e32 v4, v79, v66
	ds_read_b128 v[4:7], v4
	s_waitcnt lgkmcnt(1)
	global_store_dwordx4 v[8:9], v[0:3], off sc1
	s_nop 1
	v_add_u32_e32 v0, s16, v78
	v_ashrrev_i32_e32 v1, 31, v0
	v_lshlrev_b64 v[0:1], 10, v[0:1]
	v_lshl_add_u64 v[0:1], s[14:15], 0, v[0:1]
	v_lshl_add_u64 v[0:1], v[0:1], 0, v[66:67]
	s_waitcnt lgkmcnt(0)
	global_store_dwordx4 v[0:1], v[4:7], off sc1
	v_add_u32_e32 v0, v81, v66
	ds_read_b128 v[0:3], v0
	v_add_u32_e32 v4, s16, v80
	v_ashrrev_i32_e32 v5, 31, v4
	v_lshlrev_b64 v[4:5], 10, v[4:5]
	v_lshl_add_u64 v[4:5], s[14:15], 0, v[4:5]
	v_lshl_add_u64 v[8:9], v[4:5], 0, v[66:67]
	v_add_u32_e32 v4, v83, v66
	ds_read_b128 v[4:7], v4
	s_waitcnt lgkmcnt(1)
	global_store_dwordx4 v[8:9], v[0:3], off sc1
	s_nop 1
	v_add_u32_e32 v0, s16, v82
	v_ashrrev_i32_e32 v1, 31, v0
	v_lshlrev_b64 v[0:1], 10, v[0:1]
	v_lshl_add_u64 v[0:1], s[14:15], 0, v[0:1]
	v_lshl_add_u64 v[0:1], v[0:1], 0, v[66:67]
	s_waitcnt lgkmcnt(0)
	global_store_dwordx4 v[0:1], v[4:7], off sc1
	v_add_u32_e32 v0, v85, v66
	ds_read_b128 v[0:3], v0
	v_add_u32_e32 v4, s16, v84
	v_ashrrev_i32_e32 v5, 31, v4
	v_lshlrev_b64 v[4:5], 10, v[4:5]
	v_lshl_add_u64 v[4:5], s[14:15], 0, v[4:5]
	v_lshl_add_u64 v[8:9], v[4:5], 0, v[66:67]
	v_add_u32_e32 v4, v87, v66
	ds_read_b128 v[4:7], v4
	s_waitcnt lgkmcnt(1)
	global_store_dwordx4 v[8:9], v[0:3], off sc1
	s_nop 1
	v_add_u32_e32 v0, s16, v86
	v_ashrrev_i32_e32 v1, 31, v0
	v_lshlrev_b64 v[0:1], 10, v[0:1]
	v_lshl_add_u64 v[0:1], s[14:15], 0, v[0:1]
	v_lshl_add_u64 v[0:1], v[0:1], 0, v[66:67]
	s_waitcnt lgkmcnt(0)
	global_store_dwordx4 v[0:1], v[4:7], off sc1
	v_add_u32_e32 v0, v89, v66
	ds_read_b128 v[0:3], v0
	v_add_u32_e32 v4, s16, v88
	v_ashrrev_i32_e32 v5, 31, v4
	v_lshlrev_b64 v[4:5], 10, v[4:5]
	v_lshl_add_u64 v[4:5], s[14:15], 0, v[4:5]
	v_lshl_add_u64 v[8:9], v[4:5], 0, v[66:67]
	v_add_u32_e32 v4, v124, v66
	ds_read_b128 v[4:7], v4
	s_waitcnt lgkmcnt(1)
	global_store_dwordx4 v[8:9], v[0:3], off sc1
	s_nop 1
	v_add_u32_e32 v0, s16, v90
	v_ashrrev_i32_e32 v1, 31, v0
	v_lshlrev_b64 v[0:1], 10, v[0:1]
	v_lshl_add_u64 v[0:1], s[14:15], 0, v[0:1]
	v_lshl_add_u64 v[0:1], v[0:1], 0, v[66:67]
	s_waitcnt lgkmcnt(0)
	global_store_dwordx4 v[0:1], v[4:7], off sc1
	s_waitcnt lgkmcnt(0)
	s_barrier

.LBB0_25:
	v_lshl_add_u32 v32, s33, 6, v26
	v_or_b32_e32 v4, 1, v32
	v_ashrrev_i32_e32 v33, 31, v32
	v_ashrrev_i32_e32 v5, 31, v4
	s_or_b32 s34, s33, 1
	v_lshlrev_b64 v[0:1], 12, v[32:33]
	v_lshlrev_b64 v[4:5], 12, v[4:5]
	v_or_b32_e32 v8, 2, v32
	v_or_b32_e32 v12, 3, v32
	v_or_b32_e32 v16, 4, v32
	v_or_b32_e32 v20, 5, v32
	v_or_b32_e32 v28, 6, v32
	v_or_b32_e32 v32, 7, v32
	v_lshl_add_u32 v72, s34, 6, v26
	v_lshl_add_u64 v[0:1], v[24:25], 0, v[0:1]
	v_lshl_add_u64 v[4:5], v[24:25], 0, v[4:5]
	v_ashrrev_i32_e32 v9, 31, v8
	v_ashrrev_i32_e32 v13, 31, v12
	v_ashrrev_i32_e32 v17, 31, v16
	v_ashrrev_i32_e32 v21, 31, v20
	v_ashrrev_i32_e32 v29, 31, v28
	v_ashrrev_i32_e32 v33, 31, v32
	v_ashrrev_i32_e32 v73, 31, v72
	global_load_dwordx4 v[0:3], v[0:1], off nt
	v_lshlrev_b64 v[8:9], 12, v[8:9]
	global_load_dwordx4 v[4:7], v[4:5], off nt
	v_lshlrev_b64 v[12:13], 12, v[12:13]
	v_lshlrev_b64 v[16:17], 12, v[16:17]
	v_lshlrev_b64 v[20:21], 12, v[20:21]
	v_lshlrev_b64 v[28:29], 12, v[28:29]
	v_lshlrev_b64 v[32:33], 12, v[32:33]
	v_lshlrev_b64 v[36:37], 12, v[72:73]
	v_or_b32_e32 v40, 1, v72
	v_or_b32_e32 v44, 2, v72
	v_or_b32_e32 v48, 3, v72
	v_or_b32_e32 v52, 4, v72
	v_or_b32_e32 v56, 5, v72
	v_or_b32_e32 v60, 6, v72
	v_or_b32_e32 v72, 7, v72
	v_lshl_add_u64 v[8:9], v[24:25], 0, v[8:9]
	v_lshl_add_u64 v[12:13], v[24:25], 0, v[12:13]
	v_lshl_add_u64 v[16:17], v[24:25], 0, v[16:17]
	v_lshl_add_u64 v[20:21], v[24:25], 0, v[20:21]
	v_lshl_add_u64 v[28:29], v[24:25], 0, v[28:29]
	v_lshl_add_u64 v[32:33], v[24:25], 0, v[32:33]
	v_ashrrev_i32_e32 v41, 31, v40
	v_ashrrev_i32_e32 v45, 31, v44
	v_ashrrev_i32_e32 v49, 31, v48
	v_ashrrev_i32_e32 v53, 31, v52
	v_ashrrev_i32_e32 v57, 31, v56
	v_ashrrev_i32_e32 v61, 31, v60
	v_ashrrev_i32_e32 v73, 31, v72
	s_waitcnt vmcnt(0)
	v_cvt_pk_bf16_f32 v132, v0, v4
	v_lshl_add_u32 v4, s33, 7, v123
	global_load_dwordx4 v[8:11], v[8:9], off nt
	v_lshlrev_b64 v[40:41], 12, v[40:41]
	global_load_dwordx4 v[12:15], v[12:13], off nt
	v_lshlrev_b64 v[44:45], 12, v[44:45]
	global_load_dwordx4 v[16:19], v[16:17], off nt
	v_lshlrev_b64 v[48:49], 12, v[48:49]
	global_load_dwordx4 v[20:23], v[20:21], off nt
	v_lshlrev_b64 v[52:53], 12, v[52:53]
	global_load_dwordx4 v[28:31], v[28:29], off nt
	v_lshlrev_b64 v[56:57], 12, v[56:57]
	global_load_dwordx4 v[32:35], v[32:33], off nt
	v_lshlrev_b64 v[60:61], 12, v[60:61]
	v_lshlrev_b64 v[72:73], 12, v[72:73]
	s_waitcnt vmcnt(4)
	v_cvt_pk_bf16_f32 v133, v8, v12
	s_waitcnt vmcnt(2)
	v_cvt_pk_bf16_f32 v134, v16, v20
	s_waitcnt vmcnt(0)
	v_cvt_pk_bf16_f32 v135, v28, v32
	ds_write_b128 v4, v[132:135]
	v_cvt_pk_bf16_f32 v132, v1, v5
	v_lshl_add_u64 v[36:37], v[24:25], 0, v[36:37]
	v_lshl_add_u64 v[40:41], v[24:25], 0, v[40:41]
	v_lshl_add_u64 v[44:45], v[24:25], 0, v[44:45]
	v_lshl_add_u64 v[48:49], v[24:25], 0, v[48:49]
	v_lshl_add_u64 v[52:53], v[24:25], 0, v[52:53]
	v_lshl_add_u64 v[56:57], v[24:25], 0, v[56:57]
	v_lshl_add_u64 v[60:61], v[24:25], 0, v[60:61]
	v_lshl_add_u64 v[72:73], v[24:25], 0, v[72:73]
	v_cvt_pk_bf16_f32 v133, v9, v13
	v_cvt_pk_bf16_f32 v134, v17, v21
	v_cvt_pk_bf16_f32 v135, v29, v33
	ds_write_b128 v4, v[132:135] offset:528
	v_cvt_pk_bf16_f32 v132, v2, v6
	v_cvt_pk_bf16_f32 v0, v3, v7
	v_cvt_pk_bf16_f32 v1, v11, v15
	v_cvt_pk_bf16_f32 v2, v19, v23
	v_cvt_pk_bf16_f32 v3, v31, v35
	global_load_dwordx4 v[36:39], v[36:37], off nt
	v_cvt_pk_bf16_f32 v133, v10, v14
	global_load_dwordx4 v[40:43], v[40:41], off nt
	v_cvt_pk_bf16_f32 v134, v18, v22
	global_load_dwordx4 v[44:47], v[44:45], off nt
	v_cvt_pk_bf16_f32 v135, v30, v34
	global_load_dwordx4 v[48:51], v[48:49], off nt
	ds_write_b128 v4, v[132:135] offset:1056
	global_load_dwordx4 v[52:55], v[52:53], off nt
	ds_write_b128 v4, v[0:3] offset:1584
	global_load_dwordx4 v[56:59], v[56:57], off nt
	s_waitcnt vmcnt(4)
	v_cvt_pk_bf16_f32 v0, v36, v40
	global_load_dwordx4 v[60:63], v[60:61], off nt
	s_waitcnt vmcnt(3)
	v_cvt_pk_bf16_f32 v1, v44, v48
	global_load_dwordx4 v[128:131], v[72:73], off nt
	s_waitcnt vmcnt(2)
	v_cvt_pk_bf16_f32 v2, v52, v56
	s_waitcnt vmcnt(0)
	v_cvt_pk_bf16_f32 v3, v60, v128
	v_lshl_add_u32 v4, s34, 7, v123
	ds_write_b128 v4, v[0:3]
	v_cvt_pk_bf16_f32 v0, v37, v41
	v_cvt_pk_bf16_f32 v1, v45, v49
	v_cvt_pk_bf16_f32 v2, v53, v57
	v_cvt_pk_bf16_f32 v3, v61, v129
	ds_write_b128 v4, v[0:3] offset:528
	v_cvt_pk_bf16_f32 v0, v38, v42
	v_cvt_pk_bf16_f32 v1, v46, v50
	v_cvt_pk_bf16_f32 v2, v54, v58
	v_cvt_pk_bf16_f32 v3, v62, v130
	s_and_b64 vcc, exec, s[16:17]
	s_mov_b64 s[16:17], 0
	s_mov_b32 s33, 2
	ds_write_b128 v4, v[0:3] offset:1056
	v_cvt_pk_bf16_f32 v0, v39, v43
	v_cvt_pk_bf16_f32 v1, v47, v51
	v_cvt_pk_bf16_f32 v2, v55, v59
	v_cvt_pk_bf16_f32 v3, v63, v131
	ds_write_b128 v4, v[0:3] offset:1584
	s_cbranch_vccnz .LBB0_25
	s_lshl_b64 s[14:15], s[14:15], 1
	s_add_u32 s14, s23, s14
	s_waitcnt lgkmcnt(0)
	s_barrier
	s_addc_u32 s15, s24, s15
	s_lshl_b32 s16, s31, 1
	ds_read_b128 v[0:3], v92
	v_add_u32_e32 v4, s2, v91
	s_add_u32 s14, s14, s16
	v_ashrrev_i32_e32 v5, 31, v4
	s_addc_u32 s15, s15, 0
	v_lshlrev_b64 v[4:5], 11, v[4:5]
	v_lshl_add_u64 v[4:5], s[14:15], 0, v[4:5]
	v_mov_b32_e32 v71, v69
	v_lshl_add_u64 v[8:9], v[4:5], 0, v[70:71]
	ds_read_b128 v[4:7], v94
	s_waitcnt lgkmcnt(1)
	global_store_dwordx4 v[8:9], v[0:3], off sc1
	s_nop 1
	v_add_u32_e32 v0, s2, v93
	v_ashrrev_i32_e32 v1, 31, v0
	v_lshlrev_b64 v[0:1], 11, v[0:1]
	v_lshl_add_u64 v[0:1], s[14:15], 0, v[0:1]
	v_lshl_add_u64 v[0:1], v[0:1], 0, v[70:71]
	s_waitcnt lgkmcnt(0)
	global_store_dwordx4 v[0:1], v[4:7], off sc1
	ds_read_b128 v[0:3], v96
	s_nop 0
	v_add_u32_e32 v4, s2, v95
	v_ashrrev_i32_e32 v5, 31, v4
	v_lshlrev_b64 v[4:5], 11, v[4:5]
	v_lshl_add_u64 v[4:5], s[14:15], 0, v[4:5]
	v_lshl_add_u64 v[8:9], v[4:5], 0, v[70:71]
	ds_read_b128 v[4:7], v98
	s_waitcnt lgkmcnt(1)
	global_store_dwordx4 v[8:9], v[0:3], off sc1
	s_nop 1
	v_add_u32_e32 v0, s2, v97
	v_ashrrev_i32_e32 v1, 31, v0
	v_lshlrev_b64 v[0:1], 11, v[0:1]
	v_lshl_add_u64 v[0:1], s[14:15], 0, v[0:1]
	v_lshl_add_u64 v[0:1], v[0:1], 0, v[70:71]
	s_waitcnt lgkmcnt(0)
	global_store_dwordx4 v[0:1], v[4:7], off sc1
	ds_read_b128 v[0:3], v100
	s_nop 0
	v_add_u32_e32 v4, s2, v99
	v_ashrrev_i32_e32 v5, 31, v4
	v_lshlrev_b64 v[4:5], 11, v[4:5]
	v_lshl_add_u64 v[4:5], s[14:15], 0, v[4:5]
	v_lshl_add_u64 v[8:9], v[4:5], 0, v[70:71]
	ds_read_b128 v[4:7], v102
	s_waitcnt lgkmcnt(1)
	global_store_dwordx4 v[8:9], v[0:3], off sc1
	s_nop 1
	v_add_u32_e32 v0, s2, v101
	v_ashrrev_i32_e32 v1, 31, v0
	v_lshlrev_b64 v[0:1], 11, v[0:1]
	v_lshl_add_u64 v[0:1], s[14:15], 0, v[0:1]
	v_lshl_add_u64 v[0:1], v[0:1], 0, v[70:71]
	s_waitcnt lgkmcnt(0)
	global_store_dwordx4 v[0:1], v[4:7], off sc1
	ds_read_b128 v[0:3], v104
	s_nop 0
	v_add_u32_e32 v4, s2, v103
	v_ashrrev_i32_e32 v5, 31, v4
	v_lshlrev_b64 v[4:5], 11, v[4:5]
	v_lshl_add_u64 v[4:5], s[14:15], 0, v[4:5]
	v_lshl_add_u64 v[8:9], v[4:5], 0, v[70:71]
	ds_read_b128 v[4:7], v106
	s_waitcnt lgkmcnt(1)
	global_store_dwordx4 v[8:9], v[0:3], off sc1
	s_nop 1
	v_add_u32_e32 v0, s2, v105
	v_ashrrev_i32_e32 v1, 31, v0
	v_lshlrev_b64 v[0:1], 11, v[0:1]
	v_lshl_add_u64 v[0:1], s[14:15], 0, v[0:1]
	v_lshl_add_u64 v[0:1], v[0:1], 0, v[70:71]
	s_waitcnt lgkmcnt(0)
	global_store_dwordx4 v[0:1], v[4:7], off sc1
	ds_read_b128 v[0:3], v108
	s_nop 0
	v_add_u32_e32 v4, s2, v107
	v_ashrrev_i32_e32 v5, 31, v4
	v_lshlrev_b64 v[4:5], 11, v[4:5]
	v_lshl_add_u64 v[4:5], s[14:15], 0, v[4:5]
	v_lshl_add_u64 v[8:9], v[4:5], 0, v[70:71]
	ds_read_b128 v[4:7], v110
	s_waitcnt lgkmcnt(1)
	global_store_dwordx4 v[8:9], v[0:3], off sc1
	s_nop 1
	v_add_u32_e32 v0, s2, v109
	v_ashrrev_i32_e32 v1, 31, v0
	v_lshlrev_b64 v[0:1], 11, v[0:1]
	v_lshl_add_u64 v[0:1], s[14:15], 0, v[0:1]
	v_lshl_add_u64 v[0:1], v[0:1], 0, v[70:71]
	s_waitcnt lgkmcnt(0)
	global_store_dwordx4 v[0:1], v[4:7], off sc1
	ds_read_b128 v[0:3], v112
	s_nop 0
	v_add_u32_e32 v4, s2, v111
	v_ashrrev_i32_e32 v5, 31, v4
	v_lshlrev_b64 v[4:5], 11, v[4:5]
	v_lshl_add_u64 v[4:5], s[14:15], 0, v[4:5]
	v_lshl_add_u64 v[8:9], v[4:5], 0, v[70:71]
	ds_read_b128 v[4:7], v114
	s_waitcnt lgkmcnt(1)
	global_store_dwordx4 v[8:9], v[0:3], off sc1
	s_nop 1
	v_add_u32_e32 v0, s2, v113
	v_ashrrev_i32_e32 v1, 31, v0
	v_lshlrev_b64 v[0:1], 11, v[0:1]
	v_lshl_add_u64 v[0:1], s[14:15], 0, v[0:1]
	v_lshl_add_u64 v[0:1], v[0:1], 0, v[70:71]
	s_waitcnt lgkmcnt(0)
	global_store_dwordx4 v[0:1], v[4:7], off sc1
	ds_read_b128 v[0:3], v116
	s_nop 0
	v_add_u32_e32 v4, s2, v115
	v_ashrrev_i32_e32 v5, 31, v4
	v_lshlrev_b64 v[4:5], 11, v[4:5]
	v_lshl_add_u64 v[4:5], s[14:15], 0, v[4:5]
	v_lshl_add_u64 v[8:9], v[4:5], 0, v[70:71]
	ds_read_b128 v[4:7], v118
	s_waitcnt lgkmcnt(1)
	global_store_dwordx4 v[8:9], v[0:3], off sc1
	s_nop 1
	v_add_u32_e32 v0, s2, v117
	v_ashrrev_i32_e32 v1, 31, v0
	v_lshlrev_b64 v[0:1], 11, v[0:1]
	v_lshl_add_u64 v[0:1], s[14:15], 0, v[0:1]
	v_lshl_add_u64 v[0:1], v[0:1], 0, v[70:71]
	s_waitcnt lgkmcnt(0)
	global_store_dwordx4 v[0:1], v[4:7], off sc1
	ds_read_b128 v[0:3], v120
	s_nop 0
	v_add_u32_e32 v4, s2, v119
	v_ashrrev_i32_e32 v5, 31, v4
	v_lshlrev_b64 v[4:5], 11, v[4:5]
	v_lshl_add_u64 v[4:5], s[14:15], 0, v[4:5]
	v_lshl_add_u64 v[8:9], v[4:5], 0, v[70:71]
	ds_read_b128 v[4:7], v122
	s_waitcnt lgkmcnt(1)
	global_store_dwordx4 v[8:9], v[0:3], off sc1
	s_nop 1
	v_add_u32_e32 v0, s2, v121
	v_ashrrev_i32_e32 v1, 31, v0
	v_lshlrev_b64 v[0:1], 11, v[0:1]
	v_lshl_add_u64 v[0:1], s[14:15], 0, v[0:1]
	v_lshl_add_u64 v[0:1], v[0:1], 0, v[70:71]
	s_waitcnt lgkmcnt(0)
	global_store_dwordx4 v[0:1], v[4:7], off sc1
	s_waitcnt lgkmcnt(0)
	s_barrier

.LBB0_30:
	v_add_u32_e32 v3, s31, v2
	v_mad_i64_i32 v[4:5], s[34:35], v3, s29, v[0:1]
	v_or_b32_e32 v8, 1, v3
	v_or_b32_e32 v9, 2, v3
	v_or_b32_e32 v10, 3, v3
	v_or_b32_e32 v11, 4, v3
	v_or_b32_e32 v12, 5, v3
	v_or_b32_e32 v13, 6, v3
	v_or_b32_e32 v14, 7, v3
	v_add_u32_e32 v15, 64, v3
	v_add_u32_e32 v16, 0x41, v3
	v_add_u32_e32 v17, 0x42, v3
	v_add_u32_e32 v18, 0x43, v3
	v_add_u32_e32 v19, 0x44, v3
	v_add_u32_e32 v26, 0x45, v3
	v_add_u32_e32 v27, 0x46, v3
	v_add_u32_e32 v3, 0x47, v3
	global_load_dwordx4 v[4:7], v[4:5], off nt
	v_mad_i64_i32 v[20:21], s[34:35], v8, s29, v[0:1]
	v_mad_i64_i32 v[22:23], s[34:35], v9, s29, v[0:1]
	v_mad_i64_i32 v[24:25], s[34:35], v10, s29, v[0:1]
	v_mad_i64_i32 v[28:29], s[34:35], v11, s29, v[0:1]
	v_mad_i64_i32 v[30:31], s[34:35], v12, s29, v[0:1]
	v_mad_i64_i32 v[32:33], s[34:35], v13, s29, v[0:1]
	v_mad_i64_i32 v[34:35], s[34:35], v14, s29, v[0:1]
	v_mad_i64_i32 v[36:37], s[34:35], v15, s29, v[0:1]
	v_mad_i64_i32 v[40:41], s[34:35], v16, s29, v[0:1]
	v_mad_i64_i32 v[44:45], s[34:35], v17, s29, v[0:1]
	v_mad_i64_i32 v[48:49], s[34:35], v18, s29, v[0:1]
	v_mad_i64_i32 v[52:53], s[34:35], v19, s29, v[0:1]
	v_mad_i64_i32 v[56:57], s[34:35], v26, s29, v[0:1]
	v_mad_i64_i32 v[60:61], s[34:35], v27, s29, v[0:1]
	v_mad_i64_i32 v[128:129], s[34:35], v3, s29, v[0:1]
	global_load_dwordx4 v[8:11], v[20:21], off nt
	global_load_dwordx4 v[12:15], v[22:23], off nt
	global_load_dwordx4 v[16:19], v[24:25], off nt
	s_nop 0
	global_load_dwordx4 v[20:23], v[28:29], off nt
	global_load_dwordx4 v[24:27], v[30:31], off nt
	s_nop 0
	global_load_dwordx4 v[28:31], v[32:33], off nt
	s_nop 0
	global_load_dwordx4 v[32:35], v[34:35], off nt
	s_nop 0
	global_load_dwordx4 v[36:39], v[36:37], off nt
	s_nop 0
	global_load_dwordx4 v[40:43], v[40:41], off nt
	s_nop 0
	global_load_dwordx4 v[44:47], v[44:45], off nt
	s_nop 0
	global_load_dwordx4 v[48:51], v[48:49], off nt
	s_nop 0
	global_load_dwordx4 v[52:55], v[52:53], off nt
	s_nop 0
	global_load_dwordx4 v[56:59], v[56:57], off nt
	s_nop 0
	global_load_dwordx4 v[60:63], v[60:61], off nt
	s_nop 0
	global_load_dwordx4 v[128:131], v[128:129], off nt
	v_mov_b32_e32 v72, 0
	v_mov_b32_e32 v73, 0
	v_mov_b32_e32 v138, 0
	v_mov_b32_e32 v139, 0
	v_mov_b32_e32 v132, 0
	v_mov_b32_e32 v133, 0
	v_mov_b32_e32 v140, 0
	v_mov_b32_e32 v141, 0
	v_mov_b32_e32 v134, 0
	v_mov_b32_e32 v135, 0
	v_mov_b32_e32 v142, 0
	v_mov_b32_e32 v143, 0
	v_mov_b32_e32 v136, 0
	v_mov_b32_e32 v137, 0
	v_mov_b32_e32 v144, 0
	v_mov_b32_e32 v145, 0
	v_add_u32_e32 v68, s31, v125
	s_movk_i32 s31, 0x80
	s_and_b64 vcc, exec, s[14:15]
	s_mov_b64 s[14:15], 0
	s_waitcnt vmcnt(15)
	v_mul_f32_e32 v3, 0x42000000, v4
	v_mul_f32_e32 v4, 0x42000000, v5
	v_mul_f32_e32 v5, 0x42000000, v6
	v_mul_f32_e32 v6, 0x42000000, v7
	s_waitcnt vmcnt(14)
	v_mul_f32_e32 v7, 0x42000000, v8
	v_mul_f32_e32 v8, 0x42000000, v9
	v_mul_f32_e32 v9, 0x42000000, v10
	v_mul_f32_e32 v10, 0x42000000, v11
	s_waitcnt vmcnt(13)
	v_mul_f32_e32 v11, 0x42000000, v12
	v_mul_f32_e32 v12, 0x42000000, v13
	v_mul_f32_e32 v13, 0x42000000, v14
	v_mul_f32_e32 v14, 0x42000000, v15
	s_waitcnt vmcnt(12)
	v_mul_f32_e32 v15, 0x42000000, v16
	v_mul_f32_e32 v16, 0x42000000, v17
	v_mul_f32_e32 v17, 0x42000000, v18
	v_mul_f32_e32 v18, 0x42000000, v19
	s_waitcnt vmcnt(11)
	v_mul_f32_e32 v19, 0x42000000, v20
	v_mul_f32_e32 v20, 0x42000000, v21
	v_mul_f32_e32 v21, 0x42000000, v22
	v_mul_f32_e32 v22, 0x42000000, v23
	s_waitcnt vmcnt(10)
	v_mul_f32_e32 v23, 0x42000000, v24
	v_mul_f32_e32 v24, 0x42000000, v25
	v_mul_f32_e32 v25, 0x42000000, v26
	v_mul_f32_e32 v26, 0x42000000, v27
	s_waitcnt vmcnt(9)
	v_mul_f32_e32 v27, 0x42000000, v28
	v_mul_f32_e32 v28, 0x42000000, v29
	v_mul_f32_e32 v29, 0x42000000, v30
	v_mul_f32_e32 v30, 0x42000000, v31
	s_waitcnt vmcnt(8)
	v_mul_f32_e32 v31, 0x42000000, v32
	v_mul_f32_e32 v32, 0x42000000, v33
	v_mul_f32_e32 v33, 0x42000000, v34
	v_mul_f32_e32 v34, 0x42000000, v35
	s_waitcnt vmcnt(7)
	v_mul_f32_e32 v35, 0x42000000, v36
	v_mul_f32_e32 v36, 0x42000000, v37
	v_mul_f32_e32 v37, 0x42000000, v38
	v_mul_f32_e32 v38, 0x42000000, v39
	s_waitcnt vmcnt(6)
	v_mul_f32_e32 v39, 0x42000000, v40
	v_mul_f32_e32 v40, 0x42000000, v41
	v_mul_f32_e32 v41, 0x42000000, v42
	v_mul_f32_e32 v42, 0x42000000, v43
	s_waitcnt vmcnt(5)
	v_mul_f32_e32 v43, 0x42000000, v44
	v_mul_f32_e32 v44, 0x42000000, v45
	v_mul_f32_e32 v45, 0x42000000, v46
	v_mul_f32_e32 v46, 0x42000000, v47
	s_waitcnt vmcnt(4)
	v_mul_f32_e32 v47, 0x42000000, v48
	v_mul_f32_e32 v48, 0x42000000, v49
	v_mul_f32_e32 v49, 0x42000000, v50
	v_mul_f32_e32 v50, 0x42000000, v51
	s_waitcnt vmcnt(3)
	v_mul_f32_e32 v51, 0x42000000, v52
	v_mul_f32_e32 v52, 0x42000000, v53
	v_mul_f32_e32 v53, 0x42000000, v54
	v_mul_f32_e32 v54, 0x42000000, v55
	s_waitcnt vmcnt(2)
	v_mul_f32_e32 v55, 0x42000000, v56
	v_mul_f32_e32 v56, 0x42000000, v57
	v_cvt_pk_fp8_f32 v72, v3, v7
	v_cvt_pk_fp8_f32 v73, v19, v23
	v_cvt_pk_fp8_f32 v138, v35, v39
	v_cvt_pk_fp8_f32 v139, v51, v55
	v_mul_f32_e32 v57, 0x42000000, v58
	v_cvt_pk_fp8_f32 v132, v4, v8
	v_cvt_pk_fp8_f32 v133, v20, v24
	v_cvt_pk_fp8_f32 v140, v36, v40
	v_cvt_pk_fp8_f32 v141, v52, v56
	v_mul_f32_e32 v58, 0x42000000, v59
	v_cvt_pk_fp8_f32 v134, v5, v9
	v_cvt_pk_fp8_f32 v135, v21, v25
	v_cvt_pk_fp8_f32 v142, v37, v41
	v_cvt_pk_fp8_f32 v143, v53, v57
	s_waitcnt vmcnt(1)
	v_mul_f32_e32 v59, 0x42000000, v60
	v_mul_f32_e32 v60, 0x42000000, v61
	v_mul_f32_e32 v61, 0x42000000, v62
	v_mul_f32_e32 v62, 0x42000000, v63
	s_waitcnt vmcnt(0)
	v_mul_f32_e32 v63, 0x42000000, v128
	v_cvt_pk_fp8_f32 v136, v6, v10
	v_cvt_pk_fp8_f32 v137, v22, v26
	v_cvt_pk_fp8_f32 v144, v38, v42
	v_cvt_pk_fp8_f32 v145, v54, v58
	v_mul_f32_e32 v71, 0x42000000, v129
	v_cvt_pk_fp8_f32 v72, v11, v15 op_sel:[0,0,1]
	v_cvt_pk_fp8_f32 v73, v27, v31 op_sel:[0,0,1]
	v_cvt_pk_fp8_f32 v138, v43, v47 op_sel:[0,0,1]
	v_cvt_pk_fp8_f32 v139, v59, v63 op_sel:[0,0,1]
	v_mul_f32_e32 v127, 0x42000000, v130
	v_cvt_pk_fp8_f32 v132, v12, v16 op_sel:[0,0,1]
	v_cvt_pk_fp8_f32 v133, v28, v32 op_sel:[0,0,1]
	v_cvt_pk_fp8_f32 v140, v44, v48 op_sel:[0,0,1]
	v_cvt_pk_fp8_f32 v141, v60, v71 op_sel:[0,0,1]
	v_mul_f32_e32 v128, 0x42000000, v131
	v_cvt_pk_fp8_f32 v134, v13, v17 op_sel:[0,0,1]
	v_cvt_pk_fp8_f32 v135, v29, v33 op_sel:[0,0,1]
	v_cvt_pk_fp8_f32 v142, v45, v49 op_sel:[0,0,1]
	v_cvt_pk_fp8_f32 v143, v61, v127 op_sel:[0,0,1]
	v_cvt_pk_fp8_f32 v136, v14, v18 op_sel:[0,0,1]
	v_cvt_pk_fp8_f32 v137, v30, v34 op_sel:[0,0,1]
	v_cvt_pk_fp8_f32 v144, v46, v50 op_sel:[0,0,1]
	v_cvt_pk_fp8_f32 v145, v62, v128 op_sel:[0,0,1]
	ds_write2_b64 v68, v[72:73], v[138:139] offset1:8
	ds_write2_b64 v68, v[132:133], v[140:141] offset0:34 offset1:42
	ds_write2_b64 v68, v[134:135], v[142:143] offset0:68 offset1:76
	ds_write2_b64 v68, v[136:137], v[144:145] offset0:102 offset1:110
	s_cbranch_vccnz .LBB0_30
	s_mul_i32 s15, s16, 0x280000
	s_mul_hi_i32 s14, s16, 0x280000
	s_add_u32 s15, s25, s15
	s_waitcnt lgkmcnt(0)
	s_barrier
	v_add_u32_e32 v0, v77, v66
	s_addc_u32 s16, s27, s14
	s_ashr_i32 s31, s17, 31
	ds_read_b128 v[0:3], v0
	v_add_u32_e32 v4, s2, v76
	s_add_u32 s14, s15, s17
	v_ashrrev_i32_e32 v5, 31, v4
	s_addc_u32 s15, s16, s31
	v_lshlrev_b64 v[4:5], 10, v[4:5]
	v_lshl_add_u64 v[4:5], s[14:15], 0, v[4:5]
	v_lshl_add_u64 v[8:9], v[4:5], 0, v[66:67]
	v_add_u32_e32 v4, v79, v66
	ds_read_b128 v[4:7], v4
	s_waitcnt lgkmcnt(1)
	global_store_dwordx4 v[8:9], v[0:3], off sc1
	s_nop 1
	v_add_u32_e32 v0, s2, v78
	v_ashrrev_i32_e32 v1, 31, v0
	v_lshlrev_b64 v[0:1], 10, v[0:1]
	v_lshl_add_u64 v[0:1], s[14:15], 0, v[0:1]
	v_lshl_add_u64 v[0:1], v[0:1], 0, v[66:67]
	s_waitcnt lgkmcnt(0)
	global_store_dwordx4 v[0:1], v[4:7], off sc1
	v_add_u32_e32 v0, v81, v66
	ds_read_b128 v[0:3], v0
	v_add_u32_e32 v4, s2, v80
	v_ashrrev_i32_e32 v5, 31, v4
	v_lshlrev_b64 v[4:5], 10, v[4:5]
	v_lshl_add_u64 v[4:5], s[14:15], 0, v[4:5]
	v_lshl_add_u64 v[8:9], v[4:5], 0, v[66:67]
	v_add_u32_e32 v4, v83, v66
	ds_read_b128 v[4:7], v4
	s_waitcnt lgkmcnt(1)
	global_store_dwordx4 v[8:9], v[0:3], off sc1
	s_nop 1
	v_add_u32_e32 v0, s2, v82
	v_ashrrev_i32_e32 v1, 31, v0
	v_lshlrev_b64 v[0:1], 10, v[0:1]
	v_lshl_add_u64 v[0:1], s[14:15], 0, v[0:1]
	v_lshl_add_u64 v[0:1], v[0:1], 0, v[66:67]
	s_waitcnt lgkmcnt(0)
	global_store_dwordx4 v[0:1], v[4:7], off sc1
	v_add_u32_e32 v0, v85, v66
	ds_read_b128 v[0:3], v0
	v_add_u32_e32 v4, s2, v84
	v_ashrrev_i32_e32 v5, 31, v4
	v_lshlrev_b64 v[4:5], 10, v[4:5]
	v_lshl_add_u64 v[4:5], s[14:15], 0, v[4:5]
	v_lshl_add_u64 v[8:9], v[4:5], 0, v[66:67]
	v_add_u32_e32 v4, v87, v66
	ds_read_b128 v[4:7], v4
	s_waitcnt lgkmcnt(1)
	global_store_dwordx4 v[8:9], v[0:3], off sc1
	s_nop 1
	v_add_u32_e32 v0, s2, v86
	v_ashrrev_i32_e32 v1, 31, v0
	v_lshlrev_b64 v[0:1], 10, v[0:1]
	v_lshl_add_u64 v[0:1], s[14:15], 0, v[0:1]
	v_lshl_add_u64 v[0:1], v[0:1], 0, v[66:67]
	s_waitcnt lgkmcnt(0)
	global_store_dwordx4 v[0:1], v[4:7], off sc1
	v_add_u32_e32 v0, v89, v66
	ds_read_b128 v[0:3], v0
	v_add_u32_e32 v4, s2, v88
	v_ashrrev_i32_e32 v5, 31, v4
	v_lshlrev_b64 v[4:5], 10, v[4:5]
	v_lshl_add_u64 v[4:5], s[14:15], 0, v[4:5]
	v_lshl_add_u64 v[8:9], v[4:5], 0, v[66:67]
	v_add_u32_e32 v4, v124, v66
	ds_read_b128 v[4:7], v4
	s_waitcnt lgkmcnt(1)
	global_store_dwordx4 v[8:9], v[0:3], off sc1
	s_nop 1
	v_add_u32_e32 v0, s2, v90
	v_ashrrev_i32_e32 v1, 31, v0
	v_lshlrev_b64 v[0:1], 10, v[0:1]
	v_lshl_add_u64 v[0:1], s[14:15], 0, v[0:1]
	v_lshl_add_u64 v[0:1], v[0:1], 0, v[66:67]
	s_waitcnt lgkmcnt(0)
	global_store_dwordx4 v[0:1], v[4:7], off sc1
	s_waitcnt lgkmcnt(0)
	s_barrier
	s_branch .LBB0_8

.LBB0_255:
	s_or_b64 exec, exec, s[26:27]
	v_cvt_pk_bf16_f32 v0, v0, v1
	v_cvt_pk_bf16_f32 v1, v2, v3
	v_cvt_pk_bf16_f32 v2, v4, v5
	v_cvt_pk_bf16_f32 v3, v6, v7
	global_store_dwordx4 v[12:13], v[0:3], off sc1
	v_cmp_lt_i32_e64 s[12:13], s59, v28
	v_lshl_add_u64 v[12:13], v[12:13], 0, s[18:19]
	v_add_u32_e32 v0, 0x200, v28
	s_or_b64 s[24:25], s[12:13], s[24:25]
	v_mov_b32_e32 v28, v0
	s_andn2_b64 exec, exec, s[24:25]
	s_cbranch_execz .LBB0_279

.LBB0_281:
	v_ashrrev_i32_e32 v3, 6, v2
	v_add_u32_e32 v7, 0x200, v2
	v_and_b32_e32 v9, -16, v3
	v_lshrrev_b32_e32 v4, 5, v2
	v_bfe_u32 v5, v2, 5, 5
	s_add_i32 s23, 0, 0x10000
	s_add_i32 s24, 0, 0x18400
	v_lshlrev_b32_e32 v6, 2, v2
	v_cmp_lt_i32_e64 s[12:13], s62, v2
	v_mov_b32_e32 v2, v7
	v_add_u32_e32 v7, s22, v9
	v_bitop3_b32 v4, v4, 31, v4 bitop3:0xc
	s_or_b64 s[20:21], s[12:13], s[20:21]
	v_cmp_gt_u32_e64 s[12:13], s56, v7
	v_and_b32_e32 v3, 48, v3
	v_and_b32_e32 v6, 64, v6
	v_cndmask_b32_e64 v4, v5, v4, s[12:13]
	v_ashrrev_i32_e32 v5, 1, v7
	v_and_b32_e32 v5, 0xffffffc0, v5
	v_or3_b32 v3, v3, v31, v5
	v_lshlrev_b32_e32 v4, 3, v4
	v_mul_lo_u32 v5, v3, s58
	v_lshlrev_b32_e32 v3, 7, v3
	v_add3_u32 v4, s23, v5, v4
	v_and_b32_e32 v9, 64, v7
	v_add3_u32 v3, s24, v3, v6
	ds_read_b64 v[28:29], v4
	ds_read_b128 v[4:7], v3
	ds_read_b128 v[10:13], v3 offset:16
	ds_read_b128 v[40:43], v3 offset:32
	ds_read_b128 v[44:47], v3 offset:48
	v_cmp_eq_u32_e64 s[12:13], 0, v9
	s_waitcnt lgkmcnt(3)
	v_pk_mul_f32 v[48:49], v[28:29], v[4:5] op_sel:[0,1] op_sel_hi:[1,0]
	v_pk_mul_f32 v[4:5], v[28:29], v[4:5]
	v_pk_mul_f32 v[50:51], v[28:29], v[6:7] op_sel:[0,1] op_sel_hi:[1,0]
	v_pk_mul_f32 v[6:7], v[28:29], v[6:7]
	s_waitcnt lgkmcnt(2)
	v_pk_mul_f32 v[52:53], v[28:29], v[10:11] op_sel:[0,1] op_sel_hi:[1,0]
	v_pk_mul_f32 v[10:11], v[28:29], v[10:11]
	v_pk_mul_f32 v[54:55], v[28:29], v[12:13] op_sel:[0,1] op_sel_hi:[1,0]
	v_pk_mul_f32 v[12:13], v[28:29], v[12:13]
	s_waitcnt lgkmcnt(1)
	v_pk_mul_f32 v[56:57], v[28:29], v[40:41] op_sel:[0,1] op_sel_hi:[1,0]
	v_pk_mul_f32 v[40:41], v[28:29], v[40:41]
	v_pk_mul_f32 v[58:59], v[28:29], v[42:43] op_sel:[0,1] op_sel_hi:[1,0]
	v_pk_mul_f32 v[42:43], v[28:29], v[42:43]
	s_waitcnt lgkmcnt(0)
	v_pk_mul_f32 v[60:61], v[28:29], v[44:45] op_sel:[0,1] op_sel_hi:[1,0]
	v_pk_mul_f32 v[44:45], v[28:29], v[44:45]
	v_pk_mul_f32 v[62:63], v[28:29], v[46:47] op_sel:[0,1] op_sel_hi:[1,0]
	v_pk_mul_f32 v[28:29], v[28:29], v[46:47]
	v_add_f32_e32 v3, v48, v49
	v_sub_f32_e32 v4, v4, v5
	v_add_f32_e32 v5, v50, v51
	v_sub_f32_e32 v6, v6, v7
	v_add_f32_e32 v7, v52, v53
	v_sub_f32_e32 v10, v10, v11
	v_add_f32_e32 v11, v54, v55
	v_sub_f32_e32 v12, v12, v13
	v_add_f32_e32 v13, v56, v57
	v_sub_f32_e32 v39, v40, v41
	v_add_f32_e32 v40, v58, v59
	v_sub_f32_e32 v41, v42, v43
	v_add_f32_e32 v42, v60, v61
	v_sub_f32_e32 v43, v44, v45
	v_add_f32_e32 v44, v62, v63
	v_sub_f32_e32 v28, v28, v29
	v_cndmask_b32_e64 v3, v3, v4, s[12:13]
	v_cndmask_b32_e64 v4, v5, v6, s[12:13]
	v_cndmask_b32_e64 v5, v7, v10, s[12:13]
	v_cndmask_b32_e64 v6, v11, v12, s[12:13]
	v_cndmask_b32_e64 v7, v13, v39, s[12:13]
	v_cndmask_b32_e64 v9, v40, v41, s[12:13]
	v_cndmask_b32_e64 v10, v42, v43, s[12:13]
	v_cndmask_b32_e64 v11, v44, v28, s[12:13]
	v_cvt_pk_bf16_f32 v4, v3, v4
	v_cvt_pk_bf16_f32 v5, v5, v6
	v_cvt_pk_bf16_f32 v6, v7, v9
	v_cvt_pk_bf16_f32 v7, v10, v11
	global_store_dwordx4 v[0:1], v[4:7], off sc1
	v_lshl_add_u64 v[0:1], v[0:1], 0, s[18:19]
	s_andn2_b64 exec, exec, s[20:21]
	s_cbranch_execnz .LBB0_281
	s_branch .LBB0_220

.LBB0_450:
	s_nop 0
	global_load_dwordx4 v[2:5], v[10:11], off
	global_load_dwordx4 v[72:75], v[10:11], off offset:1024
	global_load_dwordx4 v[76:79], v[10:11], off offset:2048
	global_load_dwordx4 v[84:87], v[10:11], off offset:3072
	v_readlane_b32 s4, v252, 26
	v_cmp_gt_i32_e32 vcc, s0, v9
	s_nop 0
	v_min_i32_e32 v0, s4, v9
	s_movk_i32 s4, 0x810
	v_mad_u64_u32 v[0:1], s[4:5], v0, s4, v[8:9]
	ds_read_b128 v[80:83], v0 offset:4096
	ds_read_b128 v[88:91], v0 offset:4160
	s_waitcnt vmcnt(3) lgkmcnt(1)
	v_mfma_f32_16x16x32_bf16 v[2:5], v[2:5], v[80:83], 0
	global_load_dwordx4 v[80:83], v[12:13], off
	global_load_dwordx4 v[92:95], v[14:15], off
	s_waitcnt vmcnt(4) lgkmcnt(0)
	v_mfma_f32_16x16x32_bf16 v[72:75], v[72:75], v[88:91], 0
	ds_read_b128 v[88:91], v0 offset:4224
	ds_read_b128 v[96:99], v0 offset:4288
	s_waitcnt vmcnt(3) lgkmcnt(1)
	v_mfma_f32_16x16x32_bf16 v[2:5], v[76:79], v[88:91], v[2:5]
	global_load_dwordx4 v[76:79], v[16:17], off
	ds_read_b128 v[88:91], v0 offset:4352
	s_waitcnt vmcnt(3) lgkmcnt(1)
	v_mfma_f32_16x16x32_bf16 v[72:75], v[84:87], v[96:99], v[72:75]
	global_load_dwordx4 v[84:87], v[18:19], off
	ds_read_b128 v[96:99], v0 offset:4416
	s_waitcnt vmcnt(3) lgkmcnt(1)
	v_mfma_f32_16x16x32_bf16 v[2:5], v[80:83], v[88:91], v[2:5]
	global_load_dwordx4 v[80:83], v[20:21], off
	global_load_dwordx4 v[88:91], v[22:23], off
	s_waitcnt vmcnt(4) lgkmcnt(0)
	v_mfma_f32_16x16x32_bf16 v[72:75], v[92:95], v[96:99], v[72:75]
	ds_read_b128 v[92:95], v0 offset:4480
	ds_read_b128 v[96:99], v0 offset:4544
	s_waitcnt vmcnt(3) lgkmcnt(1)
	v_mfma_f32_16x16x32_bf16 v[2:5], v[76:79], v[92:95], v[2:5]
	global_load_dwordx4 v[76:79], v[24:25], off
	ds_read_b128 v[92:95], v0 offset:4608
	s_waitcnt vmcnt(3) lgkmcnt(1)
	v_mfma_f32_16x16x32_bf16 v[72:75], v[84:87], v[96:99], v[72:75]
	global_load_dwordx4 v[84:87], v[26:27], off
	ds_read_b128 v[96:99], v0 offset:4672
	s_waitcnt vmcnt(3) lgkmcnt(1)
	v_mfma_f32_16x16x32_bf16 v[2:5], v[80:83], v[92:95], v[2:5]
	global_load_dwordx4 v[80:83], v[28:29], off
	global_load_dwordx4 v[92:95], v[30:31], off
	s_waitcnt vmcnt(4) lgkmcnt(0)
	v_mfma_f32_16x16x32_bf16 v[72:75], v[88:91], v[96:99], v[72:75]
	ds_read_b128 v[88:91], v0 offset:4736
	ds_read_b128 v[96:99], v0 offset:4800
	s_waitcnt vmcnt(3) lgkmcnt(1)
	v_mfma_f32_16x16x32_bf16 v[2:5], v[76:79], v[88:91], v[2:5]
	global_load_dwordx4 v[76:79], v[32:33], off
	ds_read_b128 v[88:91], v0 offset:4864
	s_waitcnt vmcnt(3) lgkmcnt(1)
	v_mfma_f32_16x16x32_bf16 v[72:75], v[84:87], v[96:99], v[72:75]
	global_load_dwordx4 v[84:87], v[34:35], off
	ds_read_b128 v[96:99], v0 offset:4928
	s_waitcnt vmcnt(3) lgkmcnt(1)
	v_mfma_f32_16x16x32_bf16 v[2:5], v[80:83], v[88:91], v[2:5]
	global_load_dwordx4 v[80:83], v[36:37], off
	global_load_dwordx4 v[88:91], v[38:39], off
	s_waitcnt vmcnt(4) lgkmcnt(0)
	v_mfma_f32_16x16x32_bf16 v[72:75], v[92:95], v[96:99], v[72:75]
	ds_read_b128 v[92:95], v0 offset:4992
	ds_read_b128 v[96:99], v0 offset:5056
	s_waitcnt vmcnt(3) lgkmcnt(1)
	v_mfma_f32_16x16x32_bf16 v[2:5], v[76:79], v[92:95], v[2:5]
	global_load_dwordx4 v[76:79], v[40:41], off
	ds_read_b128 v[92:95], v0 offset:5120
	s_waitcnt vmcnt(3) lgkmcnt(1)
	v_mfma_f32_16x16x32_bf16 v[72:75], v[84:87], v[96:99], v[72:75]
	global_load_dwordx4 v[84:87], v[42:43], off
	ds_read_b128 v[96:99], v0 offset:5184
	s_waitcnt vmcnt(3) lgkmcnt(1)
	v_mfma_f32_16x16x32_bf16 v[2:5], v[80:83], v[92:95], v[2:5]
	global_load_dwordx4 v[80:83], v[44:45], off
	global_load_dwordx4 v[92:95], v[46:47], off
	s_waitcnt vmcnt(4) lgkmcnt(0)
	v_mfma_f32_16x16x32_bf16 v[72:75], v[88:91], v[96:99], v[72:75]
	ds_read_b128 v[88:91], v0 offset:5248
	ds_read_b128 v[96:99], v0 offset:5312
	s_waitcnt vmcnt(3) lgkmcnt(1)
	v_mfma_f32_16x16x32_bf16 v[2:5], v[76:79], v[88:91], v[2:5]
	global_load_dwordx4 v[76:79], v[48:49], off
	ds_read_b128 v[88:91], v0 offset:5376
	s_waitcnt vmcnt(3) lgkmcnt(1)
	v_mfma_f32_16x16x32_bf16 v[72:75], v[84:87], v[96:99], v[72:75]
	global_load_dwordx4 v[84:87], v[50:51], off
	ds_read_b128 v[96:99], v0 offset:5440
	s_waitcnt vmcnt(3) lgkmcnt(1)
	v_mfma_f32_16x16x32_bf16 v[2:5], v[80:83], v[88:91], v[2:5]
	global_load_dwordx4 v[80:83], v[52:53], off
	global_load_dwordx4 v[88:91], v[54:55], off
	s_waitcnt vmcnt(4) lgkmcnt(0)
	v_mfma_f32_16x16x32_bf16 v[72:75], v[92:95], v[96:99], v[72:75]
	ds_read_b128 v[92:95], v0 offset:5504
	ds_read_b128 v[96:99], v0 offset:5568
	s_waitcnt vmcnt(3) lgkmcnt(1)
	v_mfma_f32_16x16x32_bf16 v[2:5], v[76:79], v[92:95], v[2:5]
	global_load_dwordx4 v[76:79], v[56:57], off
	ds_read_b128 v[92:95], v0 offset:5632
	s_waitcnt vmcnt(3) lgkmcnt(1)
	v_mfma_f32_16x16x32_bf16 v[72:75], v[84:87], v[96:99], v[72:75]
	global_load_dwordx4 v[84:87], v[58:59], off
	ds_read_b128 v[96:99], v0 offset:5696
	s_waitcnt vmcnt(3) lgkmcnt(1)
	v_mfma_f32_16x16x32_bf16 v[2:5], v[80:83], v[92:95], v[2:5]
	global_load_dwordx4 v[80:83], v[60:61], off
	s_waitcnt vmcnt(3) lgkmcnt(0)
	v_mfma_f32_16x16x32_bf16 v[72:75], v[88:91], v[96:99], v[72:75]
	ds_read_b128 v[88:91], v0 offset:5760
	ds_read_b128 v[92:95], v0 offset:5824
	s_waitcnt vmcnt(2) lgkmcnt(1)
	v_mfma_f32_16x16x32_bf16 v[2:5], v[76:79], v[88:91], v[2:5]
	global_load_dwordx4 v[76:79], v[62:63], off
	ds_read_b128 v[88:91], v0 offset:5888
	s_waitcnt vmcnt(2) lgkmcnt(1)
	v_mfma_f32_16x16x32_bf16 v[72:75], v[84:87], v[92:95], v[72:75]
	global_load_dwordx4 v[84:87], v[64:65], off
	ds_read_b128 v[92:95], v0 offset:5952
	s_waitcnt vmcnt(2) lgkmcnt(1)
	v_mfma_f32_16x16x32_bf16 v[2:5], v[80:83], v[88:91], v[2:5]
	global_load_dwordx4 v[80:83], v[66:67], off
	s_waitcnt vmcnt(2) lgkmcnt(0)
	v_mfma_f32_16x16x32_bf16 v[72:75], v[76:79], v[92:95], v[72:75]
	ds_read_b128 v[76:79], v0 offset:6016
	ds_read_b128 v[88:91], v0 offset:6080
	s_waitcnt vmcnt(1) lgkmcnt(1)
	v_mfma_f32_16x16x32_bf16 v[0:3], v[84:87], v[76:79], v[2:5]
	s_waitcnt vmcnt(0) lgkmcnt(0)
	v_mfma_f32_16x16x32_bf16 v[4:7], v[80:83], v[88:91], v[72:75]
	s_and_saveexec_b64 s[4:5], vcc
	s_cbranch_execz .LBB0_449
	s_nop 0
	global_load_dwordx4 v[72:75], v[68:69], off
	s_nop 3
	v_pk_add_f32 v[0:1], v[0:1], v[4:5]
	v_add_u32_e32 v4, s8, v9
	v_ashrrev_i32_e32 v5, 31, v4
	v_pk_add_f32 v[2:3], v[2:3], v[6:7]
	v_lshlrev_b64 v[4:5], 6, v[4:5]
	v_lshl_add_u64 v[4:5], v[70:71], 0, v[4:5]
	s_waitcnt vmcnt(0)
	v_pk_add_f32 v[2:3], v[2:3], v[74:75]
	v_pk_add_f32 v[0:1], v[0:1], v[72:73]
	global_store_dwordx4 v[4:5], v[0:3], off sc1
	s_branch .LBB0_449

.LBB0_522:
	v_cvt_pk_bf16_f32 v3, v2, v3
	v_cvt_pk_bf16_f32 v4, v4, v5
	v_cvt_pk_bf16_f32 v5, v6, v7
	v_cvt_pk_bf16_f32 v6, v0, v1
	ds_bpermute_b32 v0, v161, v4
	ds_bpermute_b32 v1, v161, v5
	ds_bpermute_b32 v2, v161, v6
	ds_bpermute_b32 v3, v161, v3
	s_and_b64 vcc, exec, s[20:21]
	v_mov_b32_e32 v174, v217
	v_mov_b32_e32 v168, v215
	v_mov_b32_e32 v176, v216
	v_mov_b32_e32 v170, v214
	s_mov_b32 s6, s14
	s_mov_b32 s22, s12
	s_mov_b64 s[26:27], s[16:17]
	s_mov_b64 s[24:25], s[18:19]
	s_mov_b32 s7, s85
	s_waitcnt lgkmcnt(0)
	global_store_dwordx4 v[22:23], v[0:3], off offset:256 sc1
	s_cbranch_vccnz .LBB0_573

.LBB0_543:
	v_cvt_pk_bf16_f32 v12, v12, v13
	s_nop 0
	v_cvt_pk_bf16_f32 v13, v14, v15
	v_lshl_add_u32 v152, s6, 8, v177
	v_cvt_pk_bf16_f32 v8, v8, v9
	v_cvt_pk_bf16_f32 v9, v10, v11
	ds_bpermute_b32 v10, v161, v8
	ds_bpermute_b32 v11, v161, v9
	ds_bpermute_b32 v12, v161, v12
	ds_bpermute_b32 v13, v161, v13
	v_readlane_b32 s6, v250, 39
	v_readlane_b32 s7, v250, 40
	v_lshl_or_b32 v22, s22, 8, v197
	v_ashrrev_i32_e32 v23, 31, v22
	v_mov_b64_e32 v[8:9], s[6:7]
	v_mad_i64_i32 v[8:9], s[6:7], v152, s66, v[8:9]
	v_lshl_add_u64 v[8:9], v[22:23], 1, v[8:9]
	v_mov_b32_e32 v25, v24
	s_waitcnt lgkmcnt(0)
	global_store_dwordx4 v[8:9], v[10:13], off sc1
	v_cndmask_b32_e64 v18, 0, 1, s[24:25]
	v_pk_fma_f32 v[16:17], v[24:25], v[148:149], v[4:5]
	v_mov_b32_e32 v12, v24
	v_mov_b32_e32 v13, v24
	v_pk_fma_f32 v[10:11], v[12:13], v[150:151], v[6:7]
	v_pk_fma_f32 v[14:15], v[12:13], v[146:147], v[2:3]
	v_cmp_ne_u32_e64 s[6:7], 1, v18
	s_andn2_b64 vcc, exec, s[24:25]
	v_pk_fma_f32 v[18:19], v[24:25], v[144:145], v[0:1]
	s_cbranch_vccnz .LBB0_545
	v_pk_mul_f32 v[20:21], v[10:11], v[10:11]
	v_pk_mul_f32 v[26:27], v[16:17], v[16:17]
	v_pk_mul_f32 v[28:29], v[14:15], v[14:15]
	v_pk_mul_f32 v[30:31], v[18:19], v[18:19]
	v_pk_mul_f32 v[20:21], v[10:11], v[20:21]
	v_pk_mul_f32 v[26:27], v[16:17], v[26:27]
	v_pk_mul_f32 v[28:29], v[14:15], v[28:29]
	v_pk_mul_f32 v[30:31], v[18:19], v[30:31]
	v_pk_fma_f32 v[26:27], v[26:27], s[42:43], v[16:17] op_sel_hi:[1,0,1]
	v_pk_fma_f32 v[20:21], v[20:21], s[42:43], v[10:11] op_sel_hi:[1,0,1]
	v_pk_fma_f32 v[30:31], v[30:31], s[42:43], v[18:19] op_sel_hi:[1,0,1]
	v_pk_fma_f32 v[28:29], v[28:29], s[42:43], v[14:15] op_sel_hi:[1,0,1]
	v_pk_mul_f32 v[26:27], v[26:27], s[96:97] op_sel_hi:[1,0]
	v_pk_mul_f32 v[20:21], v[20:21], s[96:97] op_sel_hi:[1,0]
	v_pk_mul_f32 v[30:31], v[30:31], s[96:97] op_sel_hi:[1,0]
	v_pk_mul_f32 v[28:29], v[28:29], s[96:97] op_sel_hi:[1,0]
	v_exp_f32_e32 v26, v26
	v_exp_f32_e32 v27, v27
	v_exp_f32_e32 v20, v20
	v_exp_f32_e32 v21, v21
	v_exp_f32_e32 v30, v30
	v_exp_f32_e32 v31, v31
	v_exp_f32_e32 v28, v28
	v_exp_f32_e32 v29, v29
	v_pk_add_f32 v[26:27], v[26:27], 1.0 op_sel_hi:[1,0]
	v_pk_add_f32 v[20:21], v[20:21], 1.0 op_sel_hi:[1,0]
	v_pk_add_f32 v[30:31], v[30:31], 1.0 op_sel_hi:[1,0]
	v_pk_add_f32 v[28:29], v[28:29], 1.0 op_sel_hi:[1,0]
	v_rcp_f32_e32 v26, v26
	v_rcp_f32_e32 v27, v27
	v_rcp_f32_e32 v20, v20
	v_rcp_f32_e32 v21, v21
	v_rcp_f32_e32 v30, v30
	v_rcp_f32_e32 v31, v31
	v_rcp_f32_e32 v28, v28
	v_rcp_f32_e32 v29, v29
	v_pk_mul_f32 v[16:17], v[16:17], v[26:27]
	v_pk_mul_f32 v[10:11], v[10:11], v[20:21]
	v_pk_mul_f32 v[18:19], v[18:19], v[30:31]
	v_pk_mul_f32 v[14:15], v[14:15], v[28:29]
.LBB0_545:
	v_cvt_pk_bf16_f32 v16, v16, v17
	s_nop 0
	v_cvt_pk_bf16_f32 v17, v14, v15
	v_cvt_pk_bf16_f32 v10, v10, v11
	v_cvt_pk_bf16_f32 v11, v18, v19
	ds_bpermute_b32 v14, v161, v16
	ds_bpermute_b32 v15, v161, v10
	ds_bpermute_b32 v16, v161, v11
	ds_bpermute_b32 v17, v161, v17
	v_readlane_b32 s22, v250, 39
	v_readlane_b32 s23, v250, 40
	v_or_b32_e32 v18, 16, v152
	s_movk_i32 s72, 0x48
	v_mov_b64_e32 v[10:11], s[22:23]
	v_mad_i64_i32 v[10:11], s[22:23], v18, s66, v[10:11]
	v_lshl_add_u64 v[10:11], v[22:23], 1, v[10:11]
	s_waitcnt lgkmcnt(0)
	global_store_dwordx4 v[10:11], v[14:17], off sc1
	s_and_b64 vcc, exec, s[6:7]
	v_pk_fma_f32 v[18:19], v[24:25], v[136:137], v[0:1]
	v_pk_fma_f32 v[14:15], v[12:13], v[142:143], v[6:7]
	v_pk_fma_f32 v[16:17], v[24:25], v[140:141], v[4:5]
	v_pk_fma_f32 v[12:13], v[12:13], v[138:139], v[2:3]
	s_cbranch_vccnz .LBB0_547
	v_pk_mul_f32 v[20:21], v[14:15], v[14:15]
	v_pk_mul_f32 v[26:27], v[16:17], v[16:17]
	v_pk_mul_f32 v[28:29], v[12:13], v[12:13]
	v_pk_mul_f32 v[30:31], v[18:19], v[18:19]
	v_pk_mul_f32 v[20:21], v[14:15], v[20:21]
	v_pk_mul_f32 v[26:27], v[16:17], v[26:27]
	v_pk_mul_f32 v[28:29], v[12:13], v[28:29]
	v_pk_mul_f32 v[30:31], v[18:19], v[30:31]
	v_pk_fma_f32 v[26:27], v[26:27], s[42:43], v[16:17] op_sel_hi:[1,0,1]
	v_pk_fma_f32 v[20:21], v[20:21], s[42:43], v[14:15] op_sel_hi:[1,0,1]
	v_pk_fma_f32 v[30:31], v[30:31], s[42:43], v[18:19] op_sel_hi:[1,0,1]
	v_pk_fma_f32 v[28:29], v[28:29], s[42:43], v[12:13] op_sel_hi:[1,0,1]
	v_pk_mul_f32 v[26:27], v[26:27], s[96:97] op_sel_hi:[1,0]
	v_pk_mul_f32 v[20:21], v[20:21], s[96:97] op_sel_hi:[1,0]
	v_pk_mul_f32 v[30:31], v[30:31], s[96:97] op_sel_hi:[1,0]
	v_pk_mul_f32 v[28:29], v[28:29], s[96:97] op_sel_hi:[1,0]
	v_exp_f32_e32 v26, v26
	v_exp_f32_e32 v27, v27
	v_exp_f32_e32 v20, v20
	v_exp_f32_e32 v21, v21
	v_exp_f32_e32 v30, v30
	v_exp_f32_e32 v31, v31
	v_exp_f32_e32 v28, v28
	v_exp_f32_e32 v29, v29
	v_pk_add_f32 v[26:27], v[26:27], 1.0 op_sel_hi:[1,0]
	v_pk_add_f32 v[20:21], v[20:21], 1.0 op_sel_hi:[1,0]
	v_pk_add_f32 v[30:31], v[30:31], 1.0 op_sel_hi:[1,0]
	v_pk_add_f32 v[28:29], v[28:29], 1.0 op_sel_hi:[1,0]
	v_rcp_f32_e32 v26, v26
	v_rcp_f32_e32 v27, v27
	v_rcp_f32_e32 v20, v20
	v_rcp_f32_e32 v21, v21
	v_rcp_f32_e32 v30, v30
	v_rcp_f32_e32 v31, v31
	v_rcp_f32_e32 v28, v28
	v_rcp_f32_e32 v29, v29
	v_pk_mul_f32 v[16:17], v[16:17], v[26:27]
	v_pk_mul_f32 v[14:15], v[14:15], v[20:21]
	v_pk_mul_f32 v[18:19], v[18:19], v[30:31]
	v_pk_mul_f32 v[12:13], v[12:13], v[28:29]
.LBB0_547:
	v_cvt_pk_bf16_f32 v16, v16, v17
	v_cvt_pk_bf16_f32 v15, v14, v15
	v_cvt_pk_bf16_f32 v17, v18, v19
	s_nop 0
	v_cvt_pk_bf16_f32 v12, v12, v13
	ds_bpermute_b32 v14, v161, v16
	ds_bpermute_b32 v15, v161, v15
	ds_bpermute_b32 v16, v161, v17
	ds_bpermute_b32 v17, v161, v12
	v_readlane_b32 s22, v250, 39
	v_readlane_b32 s23, v250, 40
	v_or_b32_e32 v18, 32, v152
	v_pk_fma_f32 v[20:21], v[24:25], v[132:133], v[4:5]
	v_mov_b64_e32 v[12:13], s[22:23]
	v_mad_i64_i32 v[12:13], s[22:23], v18, s66, v[12:13]
	v_lshl_add_u64 v[12:13], v[22:23], 1, v[12:13]
	s_waitcnt lgkmcnt(0)
	global_store_dwordx4 v[12:13], v[14:17], off sc1
	s_and_b64 vcc, exec, s[6:7]
	v_pk_fma_f32 v[26:27], v[24:25], v[128:129], v[0:1]
	v_mov_b32_e32 v16, v24
	v_mov_b32_e32 v17, v24
	v_pk_fma_f32 v[14:15], v[16:17], v[134:135], v[6:7]
	v_pk_fma_f32 v[18:19], v[16:17], v[130:131], v[2:3]
	s_cbranch_vccnz .LBB0_549
	v_pk_mul_f32 v[28:29], v[14:15], v[14:15]
	v_pk_mul_f32 v[30:31], v[20:21], v[20:21]
	v_pk_mul_f32 v[128:129], v[18:19], v[18:19]
	v_pk_mul_f32 v[130:131], v[26:27], v[26:27]
	v_pk_mul_f32 v[28:29], v[14:15], v[28:29]
	v_pk_mul_f32 v[30:31], v[20:21], v[30:31]
	v_pk_mul_f32 v[128:129], v[18:19], v[128:129]
	v_pk_mul_f32 v[130:131], v[26:27], v[130:131]
	v_pk_fma_f32 v[30:31], v[30:31], s[42:43], v[20:21] op_sel_hi:[1,0,1]
	v_pk_fma_f32 v[28:29], v[28:29], s[42:43], v[14:15] op_sel_hi:[1,0,1]
	v_pk_fma_f32 v[130:131], v[130:131], s[42:43], v[26:27] op_sel_hi:[1,0,1]
	v_pk_fma_f32 v[128:129], v[128:129], s[42:43], v[18:19] op_sel_hi:[1,0,1]
	v_pk_mul_f32 v[30:31], v[30:31], s[96:97] op_sel_hi:[1,0]
	v_pk_mul_f32 v[28:29], v[28:29], s[96:97] op_sel_hi:[1,0]
	v_pk_mul_f32 v[130:131], v[130:131], s[96:97] op_sel_hi:[1,0]
	v_pk_mul_f32 v[128:129], v[128:129], s[96:97] op_sel_hi:[1,0]
	v_exp_f32_e32 v30, v30
	v_exp_f32_e32 v31, v31
	v_exp_f32_e32 v28, v28
	v_exp_f32_e32 v29, v29
	v_exp_f32_e32 v130, v130
	v_exp_f32_e32 v131, v131
	v_exp_f32_e32 v128, v128
	v_exp_f32_e32 v129, v129
	v_pk_add_f32 v[30:31], v[30:31], 1.0 op_sel_hi:[1,0]
	v_pk_add_f32 v[28:29], v[28:29], 1.0 op_sel_hi:[1,0]
	v_pk_add_f32 v[130:131], v[130:131], 1.0 op_sel_hi:[1,0]
	v_pk_add_f32 v[128:129], v[128:129], 1.0 op_sel_hi:[1,0]
	v_rcp_f32_e32 v30, v30
	v_rcp_f32_e32 v31, v31
	v_rcp_f32_e32 v28, v28
	v_rcp_f32_e32 v29, v29
	v_rcp_f32_e32 v130, v130
	v_rcp_f32_e32 v131, v131
	v_rcp_f32_e32 v128, v128
	v_rcp_f32_e32 v129, v129
	v_pk_mul_f32 v[20:21], v[20:21], v[30:31]
	v_pk_mul_f32 v[14:15], v[14:15], v[28:29]
	v_pk_mul_f32 v[26:27], v[26:27], v[130:131]
	v_pk_mul_f32 v[18:19], v[18:19], v[128:129]
.LBB0_549:
	v_cvt_pk_bf16_f32 v20, v20, v21
	s_nop 0
	v_cvt_pk_bf16_f32 v21, v18, v19
	v_cvt_pk_bf16_f32 v14, v14, v15
	v_cvt_pk_bf16_f32 v15, v26, v27
	ds_bpermute_b32 v18, v161, v20
	ds_bpermute_b32 v19, v161, v14
	ds_bpermute_b32 v20, v161, v15
	ds_bpermute_b32 v21, v161, v21
	v_readlane_b32 s22, v250, 39
	v_readlane_b32 s23, v250, 40
	v_or_b32_e32 v26, 48, v152
	s_and_b64 vcc, exec, s[6:7]
	v_mov_b64_e32 v[14:15], s[22:23]
	v_mad_i64_i32 v[14:15], s[22:23], v26, s66, v[14:15]
	v_lshl_add_u64 v[14:15], v[22:23], 1, v[14:15]
	s_waitcnt lgkmcnt(0)
	global_store_dwordx4 v[14:15], v[18:21], off sc1
	v_pk_fma_f32 v[26:27], v[24:25], v[120:121], v[0:1]
	s_nop 0
	v_pk_fma_f32 v[18:19], v[16:17], v[126:127], v[6:7]
	v_pk_fma_f32 v[20:21], v[24:25], v[124:125], v[4:5]
	v_pk_fma_f32 v[16:17], v[16:17], v[122:123], v[2:3]
	s_cbranch_vccnz .LBB0_551
	v_pk_mul_f32 v[28:29], v[18:19], v[18:19]
	v_pk_mul_f32 v[30:31], v[20:21], v[20:21]
	v_pk_mul_f32 v[120:121], v[16:17], v[16:17]
	v_pk_mul_f32 v[122:123], v[26:27], v[26:27]
	v_pk_mul_f32 v[28:29], v[18:19], v[28:29]
	v_pk_mul_f32 v[30:31], v[20:21], v[30:31]
	v_pk_mul_f32 v[120:121], v[16:17], v[120:121]
	v_pk_mul_f32 v[122:123], v[26:27], v[122:123]
	v_pk_fma_f32 v[30:31], v[30:31], s[42:43], v[20:21] op_sel_hi:[1,0,1]
	v_pk_fma_f32 v[28:29], v[28:29], s[42:43], v[18:19] op_sel_hi:[1,0,1]
	v_pk_fma_f32 v[122:123], v[122:123], s[42:43], v[26:27] op_sel_hi:[1,0,1]
	v_pk_fma_f32 v[120:121], v[120:121], s[42:43], v[16:17] op_sel_hi:[1,0,1]
	v_pk_mul_f32 v[30:31], v[30:31], s[96:97] op_sel_hi:[1,0]
	v_pk_mul_f32 v[28:29], v[28:29], s[96:97] op_sel_hi:[1,0]
	v_pk_mul_f32 v[122:123], v[122:123], s[96:97] op_sel_hi:[1,0]
	v_pk_mul_f32 v[120:121], v[120:121], s[96:97] op_sel_hi:[1,0]
	v_exp_f32_e32 v30, v30
	v_exp_f32_e32 v31, v31
	v_exp_f32_e32 v28, v28
	v_exp_f32_e32 v29, v29
	v_exp_f32_e32 v122, v122
	v_exp_f32_e32 v123, v123
	v_exp_f32_e32 v120, v120
	v_exp_f32_e32 v121, v121
	v_pk_add_f32 v[30:31], v[30:31], 1.0 op_sel_hi:[1,0]
	v_pk_add_f32 v[28:29], v[28:29], 1.0 op_sel_hi:[1,0]
	v_pk_add_f32 v[122:123], v[122:123], 1.0 op_sel_hi:[1,0]
	v_pk_add_f32 v[120:121], v[120:121], 1.0 op_sel_hi:[1,0]
	v_rcp_f32_e32 v30, v30
	v_rcp_f32_e32 v31, v31
	v_rcp_f32_e32 v28, v28
	v_rcp_f32_e32 v29, v29
	v_rcp_f32_e32 v122, v122
	v_rcp_f32_e32 v123, v123
	v_rcp_f32_e32 v120, v120
	v_rcp_f32_e32 v121, v121
	v_pk_mul_f32 v[20:21], v[20:21], v[30:31]
	v_pk_mul_f32 v[18:19], v[18:19], v[28:29]
	v_pk_mul_f32 v[26:27], v[26:27], v[122:123]
	v_pk_mul_f32 v[16:17], v[16:17], v[120:121]
.LBB0_551:
	v_cvt_pk_bf16_f32 v20, v20, v21
	v_cvt_pk_bf16_f32 v19, v18, v19
	v_cvt_pk_bf16_f32 v21, v26, v27
	s_nop 0
	v_cvt_pk_bf16_f32 v16, v16, v17
	ds_bpermute_b32 v18, v161, v20
	ds_bpermute_b32 v19, v161, v19
	ds_bpermute_b32 v20, v161, v21
	ds_bpermute_b32 v21, v161, v16
	v_readlane_b32 s22, v250, 39
	v_readlane_b32 s23, v250, 40
	v_add_u32_e32 v28, 0x80, v152
	s_and_b64 vcc, exec, s[6:7]
	v_mov_b64_e32 v[16:17], s[22:23]
	v_mad_i64_i32 v[16:17], s[22:23], v28, s66, v[16:17]
	v_lshl_add_u64 v[16:17], v[22:23], 1, v[16:17]
	s_waitcnt lgkmcnt(0)
	global_store_dwordx4 v[16:17], v[18:21], off sc1
	v_pk_fma_f32 v[28:29], v[24:25], v[116:117], v[4:5]
	v_pk_fma_f32 v[30:31], v[24:25], v[112:113], v[0:1]
	v_mov_b32_e32 v20, v24
	v_mov_b32_e32 v21, v24
	v_pk_fma_f32 v[18:19], v[20:21], v[118:119], v[6:7]
	v_pk_fma_f32 v[26:27], v[20:21], v[114:115], v[2:3]
	s_cbranch_vccnz .LBB0_553
	v_pk_mul_f32 v[112:113], v[18:19], v[18:19]
	v_pk_mul_f32 v[114:115], v[28:29], v[28:29]
	v_pk_mul_f32 v[116:117], v[26:27], v[26:27]
	v_pk_mul_f32 v[118:119], v[30:31], v[30:31]
	v_pk_mul_f32 v[112:113], v[18:19], v[112:113]
	v_pk_mul_f32 v[114:115], v[28:29], v[114:115]
	v_pk_mul_f32 v[116:117], v[26:27], v[116:117]
	v_pk_mul_f32 v[118:119], v[30:31], v[118:119]
	v_pk_fma_f32 v[114:115], v[114:115], s[42:43], v[28:29] op_sel_hi:[1,0,1]
	v_pk_fma_f32 v[112:113], v[112:113], s[42:43], v[18:19] op_sel_hi:[1,0,1]
	v_pk_fma_f32 v[118:119], v[118:119], s[42:43], v[30:31] op_sel_hi:[1,0,1]
	v_pk_fma_f32 v[116:117], v[116:117], s[42:43], v[26:27] op_sel_hi:[1,0,1]
	v_pk_mul_f32 v[114:115], v[114:115], s[96:97] op_sel_hi:[1,0]
	v_pk_mul_f32 v[112:113], v[112:113], s[96:97] op_sel_hi:[1,0]
	v_pk_mul_f32 v[118:119], v[118:119], s[96:97] op_sel_hi:[1,0]
	v_pk_mul_f32 v[116:117], v[116:117], s[96:97] op_sel_hi:[1,0]
	v_exp_f32_e32 v114, v114
	v_exp_f32_e32 v115, v115
	v_exp_f32_e32 v112, v112
	v_exp_f32_e32 v113, v113
	v_exp_f32_e32 v118, v118
	v_exp_f32_e32 v119, v119
	v_exp_f32_e32 v116, v116
	v_exp_f32_e32 v117, v117
	v_pk_add_f32 v[114:115], v[114:115], 1.0 op_sel_hi:[1,0]
	v_pk_add_f32 v[112:113], v[112:113], 1.0 op_sel_hi:[1,0]
	v_pk_add_f32 v[118:119], v[118:119], 1.0 op_sel_hi:[1,0]
	v_pk_add_f32 v[116:117], v[116:117], 1.0 op_sel_hi:[1,0]
	v_rcp_f32_e32 v114, v114
	v_rcp_f32_e32 v115, v115
	v_rcp_f32_e32 v112, v112
	v_rcp_f32_e32 v113, v113
	v_rcp_f32_e32 v118, v118
	v_rcp_f32_e32 v119, v119
	v_rcp_f32_e32 v116, v116
	v_rcp_f32_e32 v117, v117
	v_pk_mul_f32 v[28:29], v[28:29], v[114:115]
	v_pk_mul_f32 v[18:19], v[18:19], v[112:113]
	v_pk_mul_f32 v[30:31], v[30:31], v[118:119]
	v_pk_mul_f32 v[26:27], v[26:27], v[116:117]
.LBB0_553:
	v_cvt_pk_bf16_f32 v28, v28, v29
	s_nop 0
	v_cvt_pk_bf16_f32 v29, v26, v27
	v_cvt_pk_bf16_f32 v18, v18, v19
	v_cvt_pk_bf16_f32 v19, v30, v31
	ds_bpermute_b32 v26, v161, v28
	ds_bpermute_b32 v27, v161, v18
	ds_bpermute_b32 v28, v161, v19
	ds_bpermute_b32 v29, v161, v29
	v_readlane_b32 s22, v250, 39
	v_readlane_b32 s23, v250, 40
	v_add_u32_e32 v30, 0x90, v152
	s_and_b64 vcc, exec, s[6:7]
	v_mov_b64_e32 v[18:19], s[22:23]
	v_mad_i64_i32 v[18:19], s[22:23], v30, s66, v[18:19]
	v_lshl_add_u64 v[18:19], v[22:23], 1, v[18:19]
	s_waitcnt lgkmcnt(0)
	global_store_dwordx4 v[18:19], v[26:29], off sc1
	v_pk_fma_f32 v[30:31], v[24:25], v[104:105], v[0:1]
	s_nop 0
	v_pk_fma_f32 v[26:27], v[20:21], v[110:111], v[6:7]
	v_pk_fma_f32 v[28:29], v[24:25], v[108:109], v[4:5]
	v_pk_fma_f32 v[20:21], v[20:21], v[106:107], v[2:3]
	s_cbranch_vccnz .LBB0_555
	v_pk_mul_f32 v[104:105], v[26:27], v[26:27]
	v_pk_mul_f32 v[106:107], v[28:29], v[28:29]
	v_pk_mul_f32 v[108:109], v[20:21], v[20:21]
	v_pk_mul_f32 v[110:111], v[30:31], v[30:31]
	v_pk_mul_f32 v[104:105], v[26:27], v[104:105]
	v_pk_mul_f32 v[106:107], v[28:29], v[106:107]
	v_pk_mul_f32 v[108:109], v[20:21], v[108:109]
	v_pk_mul_f32 v[110:111], v[30:31], v[110:111]
	v_pk_fma_f32 v[106:107], v[106:107], s[42:43], v[28:29] op_sel_hi:[1,0,1]
	v_pk_fma_f32 v[104:105], v[104:105], s[42:43], v[26:27] op_sel_hi:[1,0,1]
	v_pk_fma_f32 v[110:111], v[110:111], s[42:43], v[30:31] op_sel_hi:[1,0,1]
	v_pk_fma_f32 v[108:109], v[108:109], s[42:43], v[20:21] op_sel_hi:[1,0,1]
	v_pk_mul_f32 v[106:107], v[106:107], s[96:97] op_sel_hi:[1,0]
	v_pk_mul_f32 v[104:105], v[104:105], s[96:97] op_sel_hi:[1,0]
	v_pk_mul_f32 v[110:111], v[110:111], s[96:97] op_sel_hi:[1,0]
	v_pk_mul_f32 v[108:109], v[108:109], s[96:97] op_sel_hi:[1,0]
	v_exp_f32_e32 v106, v106
	v_exp_f32_e32 v107, v107
	v_exp_f32_e32 v104, v104
	v_exp_f32_e32 v105, v105
	v_exp_f32_e32 v110, v110
	v_exp_f32_e32 v111, v111
	v_exp_f32_e32 v108, v108
	v_exp_f32_e32 v109, v109
	v_pk_add_f32 v[106:107], v[106:107], 1.0 op_sel_hi:[1,0]
	v_pk_add_f32 v[104:105], v[104:105], 1.0 op_sel_hi:[1,0]
	v_pk_add_f32 v[110:111], v[110:111], 1.0 op_sel_hi:[1,0]
	v_pk_add_f32 v[108:109], v[108:109], 1.0 op_sel_hi:[1,0]
	v_rcp_f32_e32 v106, v106
	v_rcp_f32_e32 v107, v107
	v_rcp_f32_e32 v104, v104
	v_rcp_f32_e32 v105, v105
	v_rcp_f32_e32 v110, v110
	v_rcp_f32_e32 v111, v111
	v_rcp_f32_e32 v108, v108
	v_rcp_f32_e32 v109, v109
	v_pk_mul_f32 v[28:29], v[28:29], v[106:107]
	v_pk_mul_f32 v[26:27], v[26:27], v[104:105]
	v_pk_mul_f32 v[30:31], v[30:31], v[110:111]
	v_pk_mul_f32 v[20:21], v[20:21], v[108:109]
.LBB0_555:
	v_cvt_pk_bf16_f32 v28, v28, v29
	v_cvt_pk_bf16_f32 v27, v26, v27
	v_cvt_pk_bf16_f32 v29, v30, v31
	s_nop 0
	v_cvt_pk_bf16_f32 v20, v20, v21
	ds_bpermute_b32 v26, v161, v28
	ds_bpermute_b32 v27, v161, v27
	ds_bpermute_b32 v28, v161, v29
	ds_bpermute_b32 v29, v161, v20
	v_readlane_b32 s22, v250, 39
	v_readlane_b32 s23, v250, 40
	v_add_u32_e32 v30, 0xa0, v152
	v_pk_fma_f32 v[4:5], v[24:25], v[100:101], v[4:5]
	v_mov_b64_e32 v[20:21], s[22:23]
	v_mad_i64_i32 v[20:21], s[22:23], v30, s66, v[20:21]
	v_lshl_add_u64 v[20:21], v[22:23], 1, v[20:21]
	s_waitcnt lgkmcnt(0)
	global_store_dwordx4 v[20:21], v[26:29], off sc1
	s_and_b64 vcc, exec, s[6:7]
	v_pk_fma_f32 v[0:1], v[24:25], v[96:97], v[0:1]
	v_mov_b32_e32 v26, v24
	v_mov_b32_e32 v27, v24
	v_pk_fma_f32 v[6:7], v[26:27], v[102:103], v[6:7]
	v_pk_fma_f32 v[2:3], v[26:27], v[98:99], v[2:3]
	s_cbranch_vccnz .LBB0_557
	v_pk_mul_f32 v[24:25], v[6:7], v[6:7]
	v_pk_mul_f32 v[26:27], v[4:5], v[4:5]
	v_pk_mul_f32 v[28:29], v[2:3], v[2:3]
	v_pk_mul_f32 v[30:31], v[0:1], v[0:1]
	v_pk_mul_f32 v[24:25], v[6:7], v[24:25]
	v_pk_mul_f32 v[26:27], v[4:5], v[26:27]
	v_pk_mul_f32 v[28:29], v[2:3], v[28:29]
	v_pk_mul_f32 v[30:31], v[0:1], v[30:31]
	v_pk_fma_f32 v[26:27], v[26:27], s[42:43], v[4:5] op_sel_hi:[1,0,1]
	v_pk_fma_f32 v[24:25], v[24:25], s[42:43], v[6:7] op_sel_hi:[1,0,1]
	v_pk_fma_f32 v[30:31], v[30:31], s[42:43], v[0:1] op_sel_hi:[1,0,1]
	v_pk_fma_f32 v[28:29], v[28:29], s[42:43], v[2:3] op_sel_hi:[1,0,1]
	v_pk_mul_f32 v[26:27], v[26:27], s[96:97] op_sel_hi:[1,0]
	v_pk_mul_f32 v[24:25], v[24:25], s[96:97] op_sel_hi:[1,0]
	v_pk_mul_f32 v[30:31], v[30:31], s[96:97] op_sel_hi:[1,0]
	v_pk_mul_f32 v[28:29], v[28:29], s[96:97] op_sel_hi:[1,0]
	v_exp_f32_e32 v26, v26
	v_exp_f32_e32 v27, v27
	v_exp_f32_e32 v24, v24
	v_exp_f32_e32 v25, v25
	v_exp_f32_e32 v30, v30
	v_exp_f32_e32 v31, v31
	v_exp_f32_e32 v28, v28
	v_exp_f32_e32 v29, v29
	v_pk_add_f32 v[26:27], v[26:27], 1.0 op_sel_hi:[1,0]
	v_pk_add_f32 v[24:25], v[24:25], 1.0 op_sel_hi:[1,0]
	v_pk_add_f32 v[30:31], v[30:31], 1.0 op_sel_hi:[1,0]
	v_pk_add_f32 v[28:29], v[28:29], 1.0 op_sel_hi:[1,0]
	v_rcp_f32_e32 v26, v26
	v_rcp_f32_e32 v27, v27
	v_rcp_f32_e32 v24, v24
	v_rcp_f32_e32 v25, v25
	v_rcp_f32_e32 v30, v30
	v_rcp_f32_e32 v31, v31
	v_rcp_f32_e32 v28, v28
	v_rcp_f32_e32 v29, v29
	v_pk_mul_f32 v[4:5], v[4:5], v[26:27]
	v_pk_mul_f32 v[6:7], v[6:7], v[24:25]
	v_pk_mul_f32 v[0:1], v[0:1], v[30:31]
	v_pk_mul_f32 v[2:3], v[2:3], v[28:29]
.LBB0_557:
	s_nop 0
	v_cvt_pk_bf16_f32 v3, v2, v3
	v_cvt_pk_bf16_f32 v4, v4, v5
	v_cvt_pk_bf16_f32 v5, v6, v7
	v_cvt_pk_bf16_f32 v6, v0, v1
	ds_bpermute_b32 v0, v161, v4
	ds_bpermute_b32 v1, v161, v5
	ds_bpermute_b32 v2, v161, v6
	ds_bpermute_b32 v3, v161, v3
	v_readlane_b32 s6, v250, 39
	v_readlane_b32 s7, v250, 40
	v_add_u32_e32 v6, 0xb0, v152
	s_add_i32 s3, s2, -14
	v_mov_b64_e32 v[4:5], s[6:7]
	v_mad_i64_i32 v[4:5], s[6:7], v6, s66, v[4:5]
	v_lshl_add_u64 v[22:23], v[22:23], 1, v[4:5]
	s_waitcnt lgkmcnt(0)
	global_store_dwordx4 v[22:23], v[0:3], off sc1
	s_cmp_lt_u32 s3, 3
	ds_read_b128 v[4:7], v168 offset:512
	ds_read_b128 v[0:3], v168 offset:528
	s_cselect_b64 s[22:23], -1, 0
	s_add_i32 s2, s2, -2
	s_cmp_lt_u32 s2, 3
	s_cselect_b64 vcc, -1, 0
	v_mov_b32_e32 v24, 0x3b5105ec
	v_cndmask_b32_e32 v24, v200, v24, vcc
	s_cmp_gt_u32 s3, 2
	s_waitcnt lgkmcnt(0)
	v_pk_fma_f32 v[26:27], v[24:25], v[94:95], v[6:7] op_sel_hi:[0,1,1]
	v_pk_fma_f32 v[28:29], v[24:25], v[92:93], v[4:5] op_sel_hi:[0,1,1]
	v_pk_fma_f32 v[30:31], v[24:25], v[90:91], v[2:3] op_sel_hi:[0,1,1]
	v_pk_fma_f32 v[88:89], v[24:25], v[88:89], v[0:1] op_sel_hi:[0,1,1]
	s_cbranch_scc1 .LBB0_559
	v_pk_mul_f32 v[90:91], v[26:27], v[26:27]
	v_pk_mul_f32 v[92:93], v[28:29], v[28:29]
	v_pk_mul_f32 v[94:95], v[30:31], v[30:31]
	v_pk_mul_f32 v[96:97], v[88:89], v[88:89]
	v_pk_mul_f32 v[90:91], v[26:27], v[90:91]
	v_pk_mul_f32 v[92:93], v[28:29], v[92:93]
	v_pk_mul_f32 v[94:95], v[30:31], v[94:95]
	v_pk_mul_f32 v[96:97], v[88:89], v[96:97]
	v_pk_fma_f32 v[92:93], v[92:93], s[42:43], v[28:29] op_sel_hi:[1,0,1]
	v_pk_fma_f32 v[90:91], v[90:91], s[42:43], v[26:27] op_sel_hi:[1,0,1]
	v_pk_fma_f32 v[96:97], v[96:97], s[42:43], v[88:89] op_sel_hi:[1,0,1]
	v_pk_fma_f32 v[94:95], v[94:95], s[42:43], v[30:31] op_sel_hi:[1,0,1]
	v_pk_mul_f32 v[92:93], v[92:93], s[96:97] op_sel_hi:[1,0]
	v_pk_mul_f32 v[90:91], v[90:91], s[96:97] op_sel_hi:[1,0]
	v_pk_mul_f32 v[96:97], v[96:97], s[96:97] op_sel_hi:[1,0]
	v_pk_mul_f32 v[94:95], v[94:95], s[96:97] op_sel_hi:[1,0]
	v_exp_f32_e32 v92, v92
	v_exp_f32_e32 v93, v93
	v_exp_f32_e32 v90, v90
	v_exp_f32_e32 v91, v91
	v_exp_f32_e32 v96, v96
	v_exp_f32_e32 v97, v97
	v_exp_f32_e32 v94, v94
	v_exp_f32_e32 v95, v95
	v_pk_add_f32 v[92:93], v[92:93], 1.0 op_sel_hi:[1,0]
	v_pk_add_f32 v[90:91], v[90:91], 1.0 op_sel_hi:[1,0]
	v_pk_add_f32 v[96:97], v[96:97], 1.0 op_sel_hi:[1,0]
	v_pk_add_f32 v[94:95], v[94:95], 1.0 op_sel_hi:[1,0]
	v_rcp_f32_e32 v92, v92
	v_rcp_f32_e32 v93, v93
	v_rcp_f32_e32 v90, v90
	v_rcp_f32_e32 v91, v91
	v_rcp_f32_e32 v96, v96
	v_rcp_f32_e32 v97, v97
	v_rcp_f32_e32 v94, v94
	v_rcp_f32_e32 v95, v95
	v_pk_mul_f32 v[28:29], v[28:29], v[92:93]
	v_pk_mul_f32 v[26:27], v[26:27], v[90:91]
	v_pk_mul_f32 v[88:89], v[88:89], v[96:97]
	v_pk_mul_f32 v[30:31], v[30:31], v[94:95]
.LBB0_559:
	v_cvt_pk_bf16_f32 v25, v28, v29
	v_cvt_pk_bf16_f32 v27, v26, v27
	v_cvt_pk_bf16_f32 v28, v88, v89
	s_nop 0
	v_cvt_pk_bf16_f32 v29, v30, v31
	ds_bpermute_b32 v26, v161, v25
	ds_bpermute_b32 v27, v161, v27
	ds_bpermute_b32 v28, v161, v28
	ds_bpermute_b32 v29, v161, v29
	v_mov_b32_e32 v25, v24
	v_pk_fma_f32 v[30:31], v[24:25], v[84:85], v[4:5]
	s_andn2_b64 vcc, exec, s[22:23]
	v_pk_fma_f32 v[80:81], v[24:25], v[80:81], v[0:1]
	s_waitcnt lgkmcnt(0)
	global_store_dwordx4 v[8:9], v[26:29], off offset:256 sc1
	v_mov_b32_e32 v8, v24
	v_mov_b32_e32 v9, v24
	v_pk_fma_f32 v[28:29], v[8:9], v[82:83], v[2:3]
	v_cndmask_b32_e64 v82, 0, 1, s[22:23]
	v_pk_fma_f32 v[26:27], v[8:9], v[86:87], v[6:7]
	v_cmp_ne_u32_e64 s[6:7], 1, v82
	s_cbranch_vccnz .LBB0_561
	v_pk_mul_f32 v[82:83], v[26:27], v[26:27]
	v_pk_mul_f32 v[84:85], v[30:31], v[30:31]
	v_pk_mul_f32 v[86:87], v[28:29], v[28:29]
	v_pk_mul_f32 v[88:89], v[80:81], v[80:81]
	v_pk_mul_f32 v[82:83], v[26:27], v[82:83]
	v_pk_mul_f32 v[84:85], v[30:31], v[84:85]
	v_pk_mul_f32 v[86:87], v[28:29], v[86:87]
	v_pk_mul_f32 v[88:89], v[80:81], v[88:89]
	v_pk_fma_f32 v[84:85], v[84:85], s[42:43], v[30:31] op_sel_hi:[1,0,1]
	v_pk_fma_f32 v[82:83], v[82:83], s[42:43], v[26:27] op_sel_hi:[1,0,1]
	v_pk_fma_f32 v[88:89], v[88:89], s[42:43], v[80:81] op_sel_hi:[1,0,1]
	v_pk_fma_f32 v[86:87], v[86:87], s[42:43], v[28:29] op_sel_hi:[1,0,1]
	v_pk_mul_f32 v[84:85], v[84:85], s[96:97] op_sel_hi:[1,0]
	v_pk_mul_f32 v[82:83], v[82:83], s[96:97] op_sel_hi:[1,0]
	v_pk_mul_f32 v[88:89], v[88:89], s[96:97] op_sel_hi:[1,0]
	v_pk_mul_f32 v[86:87], v[86:87], s[96:97] op_sel_hi:[1,0]
	v_exp_f32_e32 v84, v84
	v_exp_f32_e32 v85, v85
	v_exp_f32_e32 v82, v82
	v_exp_f32_e32 v83, v83
	v_exp_f32_e32 v88, v88
	v_exp_f32_e32 v89, v89
	v_exp_f32_e32 v86, v86
	v_exp_f32_e32 v87, v87
	v_pk_add_f32 v[84:85], v[84:85], 1.0 op_sel_hi:[1,0]
	v_pk_add_f32 v[82:83], v[82:83], 1.0 op_sel_hi:[1,0]
	v_pk_add_f32 v[88:89], v[88:89], 1.0 op_sel_hi:[1,0]
	v_pk_add_f32 v[86:87], v[86:87], 1.0 op_sel_hi:[1,0]
	v_rcp_f32_e32 v84, v84
	v_rcp_f32_e32 v85, v85
	v_rcp_f32_e32 v82, v82
	v_rcp_f32_e32 v83, v83
	v_rcp_f32_e32 v88, v88
	v_rcp_f32_e32 v89, v89
	v_rcp_f32_e32 v86, v86
	v_rcp_f32_e32 v87, v87
	v_pk_mul_f32 v[30:31], v[30:31], v[84:85]
	v_pk_mul_f32 v[26:27], v[26:27], v[82:83]
	v_pk_mul_f32 v[80:81], v[80:81], v[88:89]
	v_pk_mul_f32 v[28:29], v[28:29], v[86:87]
.LBB0_561:
	v_cvt_pk_bf16_f32 v27, v26, v27
	s_nop 0
	v_cvt_pk_bf16_f32 v29, v28, v29
	v_cvt_pk_bf16_f32 v30, v30, v31
	v_cvt_pk_bf16_f32 v31, v80, v81
	ds_bpermute_b32 v26, v161, v30
	ds_bpermute_b32 v27, v161, v27
	ds_bpermute_b32 v28, v161, v31
	ds_bpermute_b32 v29, v161, v29
	s_and_b64 vcc, exec, s[6:7]
	s_waitcnt lgkmcnt(0)
	global_store_dwordx4 v[10:11], v[26:29], off offset:256 sc1
	v_pk_fma_f32 v[10:11], v[8:9], v[78:79], v[6:7]
	s_nop 0
	v_pk_fma_f32 v[26:27], v[24:25], v[76:77], v[4:5]
	v_pk_fma_f32 v[8:9], v[8:9], v[74:75], v[2:3]
	v_pk_fma_f32 v[28:29], v[24:25], v[72:73], v[0:1]
	s_cbranch_vccnz .LBB0_563
	v_pk_mul_f32 v[30:31], v[10:11], v[10:11]
	v_pk_mul_f32 v[72:73], v[26:27], v[26:27]
	v_pk_mul_f32 v[74:75], v[8:9], v[8:9]
	v_pk_mul_f32 v[76:77], v[28:29], v[28:29]
	v_pk_mul_f32 v[30:31], v[10:11], v[30:31]
	v_pk_mul_f32 v[72:73], v[26:27], v[72:73]
	v_pk_mul_f32 v[74:75], v[8:9], v[74:75]
	v_pk_mul_f32 v[76:77], v[28:29], v[76:77]
	v_pk_fma_f32 v[72:73], v[72:73], s[42:43], v[26:27] op_sel_hi:[1,0,1]
	v_pk_fma_f32 v[30:31], v[30:31], s[42:43], v[10:11] op_sel_hi:[1,0,1]
	v_pk_fma_f32 v[76:77], v[76:77], s[42:43], v[28:29] op_sel_hi:[1,0,1]
	v_pk_fma_f32 v[74:75], v[74:75], s[42:43], v[8:9] op_sel_hi:[1,0,1]
	v_pk_mul_f32 v[72:73], v[72:73], s[96:97] op_sel_hi:[1,0]
	v_pk_mul_f32 v[30:31], v[30:31], s[96:97] op_sel_hi:[1,0]
	v_pk_mul_f32 v[76:77], v[76:77], s[96:97] op_sel_hi:[1,0]
	v_pk_mul_f32 v[74:75], v[74:75], s[96:97] op_sel_hi:[1,0]
	v_exp_f32_e32 v72, v72
	v_exp_f32_e32 v73, v73
	v_exp_f32_e32 v30, v30
	v_exp_f32_e32 v31, v31
	v_exp_f32_e32 v76, v76
	v_exp_f32_e32 v77, v77
	v_exp_f32_e32 v74, v74
	v_exp_f32_e32 v75, v75
	v_pk_add_f32 v[72:73], v[72:73], 1.0 op_sel_hi:[1,0]
	v_pk_add_f32 v[30:31], v[30:31], 1.0 op_sel_hi:[1,0]
	v_pk_add_f32 v[76:77], v[76:77], 1.0 op_sel_hi:[1,0]
	v_pk_add_f32 v[74:75], v[74:75], 1.0 op_sel_hi:[1,0]
	v_rcp_f32_e32 v72, v72
	v_rcp_f32_e32 v73, v73
	v_rcp_f32_e32 v30, v30
	v_rcp_f32_e32 v31, v31
	v_rcp_f32_e32 v76, v76
	v_rcp_f32_e32 v77, v77
	v_rcp_f32_e32 v74, v74
	v_rcp_f32_e32 v75, v75
	v_pk_mul_f32 v[26:27], v[26:27], v[72:73]
	v_pk_mul_f32 v[10:11], v[10:11], v[30:31]
	v_pk_mul_f32 v[28:29], v[28:29], v[76:77]
	v_pk_mul_f32 v[8:9], v[8:9], v[74:75]
.LBB0_563:
	v_cvt_pk_bf16_f32 v10, v10, v11
	v_cvt_pk_bf16_f32 v11, v28, v29
	v_cvt_pk_bf16_f32 v26, v26, v27
	s_nop 0
	v_cvt_pk_bf16_f32 v27, v8, v9
	ds_bpermute_b32 v8, v161, v26
	ds_bpermute_b32 v9, v161, v10
	ds_bpermute_b32 v10, v161, v11
	ds_bpermute_b32 v11, v161, v27
	v_pk_fma_f32 v[26:27], v[24:25], v[68:69], v[4:5]
	s_and_b64 vcc, exec, s[6:7]
	v_pk_fma_f32 v[28:29], v[24:25], v[64:65], v[0:1]
	s_waitcnt lgkmcnt(0)
	global_store_dwordx4 v[12:13], v[8:11], off offset:256 sc1
	s_nop 1
	v_mov_b32_e32 v8, v24
	v_mov_b32_e32 v9, v24
	v_pk_fma_f32 v[10:11], v[8:9], v[70:71], v[6:7]
	v_pk_fma_f32 v[12:13], v[8:9], v[66:67], v[2:3]
	s_cbranch_vccnz .LBB0_565
	v_pk_mul_f32 v[30:31], v[10:11], v[10:11]
	v_pk_mul_f32 v[64:65], v[26:27], v[26:27]
	v_pk_mul_f32 v[66:67], v[12:13], v[12:13]
	v_pk_mul_f32 v[68:69], v[28:29], v[28:29]
	v_pk_mul_f32 v[30:31], v[10:11], v[30:31]
	v_pk_mul_f32 v[64:65], v[26:27], v[64:65]
	v_pk_mul_f32 v[66:67], v[12:13], v[66:67]
	v_pk_mul_f32 v[68:69], v[28:29], v[68:69]
	v_pk_fma_f32 v[64:65], v[64:65], s[42:43], v[26:27] op_sel_hi:[1,0,1]
	v_pk_fma_f32 v[30:31], v[30:31], s[42:43], v[10:11] op_sel_hi:[1,0,1]
	v_pk_fma_f32 v[68:69], v[68:69], s[42:43], v[28:29] op_sel_hi:[1,0,1]
	v_pk_fma_f32 v[66:67], v[66:67], s[42:43], v[12:13] op_sel_hi:[1,0,1]
	v_pk_mul_f32 v[64:65], v[64:65], s[96:97] op_sel_hi:[1,0]
	v_pk_mul_f32 v[30:31], v[30:31], s[96:97] op_sel_hi:[1,0]
	v_pk_mul_f32 v[68:69], v[68:69], s[96:97] op_sel_hi:[1,0]
	v_pk_mul_f32 v[66:67], v[66:67], s[96:97] op_sel_hi:[1,0]
	v_exp_f32_e32 v64, v64
	v_exp_f32_e32 v65, v65
	v_exp_f32_e32 v30, v30
	v_exp_f32_e32 v31, v31
	v_exp_f32_e32 v68, v68
	v_exp_f32_e32 v69, v69
	v_exp_f32_e32 v66, v66
	v_exp_f32_e32 v67, v67
	v_pk_add_f32 v[64:65], v[64:65], 1.0 op_sel_hi:[1,0]
	v_pk_add_f32 v[30:31], v[30:31], 1.0 op_sel_hi:[1,0]
	v_pk_add_f32 v[68:69], v[68:69], 1.0 op_sel_hi:[1,0]
	v_pk_add_f32 v[66:67], v[66:67], 1.0 op_sel_hi:[1,0]
	v_rcp_f32_e32 v64, v64
	v_rcp_f32_e32 v65, v65
	v_rcp_f32_e32 v30, v30
	v_rcp_f32_e32 v31, v31
	v_rcp_f32_e32 v68, v68
	v_rcp_f32_e32 v69, v69
	v_rcp_f32_e32 v66, v66
	v_rcp_f32_e32 v67, v67
	v_pk_mul_f32 v[26:27], v[26:27], v[64:65]
	v_pk_mul_f32 v[10:11], v[10:11], v[30:31]
	v_pk_mul_f32 v[28:29], v[28:29], v[68:69]
	v_pk_mul_f32 v[12:13], v[12:13], v[66:67]
.LBB0_565:
	v_cvt_pk_bf16_f32 v11, v10, v11
	s_nop 0
	v_cvt_pk_bf16_f32 v13, v12, v13
	v_cvt_pk_bf16_f32 v26, v26, v27
	v_cvt_pk_bf16_f32 v27, v28, v29
	ds_bpermute_b32 v10, v161, v26
	ds_bpermute_b32 v11, v161, v11
	ds_bpermute_b32 v12, v161, v27
	ds_bpermute_b32 v13, v161, v13
	s_and_b64 vcc, exec, s[6:7]
	s_waitcnt lgkmcnt(0)
	global_store_dwordx4 v[14:15], v[10:13], off offset:256 sc1
	s_nop 1
	v_pk_fma_f32 v[10:11], v[8:9], v[62:63], v[6:7]
	v_pk_fma_f32 v[12:13], v[24:25], v[60:61], v[4:5]
	v_pk_fma_f32 v[8:9], v[8:9], v[58:59], v[2:3]
	v_pk_fma_f32 v[14:15], v[24:25], v[56:57], v[0:1]
	s_cbranch_vccnz .LBB0_567
	v_pk_mul_f32 v[26:27], v[10:11], v[10:11]
	v_pk_mul_f32 v[28:29], v[12:13], v[12:13]
	v_pk_mul_f32 v[30:31], v[8:9], v[8:9]
	v_pk_mul_f32 v[56:57], v[14:15], v[14:15]
	v_pk_mul_f32 v[26:27], v[10:11], v[26:27]
	v_pk_mul_f32 v[28:29], v[12:13], v[28:29]
	v_pk_mul_f32 v[30:31], v[8:9], v[30:31]
	v_pk_mul_f32 v[56:57], v[14:15], v[56:57]
	v_pk_fma_f32 v[28:29], v[28:29], s[42:43], v[12:13] op_sel_hi:[1,0,1]
	v_pk_fma_f32 v[26:27], v[26:27], s[42:43], v[10:11] op_sel_hi:[1,0,1]
	v_pk_fma_f32 v[56:57], v[56:57], s[42:43], v[14:15] op_sel_hi:[1,0,1]
	v_pk_fma_f32 v[30:31], v[30:31], s[42:43], v[8:9] op_sel_hi:[1,0,1]
	v_pk_mul_f32 v[28:29], v[28:29], s[96:97] op_sel_hi:[1,0]
	v_pk_mul_f32 v[26:27], v[26:27], s[96:97] op_sel_hi:[1,0]
	v_pk_mul_f32 v[56:57], v[56:57], s[96:97] op_sel_hi:[1,0]
	v_pk_mul_f32 v[30:31], v[30:31], s[96:97] op_sel_hi:[1,0]
	v_exp_f32_e32 v28, v28
	v_exp_f32_e32 v29, v29
	v_exp_f32_e32 v26, v26
	v_exp_f32_e32 v27, v27
	v_exp_f32_e32 v56, v56
	v_exp_f32_e32 v57, v57
	v_exp_f32_e32 v30, v30
	v_exp_f32_e32 v31, v31
	v_pk_add_f32 v[28:29], v[28:29], 1.0 op_sel_hi:[1,0]
	v_pk_add_f32 v[26:27], v[26:27], 1.0 op_sel_hi:[1,0]
	v_pk_add_f32 v[56:57], v[56:57], 1.0 op_sel_hi:[1,0]
	v_pk_add_f32 v[30:31], v[30:31], 1.0 op_sel_hi:[1,0]
	v_rcp_f32_e32 v28, v28
	v_rcp_f32_e32 v29, v29
	v_rcp_f32_e32 v26, v26
	v_rcp_f32_e32 v27, v27
	v_rcp_f32_e32 v56, v56
	v_rcp_f32_e32 v57, v57
	v_rcp_f32_e32 v30, v30
	v_rcp_f32_e32 v31, v31
	v_pk_mul_f32 v[12:13], v[12:13], v[28:29]
	v_pk_mul_f32 v[10:11], v[10:11], v[26:27]
	v_pk_mul_f32 v[14:15], v[14:15], v[56:57]
	v_pk_mul_f32 v[8:9], v[8:9], v[30:31]
.LBB0_567:
	v_cvt_pk_bf16_f32 v10, v10, v11
	v_cvt_pk_bf16_f32 v11, v14, v15
	v_cvt_pk_bf16_f32 v12, v12, v13
	s_nop 0
	v_cvt_pk_bf16_f32 v13, v8, v9
	ds_bpermute_b32 v8, v161, v12
	ds_bpermute_b32 v9, v161, v10
	ds_bpermute_b32 v10, v161, v11
	ds_bpermute_b32 v11, v161, v13
	v_pk_fma_f32 v[14:15], v[24:25], v[52:53], v[4:5]
	s_and_b64 vcc, exec, s[6:7]
	s_waitcnt lgkmcnt(0)
	global_store_dwordx4 v[16:17], v[8:11], off offset:256 sc1
	s_nop 1
	v_mov_b32_e32 v8, v24
	v_mov_b32_e32 v9, v24
	v_pk_fma_f32 v[10:11], v[8:9], v[54:55], v[6:7]
	v_pk_fma_f32 v[12:13], v[8:9], v[50:51], v[2:3]
	v_pk_fma_f32 v[16:17], v[24:25], v[48:49], v[0:1]
	s_cbranch_vccnz .LBB0_569
	v_pk_mul_f32 v[26:27], v[10:11], v[10:11]
	v_pk_mul_f32 v[28:29], v[14:15], v[14:15]
	v_pk_mul_f32 v[30:31], v[12:13], v[12:13]
	v_pk_mul_f32 v[48:49], v[16:17], v[16:17]
	v_pk_mul_f32 v[26:27], v[10:11], v[26:27]
	v_pk_mul_f32 v[28:29], v[14:15], v[28:29]
	v_pk_mul_f32 v[30:31], v[12:13], v[30:31]
	v_pk_mul_f32 v[48:49], v[16:17], v[48:49]
	v_pk_fma_f32 v[28:29], v[28:29], s[42:43], v[14:15] op_sel_hi:[1,0,1]
	v_pk_fma_f32 v[26:27], v[26:27], s[42:43], v[10:11] op_sel_hi:[1,0,1]
	v_pk_fma_f32 v[48:49], v[48:49], s[42:43], v[16:17] op_sel_hi:[1,0,1]
	v_pk_fma_f32 v[30:31], v[30:31], s[42:43], v[12:13] op_sel_hi:[1,0,1]
	v_pk_mul_f32 v[28:29], v[28:29], s[96:97] op_sel_hi:[1,0]
	v_pk_mul_f32 v[26:27], v[26:27], s[96:97] op_sel_hi:[1,0]
	v_pk_mul_f32 v[48:49], v[48:49], s[96:97] op_sel_hi:[1,0]
	v_pk_mul_f32 v[30:31], v[30:31], s[96:97] op_sel_hi:[1,0]
	v_exp_f32_e32 v28, v28
	v_exp_f32_e32 v29, v29
	v_exp_f32_e32 v26, v26
	v_exp_f32_e32 v27, v27
	v_exp_f32_e32 v48, v48
	v_exp_f32_e32 v49, v49
	v_exp_f32_e32 v30, v30
	v_exp_f32_e32 v31, v31
	v_pk_add_f32 v[28:29], v[28:29], 1.0 op_sel_hi:[1,0]
	v_pk_add_f32 v[26:27], v[26:27], 1.0 op_sel_hi:[1,0]
	v_pk_add_f32 v[48:49], v[48:49], 1.0 op_sel_hi:[1,0]
	v_pk_add_f32 v[30:31], v[30:31], 1.0 op_sel_hi:[1,0]
	v_rcp_f32_e32 v28, v28
	v_rcp_f32_e32 v29, v29
	v_rcp_f32_e32 v26, v26
	v_rcp_f32_e32 v27, v27
	v_rcp_f32_e32 v48, v48
	v_rcp_f32_e32 v49, v49
	v_rcp_f32_e32 v30, v30
	v_rcp_f32_e32 v31, v31
	v_pk_mul_f32 v[14:15], v[14:15], v[28:29]
	v_pk_mul_f32 v[10:11], v[10:11], v[26:27]
	v_pk_mul_f32 v[16:17], v[16:17], v[48:49]
	v_pk_mul_f32 v[12:13], v[12:13], v[30:31]
.LBB0_569:
	v_cvt_pk_bf16_f32 v11, v10, v11
	s_nop 0
	v_cvt_pk_bf16_f32 v13, v12, v13
	v_cvt_pk_bf16_f32 v14, v14, v15
	v_cvt_pk_bf16_f32 v15, v16, v17
	ds_bpermute_b32 v10, v161, v14
	ds_bpermute_b32 v11, v161, v11
	ds_bpermute_b32 v12, v161, v15
	ds_bpermute_b32 v13, v161, v13
	s_and_b64 vcc, exec, s[6:7]
	v_pk_fma_f32 v[14:15], v[24:25], v[40:41], v[0:1]
	s_waitcnt lgkmcnt(0)
	global_store_dwordx4 v[18:19], v[10:13], off offset:256 sc1
	s_nop 1
	v_pk_fma_f32 v[10:11], v[8:9], v[46:47], v[6:7]
	v_pk_fma_f32 v[12:13], v[24:25], v[44:45], v[4:5]
	v_pk_fma_f32 v[8:9], v[8:9], v[42:43], v[2:3]
	s_cbranch_vccnz .LBB0_571
	v_pk_mul_f32 v[16:17], v[10:11], v[10:11]
	v_pk_mul_f32 v[18:19], v[12:13], v[12:13]
	v_pk_mul_f32 v[26:27], v[8:9], v[8:9]
	v_pk_mul_f32 v[28:29], v[14:15], v[14:15]
	v_pk_mul_f32 v[16:17], v[10:11], v[16:17]
	v_pk_mul_f32 v[18:19], v[12:13], v[18:19]
	v_pk_mul_f32 v[26:27], v[8:9], v[26:27]
	v_pk_mul_f32 v[28:29], v[14:15], v[28:29]
	v_pk_fma_f32 v[18:19], v[18:19], s[42:43], v[12:13] op_sel_hi:[1,0,1]
	v_pk_fma_f32 v[16:17], v[16:17], s[42:43], v[10:11] op_sel_hi:[1,0,1]
	v_pk_fma_f32 v[28:29], v[28:29], s[42:43], v[14:15] op_sel_hi:[1,0,1]
	v_pk_fma_f32 v[26:27], v[26:27], s[42:43], v[8:9] op_sel_hi:[1,0,1]
	v_pk_mul_f32 v[18:19], v[18:19], s[96:97] op_sel_hi:[1,0]
	v_pk_mul_f32 v[16:17], v[16:17], s[96:97] op_sel_hi:[1,0]
	v_pk_mul_f32 v[28:29], v[28:29], s[96:97] op_sel_hi:[1,0]
	v_pk_mul_f32 v[26:27], v[26:27], s[96:97] op_sel_hi:[1,0]
	v_exp_f32_e32 v18, v18
	v_exp_f32_e32 v19, v19
	v_exp_f32_e32 v16, v16
	v_exp_f32_e32 v17, v17
	v_exp_f32_e32 v28, v28
	v_exp_f32_e32 v29, v29
	v_exp_f32_e32 v26, v26
	v_exp_f32_e32 v27, v27
	v_pk_add_f32 v[18:19], v[18:19], 1.0 op_sel_hi:[1,0]
	v_pk_add_f32 v[16:17], v[16:17], 1.0 op_sel_hi:[1,0]
	v_pk_add_f32 v[28:29], v[28:29], 1.0 op_sel_hi:[1,0]
	v_pk_add_f32 v[26:27], v[26:27], 1.0 op_sel_hi:[1,0]
	v_rcp_f32_e32 v18, v18
	v_rcp_f32_e32 v19, v19
	v_rcp_f32_e32 v16, v16
	v_rcp_f32_e32 v17, v17
	v_rcp_f32_e32 v28, v28
	v_rcp_f32_e32 v29, v29
	v_rcp_f32_e32 v26, v26
	v_rcp_f32_e32 v27, v27
	v_pk_mul_f32 v[12:13], v[12:13], v[18:19]
	v_pk_mul_f32 v[10:11], v[10:11], v[16:17]
	v_pk_mul_f32 v[14:15], v[14:15], v[28:29]
	v_pk_mul_f32 v[8:9], v[8:9], v[26:27]
.LBB0_571:
	v_cvt_pk_bf16_f32 v10, v10, v11
	v_cvt_pk_bf16_f32 v11, v14, v15
	v_cvt_pk_bf16_f32 v12, v12, v13
	s_nop 0
	v_cvt_pk_bf16_f32 v13, v8, v9
	ds_bpermute_b32 v8, v161, v12
	ds_bpermute_b32 v9, v161, v10
	ds_bpermute_b32 v10, v161, v11
	ds_bpermute_b32 v11, v161, v13
	v_pk_fma_f32 v[4:5], v[24:25], v[36:37], v[4:5]
	s_and_b64 vcc, exec, s[6:7]
	v_pk_fma_f32 v[0:1], v[24:25], v[32:33], v[0:1]
	s_waitcnt lgkmcnt(0)
	global_store_dwordx4 v[20:21], v[8:11], off offset:256 sc1
	s_nop 1
	v_mov_b32_e32 v8, v24
	v_mov_b32_e32 v9, v24
	v_pk_fma_f32 v[6:7], v[8:9], v[38:39], v[6:7]
	v_pk_fma_f32 v[2:3], v[8:9], v[34:35], v[2:3]
	s_cbranch_vccnz .LBB0_522
	v_pk_mul_f32 v[8:9], v[6:7], v[6:7]
	v_pk_mul_f32 v[10:11], v[4:5], v[4:5]
	v_pk_mul_f32 v[12:13], v[2:3], v[2:3]
	v_pk_mul_f32 v[14:15], v[0:1], v[0:1]
	v_pk_mul_f32 v[8:9], v[6:7], v[8:9]
	v_pk_mul_f32 v[10:11], v[4:5], v[10:11]
	v_pk_mul_f32 v[12:13], v[2:3], v[12:13]
	v_pk_mul_f32 v[14:15], v[0:1], v[14:15]
	v_pk_fma_f32 v[10:11], v[10:11], s[42:43], v[4:5] op_sel_hi:[1,0,1]
	v_pk_fma_f32 v[8:9], v[8:9], s[42:43], v[6:7] op_sel_hi:[1,0,1]
	v_pk_fma_f32 v[14:15], v[14:15], s[42:43], v[0:1] op_sel_hi:[1,0,1]
	v_pk_fma_f32 v[12:13], v[12:13], s[42:43], v[2:3] op_sel_hi:[1,0,1]
	v_pk_mul_f32 v[10:11], v[10:11], s[96:97] op_sel_hi:[1,0]
	v_pk_mul_f32 v[8:9], v[8:9], s[96:97] op_sel_hi:[1,0]
	v_pk_mul_f32 v[14:15], v[14:15], s[96:97] op_sel_hi:[1,0]
	v_pk_mul_f32 v[12:13], v[12:13], s[96:97] op_sel_hi:[1,0]
	v_exp_f32_e32 v10, v10
	v_exp_f32_e32 v11, v11
	v_exp_f32_e32 v8, v8
	v_exp_f32_e32 v9, v9
	v_exp_f32_e32 v14, v14
	v_exp_f32_e32 v15, v15
	v_exp_f32_e32 v12, v12
	v_exp_f32_e32 v13, v13
	v_pk_add_f32 v[10:11], v[10:11], 1.0 op_sel_hi:[1,0]
	v_pk_add_f32 v[8:9], v[8:9], 1.0 op_sel_hi:[1,0]
	v_pk_add_f32 v[14:15], v[14:15], 1.0 op_sel_hi:[1,0]
	v_pk_add_f32 v[12:13], v[12:13], 1.0 op_sel_hi:[1,0]
	v_rcp_f32_e32 v10, v10
	v_rcp_f32_e32 v11, v11
	v_rcp_f32_e32 v8, v8
	v_rcp_f32_e32 v9, v9
	v_rcp_f32_e32 v14, v14
	v_rcp_f32_e32 v15, v15
	v_rcp_f32_e32 v12, v12
	v_rcp_f32_e32 v13, v13
	v_pk_mul_f32 v[4:5], v[4:5], v[10:11]
	v_pk_mul_f32 v[6:7], v[6:7], v[8:9]
	v_pk_mul_f32 v[0:1], v[0:1], v[14:15]
	v_pk_mul_f32 v[2:3], v[2:3], v[12:13]
	s_branch .LBB0_522

.LBB0_579:
	s_waitcnt vmcnt(0)
	v_add_u32_e32 v12, s13, v88
	v_add_u32_e32 v4, 0x45, v12
	v_ashrrev_i32_e32 v13, 31, v12
	v_ashrrev_i32_e32 v5, 31, v4
	v_lshlrev_b64 v[0:1], 13, v[12:13]
	v_lshlrev_b64 v[4:5], 13, v[4:5]
	v_lshl_add_u64 v[0:1], v[64:65], 0, v[0:1]
	v_lshl_add_u64 v[4:5], v[64:65], 0, v[4:5]
	global_load_dwordx4 v[48:51], v[0:1], off nt
	v_add_u32_e32 v8, 0x46, v12
	global_load_dwordx4 v[4:7], v[4:5], off nt
	v_or_b32_e32 v0, 1, v12
	v_ashrrev_i32_e32 v1, 31, v0
	v_ashrrev_i32_e32 v9, 31, v8
	v_lshlrev_b64 v[0:1], 13, v[0:1]
	v_lshlrev_b64 v[8:9], 13, v[8:9]
	v_lshl_add_u64 v[0:1], v[64:65], 0, v[0:1]
	v_lshl_add_u64 v[8:9], v[64:65], 0, v[8:9]
	global_load_dwordx4 v[52:55], v[0:1], off nt
	v_mov_b32_e32 v67, v173
	global_load_dwordx4 v[8:11], v[8:9], off nt
	v_or_b32_e32 v0, 2, v12
	v_ashrrev_i32_e32 v1, 31, v0
	v_lshlrev_b64 v[0:1], 13, v[0:1]
	v_lshl_add_u64 v[0:1], v[64:65], 0, v[0:1]
	global_load_dwordx4 v[56:59], v[0:1], off nt
	v_or_b32_e32 v0, 3, v12
	v_ashrrev_i32_e32 v1, 31, v0
	v_lshlrev_b64 v[0:1], 13, v[0:1]
	v_lshl_add_u64 v[0:1], v[64:65], 0, v[0:1]
	global_load_dwordx4 v[60:63], v[0:1], off nt
	v_or_b32_e32 v0, 4, v12
	v_ashrrev_i32_e32 v1, 31, v0
	v_lshlrev_b64 v[0:1], 13, v[0:1]
	v_lshl_add_u64 v[0:1], v[64:65], 0, v[0:1]
	global_load_dwordx4 v[32:35], v[0:1], off nt
	v_or_b32_e32 v0, 5, v12
	v_ashrrev_i32_e32 v1, 31, v0
	v_lshlrev_b64 v[0:1], 13, v[0:1]
	v_lshl_add_u64 v[0:1], v[64:65], 0, v[0:1]
	global_load_dwordx4 v[36:39], v[0:1], off nt
	v_or_b32_e32 v0, 6, v12
	v_ashrrev_i32_e32 v1, 31, v0
	v_lshlrev_b64 v[0:1], 13, v[0:1]
	v_lshl_add_u64 v[0:1], v[64:65], 0, v[0:1]
	global_load_dwordx4 v[40:43], v[0:1], off nt
	v_or_b32_e32 v0, 7, v12
	v_ashrrev_i32_e32 v1, 31, v0
	v_lshlrev_b64 v[0:1], 13, v[0:1]
	v_lshl_add_u64 v[0:1], v[64:65], 0, v[0:1]
	global_load_dwordx4 v[44:47], v[0:1], off nt
	v_add_u32_e32 v0, 64, v12
	v_ashrrev_i32_e32 v1, 31, v0
	v_lshlrev_b64 v[0:1], 13, v[0:1]
	v_lshl_add_u64 v[0:1], v[64:65], 0, v[0:1]
	global_load_dwordx4 v[16:19], v[0:1], off nt
	v_add_u32_e32 v0, 0x41, v12
	v_ashrrev_i32_e32 v1, 31, v0
	v_lshlrev_b64 v[0:1], 13, v[0:1]
	v_lshl_add_u64 v[0:1], v[64:65], 0, v[0:1]
	global_load_dwordx4 v[20:23], v[0:1], off nt
	v_add_u32_e32 v0, 0x42, v12
	v_ashrrev_i32_e32 v1, 31, v0
	v_lshlrev_b64 v[0:1], 13, v[0:1]
	v_lshl_add_u64 v[0:1], v[64:65], 0, v[0:1]
	global_load_dwordx4 v[24:27], v[0:1], off nt
	v_add_u32_e32 v0, 0x43, v12
	v_ashrrev_i32_e32 v1, 31, v0
	v_lshlrev_b64 v[0:1], 13, v[0:1]
	v_lshl_add_u64 v[0:1], v[64:65], 0, v[0:1]
	global_load_dwordx4 v[28:31], v[0:1], off nt
	v_add_u32_e32 v0, 0x44, v12
	v_ashrrev_i32_e32 v1, 31, v0
	v_lshlrev_b64 v[0:1], 13, v[0:1]
	v_lshl_add_u64 v[0:1], v[64:65], 0, v[0:1]
	global_load_dwordx4 v[0:3], v[0:1], off nt
	v_add_u32_e32 v12, 0x47, v12
	v_ashrrev_i32_e32 v13, 31, v12
	v_lshlrev_b64 v[12:13], 13, v[12:13]
	v_lshl_add_u64 v[12:13], v[64:65], 0, v[12:13]
	global_load_dwordx4 v[12:15], v[12:13], off nt
	v_mov_b32_e32 v66, v173
	s_and_b64 vcc, exec, s[10:11]
	s_mov_b64 s[10:11], 0
	s_waitcnt vmcnt(15)
	v_mul_f32_e32 v48, 0x42000000, v48
	s_waitcnt vmcnt(14)
	v_mul_f32_e32 v4, 0x42000000, v4
	v_mul_f32_e32 v5, 0x42000000, v5
	s_waitcnt vmcnt(13)
	v_mul_f32_e32 v52, 0x42000000, v52
	v_cvt_pk_fp8_f32 v66, v48, v52
	s_waitcnt vmcnt(12)
	v_mul_f32_e32 v8, 0x42000000, v8
	s_waitcnt vmcnt(11)
	v_mul_f32_e32 v48, 0x42000000, v57
	v_mul_f32_e32 v56, 0x42000000, v56
	s_waitcnt vmcnt(10)
	v_mul_f32_e32 v60, 0x42000000, v60
	v_cvt_pk_fp8_f32 v66, v56, v60 op_sel:[0,0,1]
	s_waitcnt vmcnt(9)
	v_mul_f32_e32 v32, 0x42000000, v32
	s_waitcnt vmcnt(8)
	v_mul_f32_e32 v36, 0x42000000, v36
	v_cvt_pk_fp8_f32 v67, v32, v36
	v_mul_f32_e32 v32, 0x42000000, v49
	v_mul_f32_e32 v36, 0x42000000, v53
	v_mul_f32_e32 v49, 0x42000000, v61
	s_waitcnt vmcnt(7)
	v_mul_f32_e32 v40, 0x42000000, v40
	s_waitcnt vmcnt(6)
	v_mul_f32_e32 v44, 0x42000000, v44
	v_cvt_pk_fp8_f32 v67, v40, v44 op_sel:[0,0,1]
	v_mov_b32_e32 v40, v173
	v_cvt_pk_fp8_f32 v40, v32, v36
	v_mul_f32_e32 v32, 0x42000000, v33
	v_mul_f32_e32 v33, 0x42000000, v37
	v_mul_f32_e32 v36, 0x42000000, v41
	v_mov_b32_e32 v41, v173
	v_cvt_pk_fp8_f32 v41, v32, v33
	v_mul_f32_e32 v37, 0x42000000, v45
	v_mul_f32_e32 v32, 0x42000000, v50
	v_mul_f32_e32 v33, 0x42000000, v54
	v_cvt_pk_fp8_f32 v41, v36, v37 op_sel:[0,0,1]
	v_mov_b32_e32 v36, v173
	v_cvt_pk_fp8_f32 v36, v32, v33
	v_mul_f32_e32 v37, 0x42000000, v58
	v_mul_f32_e32 v45, 0x42000000, v62
	v_mul_f32_e32 v32, 0x42000000, v34
	v_cvt_pk_fp8_f32 v36, v37, v45 op_sel:[0,0,1]
	v_mul_f32_e32 v33, 0x42000000, v38
	v_mov_b32_e32 v37, v173
	v_cvt_pk_fp8_f32 v37, v32, v33
	v_mul_f32_e32 v34, 0x42000000, v42
	v_mul_f32_e32 v38, 0x42000000, v46
	v_mul_f32_e32 v33, 0x42000000, v51
	v_cvt_pk_fp8_f32 v37, v34, v38 op_sel:[0,0,1]
	v_mul_f32_e32 v34, 0x42000000, v55
	v_mov_b32_e32 v32, v173
	v_cvt_pk_fp8_f32 v32, v33, v34
	v_mul_f32_e32 v34, 0x42000000, v35
	v_mul_f32_e32 v35, 0x42000000, v39
	v_mov_b32_e32 v33, v173
	v_cvt_pk_fp8_f32 v33, v34, v35
	s_waitcnt vmcnt(1)
	v_mul_f32_e32 v0, 0x42000000, v0
	v_mov_b32_e32 v35, v173
	v_cvt_pk_fp8_f32 v35, v0, v4
	s_waitcnt vmcnt(0)
	v_mul_f32_e32 v12, 0x42000000, v12
	v_mul_f32_e32 v4, 0x42000000, v17
	v_mov_b32_e32 v0, v173
	v_cvt_pk_fp8_f32 v35, v8, v12 op_sel:[0,0,1]
	v_mul_f32_e32 v8, 0x42000000, v21
	v_cvt_pk_fp8_f32 v0, v4, v8
	v_mul_f32_e32 v4, 0x42000000, v1
	v_mov_b32_e32 v1, v173
	v_cvt_pk_fp8_f32 v1, v4, v5
	v_mul_f32_e32 v16, 0x42000000, v16
	v_mul_f32_e32 v20, 0x42000000, v20
	v_mov_b32_e32 v34, v173
	v_cvt_pk_fp8_f32 v34, v16, v20
	v_mul_f32_e32 v12, 0x42000000, v25
	v_mul_f32_e32 v16, 0x42000000, v29
	v_mul_f32_e32 v8, 0x42000000, v9
	v_mul_f32_e32 v9, 0x42000000, v13
	v_cvt_pk_fp8_f32 v40, v48, v49 op_sel:[0,0,1]
	v_cvt_pk_fp8_f32 v0, v12, v16 op_sel:[0,0,1]
	v_cvt_pk_fp8_f32 v1, v8, v9 op_sel:[0,0,1]
	v_add_u32_e32 v44, s13, v76
	v_mul_f32_e32 v4, 0x42000000, v22
	v_mul_f32_e32 v2, 0x42000000, v2
	ds_write2_b64 v44, v[40:41], v[0:1] offset0:34 offset1:42
	v_mul_f32_e32 v1, 0x42000000, v18
	v_mov_b32_e32 v0, v173
	v_cvt_pk_fp8_f32 v0, v1, v4
	v_mul_f32_e32 v4, 0x42000000, v6
	v_mov_b32_e32 v1, v173
	v_cvt_pk_fp8_f32 v1, v2, v4
	v_mul_f32_e32 v5, 0x42000000, v26
	v_mul_f32_e32 v8, 0x42000000, v30
	v_cvt_pk_fp8_f32 v0, v5, v8 op_sel:[0,0,1]
	v_mul_f32_e32 v5, 0x42000000, v10
	v_mul_f32_e32 v6, 0x42000000, v14
	v_cvt_pk_fp8_f32 v1, v5, v6 op_sel:[0,0,1]
	v_mul_f32_e32 v2, 0x42000000, v23
	v_mul_f32_e32 v38, 0x42000000, v59
	v_mul_f32_e32 v42, 0x42000000, v63
	ds_write2_b64 v44, v[36:37], v[0:1] offset0:68 offset1:76
	v_mul_f32_e32 v1, 0x42000000, v19
	v_mov_b32_e32 v0, v173
	v_cvt_pk_fp8_f32 v0, v1, v2
	v_mul_f32_e32 v2, 0x42000000, v3
	v_mul_f32_e32 v3, 0x42000000, v7
	v_mov_b32_e32 v1, v173
	v_cvt_pk_fp8_f32 v1, v2, v3
	v_mul_f32_e32 v4, 0x42000000, v27
	v_mul_f32_e32 v5, 0x42000000, v31
	v_cvt_pk_fp8_f32 v32, v38, v42 op_sel:[0,0,1]
	v_mul_f32_e32 v38, 0x42000000, v43
	v_mul_f32_e32 v39, 0x42000000, v47
	v_mul_f32_e32 v24, 0x42000000, v24
	v_mul_f32_e32 v28, 0x42000000, v28
	v_cvt_pk_fp8_f32 v0, v4, v5 op_sel:[0,0,1]
	v_mul_f32_e32 v4, 0x42000000, v11
	v_mul_f32_e32 v5, 0x42000000, v15
	v_cvt_pk_fp8_f32 v33, v38, v39 op_sel:[0,0,1]
	v_cvt_pk_fp8_f32 v34, v24, v28 op_sel:[0,0,1]
	v_cvt_pk_fp8_f32 v1, v4, v5 op_sel:[0,0,1]
	s_movk_i32 s13, 0x80
	ds_write2_b64 v44, v[66:67], v[34:35] offset1:8
	ds_write2_b64 v44, v[32:33], v[0:1] offset0:102 offset1:110
	s_cbranch_vccnz .LBB0_579
	s_lshl_b64 s[8:9], s[8:9], 21
	s_add_u32 s8, s95, s8
	s_addc_u32 s9, s97, s9
	s_lshl_b32 s2, s2, 8
	s_waitcnt lgkmcnt(0)
	s_barrier
	v_add_u32_e32 v88, v80, v172
	s_ashr_i32 s10, s3, 31
	ds_read_b128 v[0:3], v88
	v_add_u32_e32 v4, s2, v75
	s_add_u32 s8, s8, s3
	v_ashrrev_i32_e32 v5, 31, v4
	s_addc_u32 s9, s9, s10
	v_lshlrev_b64 v[4:5], 10, v[4:5]
	v_lshl_add_u64 v[4:5], s[8:9], 0, v[4:5]
	v_lshl_add_u64 v[4:5], v[4:5], 0, v[172:173]
	v_add_u32_e32 v89, v81, v172
	s_waitcnt lgkmcnt(0)
	global_store_dwordx4 v[4:5], v[0:3], off sc1
	ds_read_b128 v[0:3], v89
	v_add_u32_e32 v4, s2, v74
	v_ashrrev_i32_e32 v5, 31, v4
	v_lshlrev_b64 v[4:5], 10, v[4:5]
	v_lshl_add_u64 v[4:5], s[8:9], 0, v[4:5]
	v_lshl_add_u64 v[4:5], v[4:5], 0, v[172:173]
	v_add_u32_e32 v90, v82, v172
	s_waitcnt lgkmcnt(0)
	global_store_dwordx4 v[4:5], v[0:3], off sc1
	ds_read_b128 v[0:3], v90
	v_add_u32_e32 v4, s2, v73
	v_ashrrev_i32_e32 v5, 31, v4
	v_lshlrev_b64 v[4:5], 10, v[4:5]
	v_lshl_add_u64 v[4:5], s[8:9], 0, v[4:5]
	v_lshl_add_u64 v[4:5], v[4:5], 0, v[172:173]
	v_add_u32_e32 v91, v83, v172
	s_waitcnt lgkmcnt(0)
	global_store_dwordx4 v[4:5], v[0:3], off sc1
	ds_read_b128 v[0:3], v91
	v_add_u32_e32 v4, s2, v72
	v_ashrrev_i32_e32 v5, 31, v4
	v_lshlrev_b64 v[4:5], 10, v[4:5]
	v_lshl_add_u64 v[4:5], s[8:9], 0, v[4:5]
	v_lshl_add_u64 v[4:5], v[4:5], 0, v[172:173]
	v_add_u32_e32 v92, v84, v172
	s_waitcnt lgkmcnt(0)
	global_store_dwordx4 v[4:5], v[0:3], off sc1
	ds_read_b128 v[0:3], v92
	v_add_u32_e32 v4, s2, v71
	v_ashrrev_i32_e32 v5, 31, v4
	v_lshlrev_b64 v[4:5], 10, v[4:5]
	v_lshl_add_u64 v[4:5], s[8:9], 0, v[4:5]
	v_lshl_add_u64 v[4:5], v[4:5], 0, v[172:173]
	v_add_u32_e32 v93, v85, v172
	s_waitcnt lgkmcnt(0)
	global_store_dwordx4 v[4:5], v[0:3], off sc1
	ds_read_b128 v[0:3], v93
	v_add_u32_e32 v4, s2, v70
	v_ashrrev_i32_e32 v5, 31, v4
	v_lshlrev_b64 v[4:5], 10, v[4:5]
	v_lshl_add_u64 v[4:5], s[8:9], 0, v[4:5]
	v_lshl_add_u64 v[4:5], v[4:5], 0, v[172:173]
	v_add_u32_e32 v94, v86, v172
	s_waitcnt lgkmcnt(0)
	global_store_dwordx4 v[4:5], v[0:3], off sc1
	ds_read_b128 v[0:3], v94
	v_add_u32_e32 v4, s2, v69
	v_ashrrev_i32_e32 v5, 31, v4
	v_lshlrev_b64 v[4:5], 10, v[4:5]
	v_lshl_add_u64 v[4:5], s[8:9], 0, v[4:5]
	v_lshl_add_u64 v[4:5], v[4:5], 0, v[172:173]
	v_add_u32_e32 v95, v87, v172
	s_waitcnt lgkmcnt(0)
	global_store_dwordx4 v[4:5], v[0:3], off sc1
	ds_read_b128 v[0:3], v95
	v_add_u32_e32 v4, s2, v68
	v_ashrrev_i32_e32 v5, 31, v4
	v_lshlrev_b64 v[4:5], 10, v[4:5]
	v_lshl_add_u64 v[4:5], s[8:9], 0, v[4:5]
	v_lshl_add_u64 v[4:5], v[4:5], 0, v[172:173]
	s_waitcnt lgkmcnt(0)
	global_store_dwordx4 v[4:5], v[0:3], off sc1
	s_waitcnt lgkmcnt(0)
	s_barrier
	s_movk_i32 s8, 0xff60
	s_mov_b64 s[2:3], 0
	s_and_b64 vcc, exec, s[6:7]
	s_cbranch_vccz .LBB0_578
	v_readlane_b32 s0, v250, 60
	s_add_i32 s2, s0, s1
	s_ashr_i32 s3, s2, 31
	v_readlane_b32 s8, v255, 19
	s_lshl_b64 s[4:5], s[2:3], 20
	s_lshl_b64 s[2:3], s[2:3], 22
	v_readlane_b32 s14, v255, 25
	v_readlane_b32 s0, v250, 61
	v_readlane_b32 s15, v255, 26
	s_add_u32 s2, s14, s2
	v_or_b32_e32 v0, s0, v77
	s_addc_u32 s3, s15, s3
	v_readlane_b32 s0, v250, 63
	v_ashrrev_i32_e32 v1, 31, v0
	v_lshl_add_u64 v[64:65], v[0:1], 2, s[2:3]
	v_add_u32_e32 v77, s0, v78
	s_mov_b32 s1, 0
	s_mov_b64 s[6:7], -1
	v_readlane_b32 s9, v255, 20
	v_readlane_b32 s10, v255, 21
	v_readlane_b32 s11, v255, 22
	v_readlane_b32 s12, v255, 23
	v_readlane_b32 s13, v255, 24
.LBB0_582:
	v_add_u32_e32 v12, s1, v77
	v_add_u32_e32 v4, 0x45, v12
	v_ashrrev_i32_e32 v13, 31, v12
	v_ashrrev_i32_e32 v5, 31, v4
	v_lshlrev_b64 v[0:1], 12, v[12:13]
	v_lshlrev_b64 v[4:5], 12, v[4:5]
	v_lshl_add_u64 v[0:1], v[64:65], 0, v[0:1]
	v_lshl_add_u64 v[4:5], v[64:65], 0, v[4:5]
	global_load_dwordx4 v[48:51], v[0:1], off nt
	v_add_u32_e32 v8, 0x46, v12
	global_load_dwordx4 v[4:7], v[4:5], off nt
	v_or_b32_e32 v0, 1, v12
	v_ashrrev_i32_e32 v1, 31, v0
	v_ashrrev_i32_e32 v9, 31, v8
	v_lshlrev_b64 v[0:1], 12, v[0:1]
	v_lshlrev_b64 v[8:9], 12, v[8:9]
	v_lshl_add_u64 v[0:1], v[64:65], 0, v[0:1]
	v_lshl_add_u64 v[8:9], v[64:65], 0, v[8:9]
	global_load_dwordx4 v[52:55], v[0:1], off nt
	v_mov_b32_e32 v67, v173
	global_load_dwordx4 v[8:11], v[8:9], off nt
	v_or_b32_e32 v0, 2, v12
	v_ashrrev_i32_e32 v1, 31, v0
	v_lshlrev_b64 v[0:1], 12, v[0:1]
	v_lshl_add_u64 v[0:1], v[64:65], 0, v[0:1]
	global_load_dwordx4 v[56:59], v[0:1], off nt
	v_or_b32_e32 v0, 3, v12
	v_ashrrev_i32_e32 v1, 31, v0
	v_lshlrev_b64 v[0:1], 12, v[0:1]
	v_lshl_add_u64 v[0:1], v[64:65], 0, v[0:1]
	global_load_dwordx4 v[60:63], v[0:1], off nt
	v_or_b32_e32 v0, 4, v12
	v_ashrrev_i32_e32 v1, 31, v0
	v_lshlrev_b64 v[0:1], 12, v[0:1]
	v_lshl_add_u64 v[0:1], v[64:65], 0, v[0:1]
	global_load_dwordx4 v[32:35], v[0:1], off nt
	v_or_b32_e32 v0, 5, v12
	v_ashrrev_i32_e32 v1, 31, v0
	v_lshlrev_b64 v[0:1], 12, v[0:1]
	v_lshl_add_u64 v[0:1], v[64:65], 0, v[0:1]
	global_load_dwordx4 v[36:39], v[0:1], off nt
	v_or_b32_e32 v0, 6, v12
	v_ashrrev_i32_e32 v1, 31, v0
	v_lshlrev_b64 v[0:1], 12, v[0:1]
	v_lshl_add_u64 v[0:1], v[64:65], 0, v[0:1]
	global_load_dwordx4 v[40:43], v[0:1], off nt
	v_or_b32_e32 v0, 7, v12
	v_ashrrev_i32_e32 v1, 31, v0
	v_lshlrev_b64 v[0:1], 12, v[0:1]
	v_lshl_add_u64 v[0:1], v[64:65], 0, v[0:1]
	global_load_dwordx4 v[44:47], v[0:1], off nt
	v_add_u32_e32 v0, 64, v12
	v_ashrrev_i32_e32 v1, 31, v0
	v_lshlrev_b64 v[0:1], 12, v[0:1]
	v_lshl_add_u64 v[0:1], v[64:65], 0, v[0:1]
	global_load_dwordx4 v[16:19], v[0:1], off nt
	v_add_u32_e32 v0, 0x41, v12
	v_ashrrev_i32_e32 v1, 31, v0
	v_lshlrev_b64 v[0:1], 12, v[0:1]
	v_lshl_add_u64 v[0:1], v[64:65], 0, v[0:1]
	global_load_dwordx4 v[20:23], v[0:1], off nt
	v_add_u32_e32 v0, 0x42, v12
	v_ashrrev_i32_e32 v1, 31, v0
	v_lshlrev_b64 v[0:1], 12, v[0:1]
	v_lshl_add_u64 v[0:1], v[64:65], 0, v[0:1]
	global_load_dwordx4 v[24:27], v[0:1], off nt
	v_add_u32_e32 v0, 0x43, v12
	v_ashrrev_i32_e32 v1, 31, v0
	v_lshlrev_b64 v[0:1], 12, v[0:1]
	v_lshl_add_u64 v[0:1], v[64:65], 0, v[0:1]
	global_load_dwordx4 v[28:31], v[0:1], off nt
	v_add_u32_e32 v0, 0x44, v12
	v_ashrrev_i32_e32 v1, 31, v0
	v_lshlrev_b64 v[0:1], 12, v[0:1]
	v_lshl_add_u64 v[0:1], v[64:65], 0, v[0:1]
	global_load_dwordx4 v[0:3], v[0:1], off nt
	v_add_u32_e32 v12, 0x47, v12
	v_ashrrev_i32_e32 v13, 31, v12
	v_lshlrev_b64 v[12:13], 12, v[12:13]
	v_lshl_add_u64 v[12:13], v[64:65], 0, v[12:13]
	global_load_dwordx4 v[12:15], v[12:13], off nt
	v_mov_b32_e32 v66, v173
	s_and_b64 vcc, exec, s[6:7]
	s_mov_b64 s[6:7], 0
	s_waitcnt vmcnt(15)
	v_mul_f32_e32 v48, 0x42000000, v48
	s_waitcnt vmcnt(14)
	v_mul_f32_e32 v4, 0x42000000, v4
	v_mul_f32_e32 v5, 0x42000000, v5
	s_waitcnt vmcnt(13)
	v_mul_f32_e32 v52, 0x42000000, v52
	v_cvt_pk_fp8_f32 v66, v48, v52
	s_waitcnt vmcnt(12)
	v_mul_f32_e32 v8, 0x42000000, v8
	s_waitcnt vmcnt(11)
	v_mul_f32_e32 v48, 0x42000000, v57
	v_mul_f32_e32 v56, 0x42000000, v56
	s_waitcnt vmcnt(10)
	v_mul_f32_e32 v60, 0x42000000, v60
	v_cvt_pk_fp8_f32 v66, v56, v60 op_sel:[0,0,1]
	s_waitcnt vmcnt(9)
	v_mul_f32_e32 v32, 0x42000000, v32
	s_waitcnt vmcnt(8)
	v_mul_f32_e32 v36, 0x42000000, v36
	v_cvt_pk_fp8_f32 v67, v32, v36
	v_mul_f32_e32 v32, 0x42000000, v49
	v_mul_f32_e32 v36, 0x42000000, v53
	v_mul_f32_e32 v49, 0x42000000, v61
	s_waitcnt vmcnt(7)
	v_mul_f32_e32 v40, 0x42000000, v40
	s_waitcnt vmcnt(6)
	v_mul_f32_e32 v44, 0x42000000, v44
	v_cvt_pk_fp8_f32 v67, v40, v44 op_sel:[0,0,1]
	v_mov_b32_e32 v40, v173
	v_cvt_pk_fp8_f32 v40, v32, v36
	v_mul_f32_e32 v32, 0x42000000, v33
	v_mul_f32_e32 v33, 0x42000000, v37
	v_mul_f32_e32 v36, 0x42000000, v41
	v_mov_b32_e32 v41, v173
	v_cvt_pk_fp8_f32 v41, v32, v33
	v_mul_f32_e32 v37, 0x42000000, v45
	v_mul_f32_e32 v32, 0x42000000, v50
	v_mul_f32_e32 v33, 0x42000000, v54
	v_cvt_pk_fp8_f32 v41, v36, v37 op_sel:[0,0,1]
	v_mov_b32_e32 v36, v173
	v_cvt_pk_fp8_f32 v36, v32, v33
	v_mul_f32_e32 v37, 0x42000000, v58
	v_mul_f32_e32 v45, 0x42000000, v62
	v_mul_f32_e32 v32, 0x42000000, v34
	v_cvt_pk_fp8_f32 v36, v37, v45 op_sel:[0,0,1]
	v_mul_f32_e32 v33, 0x42000000, v38
	v_mov_b32_e32 v37, v173
	v_cvt_pk_fp8_f32 v37, v32, v33
	v_mul_f32_e32 v34, 0x42000000, v42
	v_mul_f32_e32 v38, 0x42000000, v46
	v_mul_f32_e32 v33, 0x42000000, v51
	v_cvt_pk_fp8_f32 v37, v34, v38 op_sel:[0,0,1]
	v_mul_f32_e32 v34, 0x42000000, v55
	v_mov_b32_e32 v32, v173
	v_cvt_pk_fp8_f32 v32, v33, v34
	v_mul_f32_e32 v34, 0x42000000, v35
	v_mul_f32_e32 v35, 0x42000000, v39
	v_mov_b32_e32 v33, v173
	v_cvt_pk_fp8_f32 v33, v34, v35
	s_waitcnt vmcnt(1)
	v_mul_f32_e32 v0, 0x42000000, v0
	v_mov_b32_e32 v35, v173
	v_cvt_pk_fp8_f32 v35, v0, v4
	s_waitcnt vmcnt(0)
	v_mul_f32_e32 v12, 0x42000000, v12
	v_mul_f32_e32 v4, 0x42000000, v17
	v_mov_b32_e32 v0, v173
	v_cvt_pk_fp8_f32 v35, v8, v12 op_sel:[0,0,1]
	v_mul_f32_e32 v8, 0x42000000, v21
	v_cvt_pk_fp8_f32 v0, v4, v8
	v_mul_f32_e32 v4, 0x42000000, v1
	v_mov_b32_e32 v1, v173
	v_cvt_pk_fp8_f32 v1, v4, v5
	v_mul_f32_e32 v16, 0x42000000, v16
	v_mul_f32_e32 v20, 0x42000000, v20
	v_mov_b32_e32 v34, v173
	v_cvt_pk_fp8_f32 v34, v16, v20
	v_mul_f32_e32 v12, 0x42000000, v25
	v_mul_f32_e32 v16, 0x42000000, v29
	v_mul_f32_e32 v8, 0x42000000, v9
	v_mul_f32_e32 v9, 0x42000000, v13
	v_cvt_pk_fp8_f32 v40, v48, v49 op_sel:[0,0,1]
	v_cvt_pk_fp8_f32 v0, v12, v16 op_sel:[0,0,1]
	v_cvt_pk_fp8_f32 v1, v8, v9 op_sel:[0,0,1]
	v_add_u32_e32 v44, s1, v76
	v_mul_f32_e32 v4, 0x42000000, v22
	v_mul_f32_e32 v2, 0x42000000, v2
	ds_write2_b64 v44, v[40:41], v[0:1] offset0:34 offset1:42
	v_mul_f32_e32 v1, 0x42000000, v18
	v_mov_b32_e32 v0, v173
	v_cvt_pk_fp8_f32 v0, v1, v4
	v_mul_f32_e32 v4, 0x42000000, v6
	v_mov_b32_e32 v1, v173
	v_cvt_pk_fp8_f32 v1, v2, v4
	v_mul_f32_e32 v5, 0x42000000, v26
	v_mul_f32_e32 v8, 0x42000000, v30
	v_cvt_pk_fp8_f32 v0, v5, v8 op_sel:[0,0,1]
	v_mul_f32_e32 v5, 0x42000000, v10
	v_mul_f32_e32 v6, 0x42000000, v14
	v_cvt_pk_fp8_f32 v1, v5, v6 op_sel:[0,0,1]
	v_mul_f32_e32 v2, 0x42000000, v23
	v_mul_f32_e32 v38, 0x42000000, v59
	v_mul_f32_e32 v42, 0x42000000, v63
	ds_write2_b64 v44, v[36:37], v[0:1] offset0:68 offset1:76
	v_mul_f32_e32 v1, 0x42000000, v19
	v_mov_b32_e32 v0, v173
	v_cvt_pk_fp8_f32 v0, v1, v2
	v_mul_f32_e32 v2, 0x42000000, v3
	v_mul_f32_e32 v3, 0x42000000, v7
	v_mov_b32_e32 v1, v173
	v_cvt_pk_fp8_f32 v1, v2, v3
	v_mul_f32_e32 v4, 0x42000000, v27
	v_mul_f32_e32 v5, 0x42000000, v31
	v_cvt_pk_fp8_f32 v32, v38, v42 op_sel:[0,0,1]
	v_mul_f32_e32 v38, 0x42000000, v43
	v_mul_f32_e32 v39, 0x42000000, v47
	v_mul_f32_e32 v24, 0x42000000, v24
	v_mul_f32_e32 v28, 0x42000000, v28
	v_cvt_pk_fp8_f32 v0, v4, v5 op_sel:[0,0,1]
	v_mul_f32_e32 v4, 0x42000000, v11
	v_mul_f32_e32 v5, 0x42000000, v15
	v_cvt_pk_fp8_f32 v33, v38, v39 op_sel:[0,0,1]
	v_cvt_pk_fp8_f32 v34, v24, v28 op_sel:[0,0,1]
	v_cvt_pk_fp8_f32 v1, v4, v5 op_sel:[0,0,1]
	s_movk_i32 s1, 0x80
	ds_write2_b64 v44, v[66:67], v[34:35] offset1:8
	ds_write2_b64 v44, v[32:33], v[0:1] offset0:102 offset1:110
	s_cbranch_vccnz .LBB0_582
	v_readlane_b32 s0, v251, 0
	s_add_u32 s2, s0, s4
	v_readlane_b32 s0, v251, 2
	s_waitcnt lgkmcnt(0)
	s_barrier
	s_addc_u32 s3, s0, s5
	v_readlane_b32 s0, v250, 61
	ds_read_b128 v[0:3], v88
	s_nop 0
	v_add_u32_e32 v4, s0, v75
	v_ashrrev_i32_e32 v5, 31, v4
	v_lshlrev_b64 v[4:5], 10, v[4:5]
	v_lshl_add_u64 v[4:5], s[2:3], 0, v[4:5]
	v_lshl_add_u64 v[4:5], v[4:5], 0, v[172:173]
	s_waitcnt lgkmcnt(0)
	global_store_dwordx4 v[4:5], v[0:3], off sc1
	ds_read_b128 v[0:3], v89
	v_add_u32_e32 v4, s0, v74
	v_ashrrev_i32_e32 v5, 31, v4
	v_lshlrev_b64 v[4:5], 10, v[4:5]
	v_lshl_add_u64 v[4:5], s[2:3], 0, v[4:5]
	v_lshl_add_u64 v[4:5], v[4:5], 0, v[172:173]
	s_waitcnt lgkmcnt(0)
	global_store_dwordx4 v[4:5], v[0:3], off sc1
	ds_read_b128 v[0:3], v90
	v_add_u32_e32 v4, s0, v73
	v_ashrrev_i32_e32 v5, 31, v4
	v_lshlrev_b64 v[4:5], 10, v[4:5]
	v_lshl_add_u64 v[4:5], s[2:3], 0, v[4:5]
	v_lshl_add_u64 v[4:5], v[4:5], 0, v[172:173]
	s_waitcnt lgkmcnt(0)
	global_store_dwordx4 v[4:5], v[0:3], off sc1
	ds_read_b128 v[0:3], v91
	v_add_u32_e32 v4, s0, v72
	v_ashrrev_i32_e32 v5, 31, v4
	v_lshlrev_b64 v[4:5], 10, v[4:5]
	v_lshl_add_u64 v[4:5], s[2:3], 0, v[4:5]
	v_lshl_add_u64 v[4:5], v[4:5], 0, v[172:173]
	s_waitcnt lgkmcnt(0)
	global_store_dwordx4 v[4:5], v[0:3], off sc1
	ds_read_b128 v[0:3], v92
	v_add_u32_e32 v4, s0, v71
	v_ashrrev_i32_e32 v5, 31, v4
	v_lshlrev_b64 v[4:5], 10, v[4:5]
	v_lshl_add_u64 v[4:5], s[2:3], 0, v[4:5]
	v_lshl_add_u64 v[4:5], v[4:5], 0, v[172:173]
	s_waitcnt lgkmcnt(0)
	global_store_dwordx4 v[4:5], v[0:3], off sc1
	ds_read_b128 v[0:3], v93
	v_add_u32_e32 v4, s0, v70
	v_ashrrev_i32_e32 v5, 31, v4
	v_lshlrev_b64 v[4:5], 10, v[4:5]
	v_lshl_add_u64 v[4:5], s[2:3], 0, v[4:5]
	v_lshl_add_u64 v[4:5], v[4:5], 0, v[172:173]
	s_waitcnt lgkmcnt(0)
	global_store_dwordx4 v[4:5], v[0:3], off sc1
	ds_read_b128 v[0:3], v94
	v_add_u32_e32 v4, s0, v69
	v_ashrrev_i32_e32 v5, 31, v4
	v_lshlrev_b64 v[4:5], 10, v[4:5]
	v_lshl_add_u64 v[4:5], s[2:3], 0, v[4:5]
	v_lshl_add_u64 v[4:5], v[4:5], 0, v[172:173]
	s_waitcnt lgkmcnt(0)
	global_store_dwordx4 v[4:5], v[0:3], off sc1
	ds_read_b128 v[0:3], v95
	v_add_u32_e32 v4, s0, v68
	v_ashrrev_i32_e32 v5, 31, v4
	v_lshlrev_b64 v[4:5], 10, v[4:5]
	v_lshl_add_u64 v[4:5], s[2:3], 0, v[4:5]
	v_lshl_add_u64 v[4:5], v[4:5], 0, v[172:173]
	s_waitcnt lgkmcnt(0)
	global_store_dwordx4 v[4:5], v[0:3], off sc1
	s_waitcnt lgkmcnt(0)
	s_barrier

.LBB0_737:
	s_or_b64 exec, exec, s[4:5]
	v_pk_add_f32 v[64:65], v[36:37], v[80:81]
	s_mov_b32 s4, 0xbfb8aa3b
	v_pk_mul_f32 v[64:65], v[64:65], s[4:5] op_sel_hi:[1,0]
	s_mov_b32 s56, 0xc1000000
	v_exp_f32_e32 v64, v64
	v_exp_f32_e32 v65, v65
	s_mov_b32 s50, 0x3fb8aa3b
	s_mov_b32 s70, 0x3e2aaaab
	v_pk_add_f32 v[66:67], v[38:39], v[82:83]
	v_pk_add_f32 v[64:65], v[64:65], 1.0 op_sel_hi:[1,0]
	s_mov_b32 s0, 0xbca3d70a
	v_rcp_f32_e32 v64, v64
	v_rcp_f32_e32 v65, v65
	s_mov_b32 s2, 0xf800000
	v_pk_mul_f32 v[66:67], v[66:67], s[4:5] op_sel_hi:[1,0]
	v_pk_add_f32 v[76:77], v[40:41], v[76:77]
	v_pk_mul_f32 v[64:65], v[64:65], v[134:135]
	v_exp_f32_e32 v66, v66
	v_pk_mul_f32 v[64:65], v[64:65], s[56:57] op_sel_hi:[1,0]
	v_exp_f32_e32 v67, v67
	v_pk_add_f32 v[80:81], v[64:65], v[64:65]
	v_pk_mul_f32 v[64:65], v[64:65], s[50:51] op_sel_hi:[1,0]
	v_pk_fma_f32 v[82:83], v[80:81], s[70:71], 0.5 op_sel_hi:[1,0,0]
	v_exp_f32_e32 v64, v64
	v_exp_f32_e32 v65, v65
	v_pk_fma_f32 v[82:83], v[80:81], v[82:83], 1.0 op_sel_hi:[1,1,0]
	v_cmp_lt_f32_e64 s[16:17], s0, v80
	v_pk_mul_f32 v[82:83], v[82:83], v[80:81] neg_lo:[0,1] neg_hi:[0,1]
	v_pk_fma_f32 v[166:167], v[64:65], v[64:65], 1.0 op_sel_hi:[1,1,0] neg_lo:[1,0,0] neg_hi:[1,0,0]
	v_pk_mul_f32 v[76:77], v[76:77], s[4:5] op_sel_hi:[1,0]
	v_cndmask_b32_e64 v80, v166, v82, s[16:17]
	v_cmp_lt_f32_e64 s[16:17], s0, v81
	v_mul_f32_e32 v82, 0x4f800000, v80
	v_exp_f32_e32 v76, v76
	v_cndmask_b32_e64 v81, v167, v83, s[16:17]
	v_cmp_gt_f32_e64 s[16:17], s2, v80
	v_exp_f32_e32 v77, v77
	v_pk_add_f32 v[66:67], v[66:67], 1.0 op_sel_hi:[1,0]
	v_cndmask_b32_e64 v80, v80, v82, s[16:17]
	v_sqrt_f32_e32 v82, v80
	v_rcp_f32_e32 v66, v66
	v_rcp_f32_e32 v67, v67
	ds_read_b128 v[52:55], v158 offset:17408
	v_add_u32_e32 v83, -1, v82
	v_fma_f32 v165, -v83, v82, v80
	v_cmp_ge_f32_e64 s[18:19], 0, v165
	v_add_u32_e32 v165, 1, v82
	v_pk_add_f32 v[76:77], v[76:77], 1.0 op_sel_hi:[1,0]
	v_cndmask_b32_e64 v83, v82, v83, s[18:19]
	v_fma_f32 v82, -v165, v82, v80
	v_cmp_lt_f32_e64 s[18:19], 0, v82
	v_rcp_f32_e32 v76, v76
	v_rcp_f32_e32 v77, v77
	v_cndmask_b32_e64 v82, v83, v165, s[18:19]
	v_mul_f32_e32 v83, 0x37800000, v82
	v_cndmask_b32_e64 v82, v82, v83, s[16:17]
	v_cmp_class_f32_e64 s[16:17], v80, v203
	v_pk_mul_f32 v[66:67], v[66:67], v[136:137]
	v_pk_add_f32 v[78:79], v[42:43], v[78:79]
	v_cndmask_b32_e64 v80, v82, v80, s[16:17]
	v_cmp_gt_f32_e64 s[16:17], s2, v81
	v_mul_f32_e32 v82, 0x4f800000, v81
	v_pk_mul_f32 v[66:67], v[66:67], s[56:57] op_sel_hi:[1,0]
	v_cndmask_b32_e64 v81, v81, v82, s[16:17]
	v_sqrt_f32_e32 v82, v81
	s_waitcnt lgkmcnt(0)
	v_pk_mul_f32 v[52:53], v[76:77], v[52:53]
	v_pk_mul_f32 v[76:77], v[78:79], s[4:5] op_sel_hi:[1,0]
	v_pk_add_f32 v[78:79], v[66:67], v[66:67]
	v_add_u32_e32 v83, -1, v82
	v_fma_f32 v165, -v83, v82, v81
	v_cmp_ge_f32_e64 s[18:19], 0, v165
	v_add_u32_e32 v165, 1, v82
	v_pk_mul_f32 v[66:67], v[66:67], s[50:51] op_sel_hi:[1,0]
	v_cndmask_b32_e64 v83, v82, v83, s[18:19]
	v_fma_f32 v82, -v165, v82, v81
	v_cmp_lt_f32_e64 s[18:19], 0, v82
	v_exp_f32_e32 v66, v66
	v_exp_f32_e32 v67, v67
	v_cndmask_b32_e64 v82, v83, v165, s[18:19]
	v_mul_f32_e32 v83, 0x37800000, v82
	v_cndmask_b32_e64 v82, v82, v83, s[16:17]
	v_cmp_class_f32_e64 s[16:17], v81, v203
	v_pk_fma_f32 v[166:167], v[66:67], v[66:67], 1.0 op_sel_hi:[1,1,0] neg_lo:[1,0,0] neg_hi:[1,0,0]
	v_exp_f32_e32 v76, v76
	v_cndmask_b32_e64 v81, v82, v81, s[16:17]
	v_pk_fma_f32 v[82:83], v[78:79], s[70:71], 0.5 op_sel_hi:[1,0,0]
	v_cmp_lt_f32_e64 s[16:17], s0, v78
	v_pk_fma_f32 v[82:83], v[78:79], v[82:83], 1.0 op_sel_hi:[1,1,0]
	v_exp_f32_e32 v77, v77
	v_pk_mul_f32 v[82:83], v[82:83], v[78:79] neg_lo:[0,1] neg_hi:[0,1]
	v_pk_mul_f32 v[52:53], v[80:81], v[52:53]
	v_cndmask_b32_e64 v78, v166, v82, s[16:17]
	v_cmp_lt_f32_e64 s[16:17], s0, v79
	v_mul_f32_e32 v82, 0x4f800000, v78
	v_pk_add_f32 v[76:77], v[76:77], 1.0 op_sel_hi:[1,0]
	v_cndmask_b32_e64 v79, v167, v83, s[16:17]
	v_cmp_gt_f32_e64 s[16:17], s2, v78
	v_rcp_f32_e32 v76, v76
	v_rcp_f32_e32 v77, v77
	v_cndmask_b32_e64 v78, v78, v82, s[16:17]
	v_sqrt_f32_e32 v82, v78
	v_pk_add_f32 v[68:69], v[40:41], v[68:69]
	v_pk_mul_f32 v[54:55], v[76:77], v[54:55]
	v_pk_mul_f32 v[68:69], v[68:69], s[4:5] op_sel_hi:[1,0]
	v_add_u32_e32 v83, -1, v82
	v_fma_f32 v165, -v83, v82, v78
	v_cmp_ge_f32_e64 s[18:19], 0, v165
	v_add_u32_e32 v165, 1, v82
	v_exp_f32_e32 v68, v68
	v_cndmask_b32_e64 v83, v82, v83, s[18:19]
	v_fma_f32 v82, -v165, v82, v78
	v_cmp_lt_f32_e64 s[18:19], 0, v82
	v_exp_f32_e32 v69, v69
	v_pk_add_f32 v[70:71], v[42:43], v[70:71]
	v_cndmask_b32_e64 v82, v83, v165, s[18:19]
	v_mul_f32_e32 v83, 0x37800000, v82
	v_cndmask_b32_e64 v82, v82, v83, s[16:17]
	v_cmp_class_f32_e64 s[16:17], v78, v203
	v_pk_add_f32 v[68:69], v[68:69], 1.0 op_sel_hi:[1,0]
	v_pk_add_f32 v[60:61], v[36:37], v[60:61]
	v_cndmask_b32_e64 v78, v82, v78, s[16:17]
	v_cmp_gt_f32_e64 s[16:17], s2, v79
	v_mul_f32_e32 v82, 0x4f800000, v79
	v_rcp_f32_e32 v68, v68
	v_cndmask_b32_e64 v79, v79, v82, s[16:17]
	v_sqrt_f32_e32 v82, v79
	v_rcp_f32_e32 v69, v69
	v_pk_mul_f32 v[60:61], v[60:61], s[4:5] op_sel_hi:[1,0]
	v_pk_add_f32 v[56:57], v[40:41], v[56:57]
	v_add_u32_e32 v83, -1, v82
	v_fma_f32 v165, -v83, v82, v79
	v_cmp_ge_f32_e64 s[18:19], 0, v165
	v_add_u32_e32 v165, 1, v82
	v_exp_f32_e32 v60, v60
	v_cndmask_b32_e64 v83, v82, v83, s[18:19]
	v_fma_f32 v82, -v165, v82, v79
	v_cmp_lt_f32_e64 s[18:19], 0, v82
	v_exp_f32_e32 v61, v61
	v_pk_mul_f32 v[56:57], v[56:57], s[4:5] op_sel_hi:[1,0]
	v_cndmask_b32_e64 v82, v83, v165, s[18:19]
	v_mul_f32_e32 v83, 0x37800000, v82
	v_cndmask_b32_e64 v82, v82, v83, s[16:17]
	v_cmp_class_f32_e64 s[16:17], v79, v203
	v_exp_f32_e32 v56, v56
	v_exp_f32_e32 v57, v57
	v_cndmask_b32_e64 v79, v82, v79, s[16:17]
	v_pk_mul_f32 v[54:55], v[54:55], v[78:79]
	ds_write_b128 v143, v[64:67] offset:44032
	ds_write_b128 v143, v[52:55] offset:61440
	v_pk_add_f32 v[64:65], v[36:37], v[72:73]
	v_pk_add_f32 v[66:67], v[38:39], v[74:75]
	v_pk_mul_f32 v[64:65], v[64:65], s[4:5] op_sel_hi:[1,0]
	v_pk_mul_f32 v[66:67], v[66:67], s[4:5] op_sel_hi:[1,0]
	v_exp_f32_e32 v64, v64
	v_exp_f32_e32 v65, v65
	v_exp_f32_e32 v66, v66
	v_exp_f32_e32 v67, v67
	ds_read_b128 v[52:55], v158 offset:21760
	v_pk_add_f32 v[64:65], v[64:65], 1.0 op_sel_hi:[1,0]
	v_pk_add_f32 v[60:61], v[60:61], 1.0 op_sel_hi:[1,0]
	v_rcp_f32_e32 v64, v64
	v_rcp_f32_e32 v65, v65
	v_pk_add_f32 v[66:67], v[66:67], 1.0 op_sel_hi:[1,0]
	s_waitcnt lgkmcnt(0)
	v_pk_mul_f32 v[52:53], v[68:69], v[52:53]
	v_rcp_f32_e32 v66, v66
	v_pk_mul_f32 v[64:65], v[64:65], v[134:135]
	v_rcp_f32_e32 v67, v67
	v_pk_mul_f32 v[64:65], v[64:65], s[56:57] op_sel_hi:[1,0]
	v_pk_mul_f32 v[68:69], v[70:71], s[4:5] op_sel_hi:[1,0]
	v_pk_add_f32 v[72:73], v[64:65], v[64:65]
	v_pk_mul_f32 v[64:65], v[64:65], s[50:51] op_sel_hi:[1,0]
	v_pk_fma_f32 v[74:75], v[72:73], s[70:71], 0.5 op_sel_hi:[1,0,0]
	v_exp_f32_e32 v64, v64
	v_exp_f32_e32 v65, v65
	v_pk_fma_f32 v[74:75], v[72:73], v[74:75], 1.0 op_sel_hi:[1,1,0]
	v_cmp_lt_f32_e64 s[16:17], s0, v72
	v_pk_mul_f32 v[74:75], v[74:75], v[72:73] neg_lo:[0,1] neg_hi:[0,1]
	v_pk_fma_f32 v[76:77], v[64:65], v[64:65], 1.0 op_sel_hi:[1,1,0] neg_lo:[1,0,0] neg_hi:[1,0,0]
	v_pk_mul_f32 v[66:67], v[66:67], v[136:137]
	v_cndmask_b32_e64 v72, v76, v74, s[16:17]
	v_cmp_lt_f32_e64 s[16:17], s0, v73
	v_mul_f32_e32 v74, 0x4f800000, v72
	v_pk_mul_f32 v[66:67], v[66:67], s[56:57] op_sel_hi:[1,0]
	v_cndmask_b32_e64 v73, v77, v75, s[16:17]
	v_cmp_gt_f32_e64 s[16:17], s2, v72
	v_pk_add_f32 v[70:71], v[66:67], v[66:67]
	v_pk_mul_f32 v[66:67], v[66:67], s[50:51] op_sel_hi:[1,0]
	v_cndmask_b32_e64 v72, v72, v74, s[16:17]
	v_sqrt_f32_e32 v74, v72
	v_exp_f32_e32 v66, v66
	v_exp_f32_e32 v67, v67
	v_exp_f32_e32 v68, v68
	v_add_u32_e32 v75, -1, v74
	v_fma_f32 v76, -v75, v74, v72
	v_cmp_ge_f32_e64 s[18:19], 0, v76
	v_add_u32_e32 v76, 1, v74
	v_exp_f32_e32 v69, v69
	v_cndmask_b32_e64 v75, v74, v75, s[18:19]
	v_fma_f32 v74, -v76, v74, v72
	v_cmp_lt_f32_e64 s[18:19], 0, v74
	v_pk_add_f32 v[68:69], v[68:69], 1.0 op_sel_hi:[1,0]
	v_rcp_f32_e32 v60, v60
	v_cndmask_b32_e64 v74, v75, v76, s[18:19]
	v_mul_f32_e32 v75, 0x37800000, v74
	v_cndmask_b32_e64 v74, v74, v75, s[16:17]
	v_cmp_class_f32_e64 s[16:17], v72, v203
	v_rcp_f32_e32 v68, v68
	v_rcp_f32_e32 v69, v69
	v_cndmask_b32_e64 v72, v74, v72, s[16:17]
	v_cmp_gt_f32_e64 s[16:17], s2, v73
	v_mul_f32_e32 v74, 0x4f800000, v73
	v_rcp_f32_e32 v61, v61
	v_cndmask_b32_e64 v73, v73, v74, s[16:17]
	v_sqrt_f32_e32 v74, v73
	v_pk_mul_f32 v[54:55], v[68:69], v[54:55]
	v_pk_add_f32 v[56:57], v[56:57], 1.0 op_sel_hi:[1,0]
	v_pk_add_f32 v[62:63], v[38:39], v[62:63]
	v_add_u32_e32 v75, -1, v74
	v_fma_f32 v76, -v75, v74, v73
	v_cmp_ge_f32_e64 s[18:19], 0, v76
	v_add_u32_e32 v76, 1, v74
	v_pk_mul_f32 v[62:63], v[62:63], s[4:5] op_sel_hi:[1,0]
	v_cndmask_b32_e64 v75, v74, v75, s[18:19]
	v_fma_f32 v74, -v76, v74, v73
	v_cmp_lt_f32_e64 s[18:19], 0, v74
	v_exp_f32_e32 v62, v62
	v_exp_f32_e32 v63, v63
	v_cndmask_b32_e64 v74, v75, v76, s[18:19]
	v_mul_f32_e32 v75, 0x37800000, v74
	v_cndmask_b32_e64 v74, v74, v75, s[16:17]
	v_cmp_class_f32_e64 s[16:17], v73, v203
	v_pk_fma_f32 v[76:77], v[66:67], v[66:67], 1.0 op_sel_hi:[1,1,0] neg_lo:[1,0,0] neg_hi:[1,0,0]
	v_pk_add_f32 v[58:59], v[42:43], v[58:59]
	v_cndmask_b32_e64 v73, v74, v73, s[16:17]
	v_pk_fma_f32 v[74:75], v[70:71], s[70:71], 0.5 op_sel_hi:[1,0,0]
	v_cmp_lt_f32_e64 s[16:17], s0, v70
	v_pk_fma_f32 v[74:75], v[70:71], v[74:75], 1.0 op_sel_hi:[1,1,0]
	v_pk_mul_f32 v[52:53], v[72:73], v[52:53]
	v_pk_mul_f32 v[74:75], v[74:75], v[70:71] neg_lo:[0,1] neg_hi:[0,1]
	v_pk_mul_f32 v[58:59], v[58:59], s[4:5] op_sel_hi:[1,0]
	v_cndmask_b32_e64 v70, v76, v74, s[16:17]
	v_cmp_lt_f32_e64 s[16:17], s0, v71
	v_mul_f32_e32 v74, 0x4f800000, v70
	v_exp_f32_e32 v58, v58
	v_cndmask_b32_e64 v71, v77, v75, s[16:17]
	v_cmp_gt_f32_e64 s[16:17], s2, v70
	v_exp_f32_e32 v59, v59
	v_pk_add_f32 v[62:63], v[62:63], 1.0 op_sel_hi:[1,0]
	v_cndmask_b32_e64 v70, v70, v74, s[16:17]
	v_sqrt_f32_e32 v74, v70
	v_rcp_f32_e32 v62, v62
	v_rcp_f32_e32 v63, v63
	v_pk_add_f32 v[58:59], v[58:59], 1.0 op_sel_hi:[1,0]
	v_add_u32_e32 v75, -1, v74
	v_fma_f32 v76, -v75, v74, v70
	v_cmp_ge_f32_e64 s[18:19], 0, v76
	v_add_u32_e32 v76, 1, v74
	v_pk_add_f32 v[36:37], v[36:37], v[48:49]
	v_cndmask_b32_e64 v75, v74, v75, s[18:19]
	v_fma_f32 v74, -v76, v74, v70
	v_cmp_lt_f32_e64 s[18:19], 0, v74
	v_pk_mul_f32 v[36:37], v[36:37], s[4:5] op_sel_hi:[1,0]
	v_pk_add_f32 v[40:41], v[40:41], v[44:45]
	v_cndmask_b32_e64 v74, v75, v76, s[18:19]
	v_mul_f32_e32 v75, 0x37800000, v74
	v_cndmask_b32_e64 v74, v74, v75, s[16:17]
	v_cmp_class_f32_e64 s[16:17], v70, v203
	v_exp_f32_e32 v36, v36
	v_exp_f32_e32 v37, v37
	v_cndmask_b32_e64 v70, v74, v70, s[16:17]
	v_cmp_gt_f32_e64 s[16:17], s2, v71
	v_mul_f32_e32 v74, 0x4f800000, v71
	v_pk_add_f32 v[36:37], v[36:37], 1.0 op_sel_hi:[1,0]
	v_cndmask_b32_e64 v71, v71, v74, s[16:17]
	v_sqrt_f32_e32 v74, v71
	v_rcp_f32_e32 v36, v36
	v_rcp_f32_e32 v37, v37
	v_pk_add_f32 v[42:43], v[42:43], v[46:47]
	v_add_u32_e32 v75, -1, v74
	v_fma_f32 v76, -v75, v74, v71
	v_cmp_ge_f32_e64 s[18:19], 0, v76
	v_add_u32_e32 v76, 1, v74
	v_pk_mul_f32 v[36:37], v[36:37], v[134:135]
	v_cndmask_b32_e64 v75, v74, v75, s[18:19]
	v_fma_f32 v74, -v76, v74, v71
	v_cmp_lt_f32_e64 s[18:19], 0, v74
	v_pk_mul_f32 v[36:37], v[36:37], s[56:57] op_sel_hi:[1,0]
	v_pk_add_f32 v[38:39], v[38:39], v[50:51]
	v_cndmask_b32_e64 v74, v75, v76, s[18:19]
	v_mul_f32_e32 v75, 0x37800000, v74
	v_cndmask_b32_e64 v74, v74, v75, s[16:17]
	v_cmp_class_f32_e64 s[16:17], v71, v203
	v_pk_add_f32 v[44:45], v[36:37], v[36:37]
	v_pk_mul_f32 v[36:37], v[36:37], s[50:51] op_sel_hi:[1,0]
	v_cndmask_b32_e64 v71, v74, v71, s[16:17]
	v_pk_mul_f32 v[54:55], v[54:55], v[70:71]
	ds_write_b128 v144, v[64:67] offset:44032
	ds_write_b128 v144, v[52:55] offset:61440
	v_rcp_f32_e32 v64, v56
	v_rcp_f32_e32 v65, v57
	v_pk_mul_f32 v[56:57], v[60:61], v[134:135]
	ds_read_b128 v[52:55], v158 offset:26112
	v_pk_mul_f32 v[56:57], v[56:57], s[56:57] op_sel_hi:[1,0]
	v_exp_f32_e32 v36, v36
	v_pk_add_f32 v[60:61], v[56:57], v[56:57]
	v_pk_mul_f32 v[56:57], v[56:57], s[50:51] op_sel_hi:[1,0]
	v_pk_fma_f32 v[66:67], v[60:61], s[70:71], 0.5 op_sel_hi:[1,0,0]
	v_exp_f32_e32 v56, v56
	v_exp_f32_e32 v57, v57
	v_pk_fma_f32 v[66:67], v[60:61], v[66:67], 1.0 op_sel_hi:[1,1,0]
	v_cmp_lt_f32_e64 s[16:17], s0, v60
	v_pk_mul_f32 v[66:67], v[66:67], v[60:61] neg_lo:[0,1] neg_hi:[0,1]
	v_pk_fma_f32 v[68:69], v[56:57], v[56:57], 1.0 op_sel_hi:[1,1,0] neg_lo:[1,0,0] neg_hi:[1,0,0]
	s_waitcnt lgkmcnt(0)
	v_pk_mul_f32 v[52:53], v[64:65], v[52:53]
	v_cndmask_b32_e64 v60, v68, v66, s[16:17]
	v_cmp_lt_f32_e64 s[16:17], s0, v61
	v_mul_f32_e32 v66, 0x4f800000, v60
	v_rcp_f32_e32 v64, v58
	v_cndmask_b32_e64 v61, v69, v67, s[16:17]
	v_cmp_gt_f32_e64 s[16:17], s2, v60
	v_rcp_f32_e32 v65, v59
	v_pk_mul_f32 v[58:59], v[62:63], v[136:137]
	v_cndmask_b32_e64 v60, v60, v66, s[16:17]
	v_sqrt_f32_e32 v66, v60
	v_pk_mul_f32 v[58:59], v[58:59], s[56:57] op_sel_hi:[1,0]
	v_exp_f32_e32 v37, v37
	v_pk_add_f32 v[62:63], v[58:59], v[58:59]
	v_add_u32_e32 v67, -1, v66
	v_fma_f32 v68, -v67, v66, v60
	v_cmp_ge_f32_e64 s[18:19], 0, v68
	v_add_u32_e32 v68, 1, v66
	v_pk_mul_f32 v[58:59], v[58:59], s[50:51] op_sel_hi:[1,0]
	v_cndmask_b32_e64 v67, v66, v67, s[18:19]
	v_fma_f32 v66, -v68, v66, v60
	v_cmp_lt_f32_e64 s[18:19], 0, v66
	v_exp_f32_e32 v58, v58
	v_exp_f32_e32 v59, v59
	v_cndmask_b32_e64 v66, v67, v68, s[18:19]
	v_mul_f32_e32 v67, 0x37800000, v66
	v_cndmask_b32_e64 v66, v66, v67, s[16:17]
	v_cmp_class_f32_e64 s[16:17], v60, v203
	v_pk_fma_f32 v[46:47], v[44:45], s[70:71], 0.5 op_sel_hi:[1,0,0]
	v_pk_fma_f32 v[48:49], v[36:37], v[36:37], 1.0 op_sel_hi:[1,1,0] neg_lo:[1,0,0] neg_hi:[1,0,0]
	v_cndmask_b32_e64 v60, v66, v60, s[16:17]
	v_cmp_gt_f32_e64 s[16:17], s2, v61
	v_mul_f32_e32 v66, 0x4f800000, v61
	v_pk_fma_f32 v[46:47], v[44:45], v[46:47], 1.0 op_sel_hi:[1,1,0]
	v_cndmask_b32_e64 v61, v61, v66, s[16:17]
	v_sqrt_f32_e32 v66, v61
	v_pk_mul_f32 v[46:47], v[46:47], v[44:45] neg_lo:[0,1] neg_hi:[0,1]
	v_pk_mul_f32 v[38:39], v[38:39], s[4:5] op_sel_hi:[1,0]
	v_pk_mul_f32 v[40:41], v[40:41], s[4:5] op_sel_hi:[1,0]
	v_add_u32_e32 v67, -1, v66
	v_fma_f32 v68, -v67, v66, v61
	v_cmp_ge_f32_e64 s[18:19], 0, v68
	v_add_u32_e32 v68, 1, v66
	v_exp_f32_e32 v38, v38
	v_cndmask_b32_e64 v67, v66, v67, s[18:19]
	v_fma_f32 v66, -v68, v66, v61
	v_cmp_lt_f32_e64 s[18:19], 0, v66
	v_exp_f32_e32 v39, v39
	v_pk_mul_f32 v[42:43], v[42:43], s[4:5] op_sel_hi:[1,0]
	v_cndmask_b32_e64 v66, v67, v68, s[18:19]
	v_mul_f32_e32 v67, 0x37800000, v66
	v_cndmask_b32_e64 v66, v66, v67, s[16:17]
	v_cmp_class_f32_e64 s[16:17], v61, v203
	v_pk_fma_f32 v[68:69], v[58:59], v[58:59], 1.0 op_sel_hi:[1,1,0] neg_lo:[1,0,0] neg_hi:[1,0,0]
	v_pk_add_f32 v[38:39], v[38:39], 1.0 op_sel_hi:[1,0]
	v_cndmask_b32_e64 v61, v66, v61, s[16:17]
	v_pk_fma_f32 v[66:67], v[62:63], s[70:71], 0.5 op_sel_hi:[1,0,0]
	v_cmp_lt_f32_e64 s[16:17], s0, v62
	v_pk_fma_f32 v[66:67], v[62:63], v[66:67], 1.0 op_sel_hi:[1,1,0]
	v_rcp_f32_e32 v38, v38
	v_pk_mul_f32 v[66:67], v[66:67], v[62:63] neg_lo:[0,1] neg_hi:[0,1]
	v_rcp_f32_e32 v39, v39
	v_cndmask_b32_e64 v62, v68, v66, s[16:17]
	v_cmp_lt_f32_e64 s[16:17], s0, v63
	v_mul_f32_e32 v66, 0x4f800000, v62
	v_pk_mul_f32 v[38:39], v[38:39], v[136:137]
	v_cndmask_b32_e64 v63, v69, v67, s[16:17]
	v_cmp_gt_f32_e64 s[16:17], s2, v62
	v_pk_mul_f32 v[38:39], v[38:39], s[56:57] op_sel_hi:[1,0]
	v_exp_f32_e32 v40, v40
	v_cndmask_b32_e64 v62, v62, v66, s[16:17]
	v_sqrt_f32_e32 v66, v62
	v_exp_f32_e32 v41, v41
	v_exp_f32_e32 v42, v42
	v_exp_f32_e32 v43, v43
	v_add_u32_e32 v67, -1, v66
	v_fma_f32 v68, -v67, v66, v62
	v_cmp_ge_f32_e64 s[18:19], 0, v68
	v_add_u32_e32 v68, 1, v66
	v_pk_mul_f32 v[54:55], v[64:65], v[54:55]
	v_cndmask_b32_e64 v67, v66, v67, s[18:19]
	v_fma_f32 v66, -v68, v66, v62
	v_cmp_lt_f32_e64 s[18:19], 0, v66
	v_pk_mul_f32 v[52:53], v[60:61], v[52:53]
	v_pk_add_f32 v[40:41], v[40:41], 1.0 op_sel_hi:[1,0]
	v_cndmask_b32_e64 v66, v67, v68, s[18:19]
	v_mul_f32_e32 v67, 0x37800000, v66
	v_cndmask_b32_e64 v66, v66, v67, s[16:17]
	v_cmp_class_f32_e64 s[16:17], v62, v203
	v_pk_add_f32 v[42:43], v[42:43], 1.0 op_sel_hi:[1,0]
	v_rcp_f32_e32 v40, v40
	v_cndmask_b32_e64 v62, v66, v62, s[16:17]
	v_cmp_gt_f32_e64 s[16:17], s2, v63
	v_mul_f32_e32 v66, 0x4f800000, v63
	v_rcp_f32_e32 v41, v41
	v_cndmask_b32_e64 v63, v63, v66, s[16:17]
	v_sqrt_f32_e32 v66, v63
	v_rcp_f32_e32 v42, v42
	v_rcp_f32_e32 v43, v43
	v_add_u32_e32 v67, -1, v66
	v_fma_f32 v68, -v67, v66, v63
	v_cmp_ge_f32_e64 s[18:19], 0, v68
	v_add_u32_e32 v68, 1, v66
	s_nop 0
	v_cndmask_b32_e64 v67, v66, v67, s[18:19]
	v_fma_f32 v66, -v68, v66, v63
	v_cmp_lt_f32_e64 s[18:19], 0, v66
	s_nop 1
	v_cndmask_b32_e64 v66, v67, v68, s[18:19]
	v_mul_f32_e32 v67, 0x37800000, v66
	v_cndmask_b32_e64 v66, v66, v67, s[16:17]
	v_cmp_class_f32_e64 s[16:17], v63, v203
	s_nop 1
	v_cndmask_b32_e64 v63, v66, v63, s[16:17]
	v_cmp_lt_f32_e64 s[16:17], s0, v44
	v_pk_mul_f32 v[54:55], v[54:55], v[62:63]
	ds_write_b128 v145, v[56:59] offset:44032
	ds_write_b128 v145, v[52:55] offset:61440
	v_cndmask_b32_e64 v44, v48, v46, s[16:17]
	v_cmp_lt_f32_e64 s[16:17], s0, v45
	v_mul_f32_e32 v46, 0x4f800000, v44
	ds_read_b128 v[52:55], v158 offset:30464
	v_cndmask_b32_e64 v45, v49, v47, s[16:17]
	v_cmp_gt_f32_e64 s[16:17], s2, v44
	s_waitcnt lgkmcnt(0)
	v_pk_mul_f32 v[40:41], v[40:41], v[52:53]
	v_cndmask_b32_e64 v44, v44, v46, s[16:17]
	v_sqrt_f32_e32 v46, v44
	v_pk_mul_f32 v[42:43], v[42:43], v[54:55]
	v_add_u32_e32 v47, -1, v46
	v_fma_f32 v48, -v47, v46, v44
	v_cmp_ge_f32_e64 s[18:19], 0, v48
	v_add_u32_e32 v48, 1, v46
	s_nop 0
	v_cndmask_b32_e64 v47, v46, v47, s[18:19]
	v_fma_f32 v46, -v48, v46, v44
	v_cmp_lt_f32_e64 s[18:19], 0, v46
	s_nop 1
	v_cndmask_b32_e64 v46, v47, v48, s[18:19]
	v_mul_f32_e32 v47, 0x37800000, v46
	v_cndmask_b32_e64 v46, v46, v47, s[16:17]
	v_cmp_class_f32_e64 s[16:17], v44, v203
	s_nop 1
	v_cndmask_b32_e64 v44, v46, v44, s[16:17]
	v_cmp_gt_f32_e64 s[16:17], s2, v45
	v_mul_f32_e32 v46, 0x4f800000, v45
	s_nop 0
	v_cndmask_b32_e64 v45, v45, v46, s[16:17]
	v_sqrt_f32_e32 v46, v45
	s_nop 0
	v_add_u32_e32 v47, -1, v46
	v_fma_f32 v48, -v47, v46, v45
	v_cmp_ge_f32_e64 s[18:19], 0, v48
	v_add_u32_e32 v48, 1, v46
	s_nop 0
	v_cndmask_b32_e64 v47, v46, v47, s[18:19]
	v_fma_f32 v46, -v48, v46, v45
	v_cmp_lt_f32_e64 s[18:19], 0, v46
	s_nop 1
	v_cndmask_b32_e64 v46, v47, v48, s[18:19]
	v_mul_f32_e32 v47, 0x37800000, v46
	v_cndmask_b32_e64 v46, v46, v47, s[16:17]
	v_cmp_class_f32_e64 s[16:17], v45, v203
	s_nop 1
	v_cndmask_b32_e64 v45, v46, v45, s[16:17]
	v_pk_add_f32 v[46:47], v[38:39], v[38:39]
	v_pk_mul_f32 v[38:39], v[38:39], s[50:51] op_sel_hi:[1,0]
	v_pk_fma_f32 v[48:49], v[46:47], s[70:71], 0.5 op_sel_hi:[1,0,0]
	v_exp_f32_e32 v38, v38
	v_exp_f32_e32 v39, v39
	v_pk_fma_f32 v[48:49], v[46:47], v[48:49], 1.0 op_sel_hi:[1,1,0]
	v_cmp_lt_f32_e64 s[16:17], s0, v46
	v_pk_mul_f32 v[48:49], v[48:49], v[46:47] neg_lo:[0,1] neg_hi:[0,1]
	v_pk_fma_f32 v[50:51], v[38:39], v[38:39], 1.0 op_sel_hi:[1,1,0] neg_lo:[1,0,0] neg_hi:[1,0,0]
	v_pk_mul_f32 v[40:41], v[44:45], v[40:41]
	v_cndmask_b32_e64 v46, v50, v48, s[16:17]
	v_cmp_lt_f32_e64 s[16:17], s0, v47
	v_mul_f32_e32 v48, 0x4f800000, v46
	s_nop 0
	v_cndmask_b32_e64 v47, v51, v49, s[16:17]
	v_cmp_gt_f32_e64 s[16:17], s2, v46
	s_nop 1
	v_cndmask_b32_e64 v46, v46, v48, s[16:17]
	v_sqrt_f32_e32 v48, v46
	s_nop 0
	v_add_u32_e32 v49, -1, v48
	v_fma_f32 v50, -v49, v48, v46
	v_cmp_ge_f32_e64 s[18:19], 0, v50
	v_add_u32_e32 v50, 1, v48
	s_nop 0
	v_cndmask_b32_e64 v49, v48, v49, s[18:19]
	v_fma_f32 v48, -v50, v48, v46
	v_cmp_lt_f32_e64 s[18:19], 0, v48
	s_nop 1
	v_cndmask_b32_e64 v48, v49, v50, s[18:19]
	v_mul_f32_e32 v49, 0x37800000, v48
	v_cndmask_b32_e64 v48, v48, v49, s[16:17]
	v_cmp_class_f32_e64 s[16:17], v46, v203
	s_nop 1
	v_cndmask_b32_e64 v46, v48, v46, s[16:17]
	v_cmp_gt_f32_e64 s[16:17], s2, v47
	v_mul_f32_e32 v48, 0x4f800000, v47
	s_lshl_b64 s[2:3], s[44:45], 15
	v_cndmask_b32_e64 v47, v47, v48, s[16:17]
	v_sqrt_f32_e32 v48, v47
	s_add_u32 s4, s33, s2
	s_addc_u32 s5, s73, s3
	v_add_u32_e32 v49, -1, v48
	v_fma_f32 v50, -v49, v48, v47
	v_cmp_ge_f32_e64 s[18:19], 0, v50
	v_add_u32_e32 v50, 1, v48
	s_nop 0
	v_cndmask_b32_e64 v49, v48, v49, s[18:19]
	v_fma_f32 v48, -v50, v48, v47
	v_cmp_lt_f32_e64 s[18:19], 0, v48
	s_nop 1
	v_cndmask_b32_e64 v48, v49, v50, s[18:19]
	v_mul_f32_e32 v49, 0x37800000, v48
	v_cndmask_b32_e64 v48, v48, v49, s[16:17]
	v_cmp_class_f32_e64 s[16:17], v47, v203
	s_nop 1
	v_cndmask_b32_e64 v47, v48, v47, s[16:17]
	v_pk_mul_f32 v[42:43], v[42:43], v[46:47]
	ds_write_b128 v146, v[36:39] offset:44032
	ds_write_b128 v146, v[40:43] offset:61440
	s_waitcnt lgkmcnt(0)
	s_barrier
	ds_read_b128 v[36:39], v88 offset:44032
	ds_read_b128 v[40:43], v88 offset:44048
	s_waitcnt lgkmcnt(1)
	v_sub_f32_e32 v38, 1.0, v38
	v_sub_f32_e32 v36, 1.0, v36
	v_sub_f32_e32 v37, 1.0, v37
	s_waitcnt lgkmcnt(0)
	v_sub_f32_e32 v40, 1.0, v40
	v_sub_f32_e32 v41, 1.0, v41
	v_sub_f32_e32 v39, 1.0, v39
	v_cvt_pk_bf16_f32 v36, v36, v37
	v_cvt_pk_bf16_f32 v37, v38, v39
	v_cvt_pk_bf16_f32 v38, v40, v41
	v_lshl_add_u64 v[40:41], s[4:5], 0, v[90:91]
	v_sub_f32_e32 v42, 1.0, v42
	v_sub_f32_e32 v43, 1.0, v43
	v_cvt_pk_bf16_f32 v39, v42, v43
	global_store_dwordx4 v[40:41], v[36:39], off sc1
	ds_read_b128 v[36:39], v88 offset:61440
	ds_read_b128 v[40:43], v88 offset:61456
	s_waitcnt lgkmcnt(1)
	v_cvt_pk_bf16_f32 v36, v36, v37
	v_cvt_pk_bf16_f32 v37, v38, v39
	s_waitcnt lgkmcnt(0)
	v_cvt_pk_bf16_f32 v38, v40, v41
	v_lshl_add_u64 v[40:41], s[4:5], 0, v[130:131]
	v_cvt_pk_bf16_f32 v39, v42, v43
	global_store_dwordx4 v[40:41], v[36:39], off sc1
	ds_read_b128 v[36:39], v89 offset:34816
	ds_read_b128 v[40:43], v89 offset:34832
	s_waitcnt lgkmcnt(1)
	v_sub_f32_e32 v38, 1.0, v38
	v_sub_f32_e32 v36, 1.0, v36
	v_sub_f32_e32 v37, 1.0, v37
	s_waitcnt lgkmcnt(0)
	v_sub_f32_e32 v40, 1.0, v40
	v_sub_f32_e32 v41, 1.0, v41
	v_sub_f32_e32 v39, 1.0, v39
	v_cvt_pk_bf16_f32 v36, v36, v37
	v_cvt_pk_bf16_f32 v37, v38, v39
	v_cvt_pk_bf16_f32 v38, v40, v41
	v_lshl_add_u64 v[40:41], s[4:5], 0, v[92:93]
	v_sub_f32_e32 v42, 1.0, v42
	v_sub_f32_e32 v43, 1.0, v43
	v_cvt_pk_bf16_f32 v39, v42, v43
	global_store_dwordx4 v[40:41], v[36:39], off sc1
	ds_read_b128 v[36:39], v89 offset:52224
	ds_read_b128 v[40:43], v89 offset:52240
	s_waitcnt lgkmcnt(1)
	v_cvt_pk_bf16_f32 v36, v36, v37
	v_cvt_pk_bf16_f32 v37, v38, v39
	s_waitcnt lgkmcnt(0)
	v_cvt_pk_bf16_f32 v38, v40, v41
	v_lshl_add_u64 v[40:41], s[4:5], 0, v[94:95]
	v_cvt_pk_bf16_f32 v39, v42, v43
	global_store_dwordx4 v[40:41], v[36:39], off sc1
	ds_read2st64_b32 v[36:37], v96 offset0:172 offset1:240
	ds_read2st64_b32 v[38:39], v98 offset0:172 offset1:240
	ds_read2st64_b32 v[40:41], v100 offset0:172 offset1:240
	ds_read2st64_b32 v[42:43], v102 offset0:172 offset1:240
	ds_read2st64_b32 v[44:45], v106 offset0:172 offset1:240
	ds_read2st64_b32 v[46:47], v108 offset0:172 offset1:240
	ds_read2st64_b32 v[48:49], v110 offset0:172 offset1:240
	ds_read2st64_b32 v[50:51], v112 offset0:172 offset1:240
	ds_read2st64_b32 v[52:53], v114 offset0:172 offset1:240
	ds_read2st64_b32 v[54:55], v116 offset0:172 offset1:240
	ds_read2st64_b32 v[56:57], v118 offset0:172 offset1:240
	ds_read2st64_b32 v[58:59], v120 offset0:172 offset1:240
	ds_read2st64_b32 v[60:61], v122 offset0:172 offset1:240
	ds_read2st64_b32 v[62:63], v124 offset0:172 offset1:240
	ds_read2st64_b32 v[64:65], v126 offset0:172 offset1:240
	ds_read2st64_b32 v[66:67], v128 offset0:172 offset1:240
	s_waitcnt lgkmcnt(14)
	v_fma_f32 v37, 0, v36, v37
	v_fmac_f32_e32 v39, v37, v38
	s_waitcnt lgkmcnt(13)
	v_fmac_f32_e32 v41, v39, v40
	s_waitcnt lgkmcnt(12)
	v_fmac_f32_e32 v43, v41, v42
	s_waitcnt lgkmcnt(11)
	v_fmac_f32_e32 v45, v43, v44
	s_waitcnt lgkmcnt(10)
	v_fmac_f32_e32 v47, v45, v46
	s_waitcnt lgkmcnt(9)
	v_fmac_f32_e32 v49, v47, v48
	s_waitcnt lgkmcnt(8)
	v_fmac_f32_e32 v51, v49, v50
	s_waitcnt lgkmcnt(7)
	v_fmac_f32_e32 v53, v51, v52
	v_mul_f32_e32 v36, v36, v38
	v_mov_b32_e32 v37, v53
	s_waitcnt lgkmcnt(6)
	v_mov_b32_e32 v41, v54
	v_pk_mul_f32 v[38:39], v[36:37], v[40:41]
	v_mov_b32_e32 v43, v55
	v_pk_mul_f32 v[38:39], v[38:39], v[42:43]
	v_pk_fma_f32 v[36:37], v[36:37], v[40:41], v[42:43]
	s_waitcnt lgkmcnt(5)
	v_mov_b32_e32 v45, v56
	v_mov_b32_e32 v36, v38
	v_pk_mul_f32 v[38:39], v[38:39], v[44:45]
	v_mov_b32_e32 v47, v57
	v_pk_mul_f32 v[38:39], v[38:39], v[46:47]
	v_pk_fma_f32 v[36:37], v[36:37], v[44:45], v[46:47]
	s_waitcnt lgkmcnt(4)
	v_mov_b32_e32 v49, v58
	v_mov_b32_e32 v39, v37
	v_pk_mul_f32 v[36:37], v[38:39], v[48:49]
	v_mov_b32_e32 v51, v59
	v_pk_mul_f32 v[36:37], v[36:37], v[50:51]
	v_pk_fma_f32 v[38:39], v[38:39], v[48:49], v[50:51]
	s_waitcnt lgkmcnt(3)
	v_mov_b32_e32 v53, v60
	v_mov_b32_e32 v38, v36
	v_pk_mul_f32 v[36:37], v[36:37], v[52:53]
	v_mov_b32_e32 v55, v61
	v_pk_mul_f32 v[36:37], v[36:37], v[54:55]
	v_pk_fma_f32 v[38:39], v[38:39], v[52:53], v[54:55]
	s_waitcnt lgkmcnt(2)
	v_mov_b32_e32 v57, v62
	v_mov_b32_e32 v37, v39
	v_pk_mul_f32 v[38:39], v[36:37], v[56:57]
	v_mov_b32_e32 v59, v63
	v_pk_mul_f32 v[38:39], v[38:39], v[58:59]
	v_pk_fma_f32 v[36:37], v[36:37], v[56:57], v[58:59]
	s_waitcnt lgkmcnt(1)
	v_mov_b32_e32 v61, v64
	v_mov_b32_e32 v36, v38
	v_pk_mul_f32 v[38:39], v[38:39], v[60:61]
	v_mov_b32_e32 v63, v65
	v_pk_mul_f32 v[40:41], v[38:39], v[62:63]
	v_pk_fma_f32 v[36:37], v[36:37], v[60:61], v[62:63]
	s_waitcnt lgkmcnt(0)
	v_mov_b32_e32 v65, v66
	v_mov_b32_e32 v41, v37
	v_pk_mul_f32 v[36:37], v[40:41], v[64:65]
	s_nop 0
	v_pk_mul_f32 v[38:39], v[36:37], v[66:67]
	v_pk_fma_f32 v[36:37], v[40:41], v[64:65], v[66:67]
	v_mov_b32_e32 v40, 1.0
	v_mov_b32_e32 v39, v37
	ds_write_b64 v159, v[38:39]
	s_waitcnt lgkmcnt(0)
	s_barrier
	v_mov_b32_e32 v41, 0
	s_and_saveexec_b64 s[2:3], s[8:9]
	s_cbranch_execz .LBB0_741
	v_add_u32_e32 v36, 0x23c00, v160
	ds_read_b64 v[40:41], v36
	s_waitcnt lgkmcnt(0)
	v_fmac_f32_e32 v41, 0, v40
	s_or_b64 exec, exec, s[2:3]
	s_and_saveexec_b64 s[2:3], s[10:11]
	s_cbranch_execnz .LBB0_742

.LBB0_781:
	v_add_co_u32_e32 v136, vcc, s0, v118
	global_load_dwordx4 v[128:131], v[118:119], off
	s_nop 0
	v_addc_co_u32_e32 v137, vcc, 0, v119, vcc
	v_add_co_u32_e32 v156, vcc, s7, v118
	s_nop 1
	v_addc_co_u32_e32 v157, vcc, 0, v119, vcc
	v_add_co_u32_e32 v158, vcc, s67, v118
	global_load_dwordx4 v[132:135], v[136:137], off
	global_load_dwordx4 v[140:143], v[156:157], off
	v_addc_co_u32_e32 v159, vcc, 0, v119, vcc
	global_load_dwordx4 v[144:147], v[158:159], off
	ds_read_b128 v[148:151], v126
	ds_read_b128 v[152:155], v126 offset:16640
	s_waitcnt vmcnt(15) lgkmcnt(7)
	v_mfma_f32_16x16x32_bf16 v[100:103], v[28:31], v[68:71], v[100:103]
	s_waitcnt vmcnt(13)
	v_mfma_f32_16x16x32_bf16 v[96:99], v[40:43], v[68:71], v[96:99]
	s_waitcnt vmcnt(8)
	v_mfma_f32_16x16x32_bf16 v[92:95], v[52:55], v[68:71], v[92:95]
	v_mfma_f32_16x16x32_bf16 v[88:91], v[36:39], v[68:71], v[88:91]
	s_waitcnt lgkmcnt(5)
	v_mfma_f32_16x16x32_bf16 v[84:87], v[28:31], v[60:63], v[84:87]
	v_mfma_f32_16x16x32_bf16 v[80:83], v[40:43], v[60:63], v[80:83]
	v_mfma_f32_16x16x32_bf16 v[76:79], v[52:55], v[60:63], v[76:79]
	v_mfma_f32_16x16x32_bf16 v[72:75], v[36:39], v[60:63], v[72:75]
	global_load_dwordx4 v[28:31], v[118:119], off offset:1024
	global_load_dwordx4 v[40:43], v[136:137], off offset:1024
	global_load_dwordx4 v[52:55], v[156:157], off offset:1024
	global_load_dwordx4 v[36:39], v[158:159], off offset:1024
	ds_read_b128 v[68:71], v126 offset:64
	ds_read_b128 v[60:63], v126 offset:16704
	v_mfma_f32_16x16x32_bf16 v[100:103], v[8:11], v[64:67], v[100:103]
	v_mfma_f32_16x16x32_bf16 v[96:99], v[20:23], v[64:67], v[96:99]
	s_waitcnt vmcnt(10)
	v_mfma_f32_16x16x32_bf16 v[92:95], v[32:35], v[64:67], v[92:95]
	v_mfma_f32_16x16x32_bf16 v[88:91], v[24:27], v[64:67], v[88:91]
	s_waitcnt lgkmcnt(5)
	v_mfma_f32_16x16x32_bf16 v[84:87], v[8:11], v[56:59], v[84:87]
	v_mfma_f32_16x16x32_bf16 v[80:83], v[20:23], v[56:59], v[80:83]
	v_mfma_f32_16x16x32_bf16 v[76:79], v[32:35], v[56:59], v[76:79]
	v_mfma_f32_16x16x32_bf16 v[72:75], v[24:27], v[56:59], v[72:75]
	global_load_dwordx4 v[8:11], v[118:119], off offset:2048
	global_load_dwordx4 v[20:23], v[136:137], off offset:2048
	global_load_dwordx4 v[32:35], v[156:157], off offset:2048
	global_load_dwordx4 v[24:27], v[158:159], off offset:2048
	ds_read_b128 v[64:67], v126 offset:128
	ds_read_b128 v[56:59], v126 offset:16768
	v_mfma_f32_16x16x32_bf16 v[100:103], v[0:3], v[48:51], v[100:103]
	v_mfma_f32_16x16x32_bf16 v[96:99], v[4:7], v[48:51], v[96:99]
	s_waitcnt vmcnt(13)
	v_mfma_f32_16x16x32_bf16 v[92:95], v[16:19], v[48:51], v[92:95]
	s_waitcnt vmcnt(12)
	v_mfma_f32_16x16x32_bf16 v[88:91], v[12:15], v[48:51], v[88:91]
	s_waitcnt lgkmcnt(6)
	v_mfma_f32_16x16x32_bf16 v[84:87], v[0:3], v[44:47], v[84:87]
	v_mfma_f32_16x16x32_bf16 v[80:83], v[4:7], v[44:47], v[80:83]
	v_mfma_f32_16x16x32_bf16 v[76:79], v[16:19], v[44:47], v[76:79]
	v_mfma_f32_16x16x32_bf16 v[72:75], v[12:15], v[44:47], v[72:75]
	global_load_dwordx4 v[0:3], v[118:119], off offset:3072
	global_load_dwordx4 v[4:7], v[136:137], off offset:3072
	global_load_dwordx4 v[16:19], v[156:157], off offset:3072
	global_load_dwordx4 v[12:15], v[158:159], off offset:3072
	ds_read_b128 v[48:51], v126 offset:192
	ds_read_b128 v[44:47], v126 offset:16832
	s_waitcnt vmcnt(15) lgkmcnt(7)
	v_mfma_f32_16x16x32_bf16 v[100:103], v[128:131], v[148:151], v[100:103]
	s_waitcnt vmcnt(14)
	v_mfma_f32_16x16x32_bf16 v[96:99], v[132:135], v[148:151], v[96:99]
	s_waitcnt vmcnt(13)
	v_mfma_f32_16x16x32_bf16 v[92:95], v[140:143], v[148:151], v[92:95]
	s_waitcnt vmcnt(12)
	v_mfma_f32_16x16x32_bf16 v[88:91], v[144:147], v[148:151], v[88:91]
	s_waitcnt lgkmcnt(6)
	v_mfma_f32_16x16x32_bf16 v[84:87], v[128:131], v[152:155], v[84:87]
	v_mfma_f32_16x16x32_bf16 v[80:83], v[132:135], v[152:155], v[80:83]
	v_mfma_f32_16x16x32_bf16 v[76:79], v[140:143], v[152:155], v[76:79]
	v_mfma_f32_16x16x32_bf16 v[72:75], v[144:147], v[152:155], v[72:75]
	s_add_i32 s2, s2, 4
	v_lshl_add_u64 v[118:119], v[118:119], 0, s[52:53]
	s_cmp_lt_u32 s2, 8
	v_add_u32_e32 v126, 0x100, v126
	s_cbranch_scc1 .LBB0_781
	v_add_co_u32_e32 v118, vcc, 0x3000, v116
	s_nop 1
	v_addc_co_u32_e32 v119, vcc, 0, v117, vcc
	v_add_co_u32_e32 v130, vcc, 0x7000, v116
	s_nop 1
	v_addc_co_u32_e32 v131, vcc, 0, v117, vcc
	global_load_dwordx4 v[126:129], v[118:119], off offset:3072
	s_nop 0
	global_load_dwordx4 v[130:133], v[130:131], off offset:3072
	v_add_co_u32_e32 v118, vcc, 0xb000, v116
	s_nop 1
	v_addc_co_u32_e32 v119, vcc, 0, v117, vcc
	v_add_co_u32_e32 v134, vcc, 0xf000, v116
	s_nop 1
	v_addc_co_u32_e32 v135, vcc, 0, v117, vcc
	global_load_dwordx4 v[116:119], v[118:119], off offset:3072
	s_nop 0
	global_load_dwordx4 v[134:137], v[134:135], off offset:3072
	ds_read_b128 v[140:143], v125 offset:960
	ds_read_b128 v[144:147], v125 offset:17600
	s_waitcnt vmcnt(15) lgkmcnt(7)
	v_mfma_f32_16x16x32_bf16 v[100:103], v[28:31], v[68:71], v[100:103]
	s_waitcnt vmcnt(14)
	v_mfma_f32_16x16x32_bf16 v[96:99], v[40:43], v[68:71], v[96:99]
	s_waitcnt vmcnt(13)
	v_mfma_f32_16x16x32_bf16 v[92:95], v[52:55], v[68:71], v[92:95]
	s_waitcnt vmcnt(12)
	v_mfma_f32_16x16x32_bf16 v[68:71], v[36:39], v[68:71], v[88:91]
	s_waitcnt lgkmcnt(6)
	v_mfma_f32_16x16x32_bf16 v[28:31], v[28:31], v[60:63], v[84:87]
	v_mfma_f32_16x16x32_bf16 v[40:43], v[40:43], v[60:63], v[80:83]
	v_mfma_f32_16x16x32_bf16 v[52:55], v[52:55], v[60:63], v[76:79]
	v_mfma_f32_16x16x32_bf16 v[36:39], v[36:39], v[60:63], v[72:75]
	s_waitcnt vmcnt(11) lgkmcnt(5)
	v_mfma_f32_16x16x32_bf16 v[60:63], v[8:11], v[64:67], v[100:103]
	s_waitcnt vmcnt(10)
	v_mfma_f32_16x16x32_bf16 v[72:75], v[20:23], v[64:67], v[96:99]
	s_waitcnt vmcnt(9)
	v_mfma_f32_16x16x32_bf16 v[76:79], v[32:35], v[64:67], v[92:95]
	s_waitcnt vmcnt(8)
	v_mfma_f32_16x16x32_bf16 v[64:67], v[24:27], v[64:67], v[68:71]
	s_waitcnt lgkmcnt(4)
	v_mfma_f32_16x16x32_bf16 v[8:11], v[8:11], v[56:59], v[28:31]
	v_mfma_f32_16x16x32_bf16 v[20:23], v[20:23], v[56:59], v[40:43]
	v_mfma_f32_16x16x32_bf16 v[28:31], v[32:35], v[56:59], v[52:55]
	v_mfma_f32_16x16x32_bf16 v[24:27], v[24:27], v[56:59], v[36:39]
	s_waitcnt vmcnt(7) lgkmcnt(3)
	v_mfma_f32_16x16x32_bf16 v[32:35], v[0:3], v[48:51], v[60:63]
	s_waitcnt vmcnt(6)
	v_mfma_f32_16x16x32_bf16 v[36:39], v[4:7], v[48:51], v[72:75]
	s_waitcnt vmcnt(5)
	v_mfma_f32_16x16x32_bf16 v[40:43], v[16:19], v[48:51], v[76:79]
	s_waitcnt vmcnt(4)
	v_mfma_f32_16x16x32_bf16 v[48:51], v[12:15], v[48:51], v[64:67]
	s_waitcnt lgkmcnt(2)
	v_mfma_f32_16x16x32_bf16 v[0:3], v[0:3], v[44:47], v[8:11]
	v_mfma_f32_16x16x32_bf16 v[4:7], v[4:7], v[44:47], v[20:23]
	v_mfma_f32_16x16x32_bf16 v[8:11], v[16:19], v[44:47], v[28:31]
	v_mfma_f32_16x16x32_bf16 v[12:15], v[12:15], v[44:47], v[24:27]
	s_waitcnt vmcnt(3) lgkmcnt(1)
	v_mfma_f32_16x16x32_bf16 v[16:19], v[126:129], v[140:143], v[32:35]
	s_ashr_i32 s7, s6, 31
	s_add_i32 s4, s4, s37
	s_cmpk_lt_i32 s4, 0x90
	s_waitcnt vmcnt(2)
	v_mfma_f32_16x16x32_bf16 v[20:23], v[130:133], v[140:143], v[36:39]
	v_lshl_add_u64 v[32:33], v[110:111], 0, s[6:7]
	s_nop 1
	ds_bpermute_b32 v16, v123, v16
	ds_bpermute_b32 v17, v123, v17
	ds_bpermute_b32 v18, v123, v18
	ds_bpermute_b32 v19, v123, v19
	v_mov_b32_e32 v34, 0x240
	v_mad_i64_i32 v[32:33], s[2:3], s5, v34, v[32:33]
	v_lshlrev_b64 v[32:33], 10, v[32:33]
	v_lshl_add_u64 v[34:35], v[112:113], 0, v[32:33]
	v_readlane_b32 s2, v251, 33
	s_waitcnt lgkmcnt(0)
	global_store_dwordx4 v[34:35], v[16:19], off sc1
	ds_bpermute_b32 v16, v123, v20
	ds_bpermute_b32 v17, v123, v21
	ds_bpermute_b32 v18, v123, v22
	ds_bpermute_b32 v19, v123, v23
	v_readlane_b32 s3, v251, 34
	s_waitcnt vmcnt(2)
	v_mfma_f32_16x16x32_bf16 v[24:27], v[116:119], v[140:143], v[40:43]
	v_lshl_add_u64 v[20:21], s[2:3], 0, v[32:33]
	v_lshl_add_u64 v[20:21], v[20:21], 0, v[172:173]
	s_mov_b32 s2, 0x4b62b000
	v_add_co_u32_e32 v22, vcc, s2, v20
	s_waitcnt vmcnt(1)
	v_mfma_f32_16x16x32_bf16 v[28:31], v[134:137], v[140:143], v[48:51]
	v_addc_co_u32_e32 v23, vcc, 0, v21, vcc
	s_waitcnt lgkmcnt(0)
	global_store_dwordx4 v[22:23], v[16:19], off offset:1600 sc1
	ds_bpermute_b32 v16, v123, v24
	ds_bpermute_b32 v17, v123, v25
	ds_bpermute_b32 v18, v123, v26
	ds_bpermute_b32 v19, v123, v27
	v_mfma_f32_16x16x32_bf16 v[0:3], v[126:129], v[144:147], v[0:3]
	s_waitcnt lgkmcnt(0)
	global_store_dwordx4 v[22:23], v[16:19], off offset:1664 sc1
	ds_bpermute_b32 v16, v123, v28
	ds_bpermute_b32 v17, v123, v29
	ds_bpermute_b32 v18, v123, v30
	ds_bpermute_b32 v19, v123, v31
	s_nop 1
	ds_bpermute_b32 v0, v123, v0
	ds_bpermute_b32 v1, v123, v1
	ds_bpermute_b32 v2, v123, v2
	ds_bpermute_b32 v3, v123, v3
	v_mfma_f32_16x16x32_bf16 v[4:7], v[130:133], v[144:147], v[4:7]
	s_waitcnt lgkmcnt(4)
	global_store_dwordx4 v[22:23], v[16:19], off offset:1728 sc1
	s_nop 1
	v_add_co_u32_e32 v16, vcc, s0, v34
	v_mfma_f32_16x16x32_bf16 v[8:11], v[116:119], v[144:147], v[8:11]
	s_nop 0
	v_addc_co_u32_e32 v17, vcc, 0, v35, vcc
	s_waitcnt lgkmcnt(0)
	global_store_dwordx4 v[16:17], v[0:3], off sc1
	ds_bpermute_b32 v0, v123, v4
	ds_bpermute_b32 v1, v123, v5
	ds_bpermute_b32 v2, v123, v6
	ds_bpermute_b32 v3, v123, v7
	s_mov_b32 s0, 0x4b62f000
	v_add_co_u32_e32 v4, vcc, s0, v20
	v_mfma_f32_16x16x32_bf16 v[12:15], v[134:137], v[144:147], v[12:15]
	s_nop 0
	v_addc_co_u32_e32 v5, vcc, 0, v21, vcc
	s_waitcnt lgkmcnt(0)
	global_store_dwordx4 v[4:5], v[0:3], off offset:1600 sc1
	ds_bpermute_b32 v0, v123, v8
	ds_bpermute_b32 v1, v123, v9
	ds_bpermute_b32 v2, v123, v10
	ds_bpermute_b32 v3, v123, v11
	s_waitcnt lgkmcnt(0)
	global_store_dwordx4 v[4:5], v[0:3], off offset:1664 sc1
	ds_bpermute_b32 v0, v123, v12
	ds_bpermute_b32 v1, v123, v13
	ds_bpermute_b32 v2, v123, v14
	ds_bpermute_b32 v3, v123, v15
	s_waitcnt lgkmcnt(0)
	global_store_dwordx4 v[4:5], v[0:3], off offset:1728 sc1
	s_waitcnt lgkmcnt(0)
	s_barrier
	s_cbranch_scc1 .LBB0_748

.LBB0_819:
	v_lshl_add_u64 v[136:137], s[6:7], 0, v[106:107]
	v_add_co_u32_e32 v140, vcc, s2, v136
	s_nop 1
	v_addc_co_u32_e32 v141, vcc, 0, v137, vcc
	v_add_co_u32_e32 v142, vcc, s3, v136
	global_load_dwordx4 v[112:115], v[136:137], off
	global_load_dwordx4 v[116:119], v[140:141], off
	v_addc_co_u32_e32 v143, vcc, 0, v137, vcc
	v_add_co_u32_e32 v144, vcc, s67, v136
	s_nop 1
	v_addc_co_u32_e32 v145, vcc, 0, v137, vcc
	global_load_dwordx4 v[120:123], v[142:143], off
	global_load_dwordx4 v[124:127], v[144:145], off
	ds_read_b128 v[128:131], v111
	ds_read_b128 v[132:135], v111 offset:16640
	s_waitcnt vmcnt(15) lgkmcnt(7)
	v_mfma_f32_16x16x32_bf16 v[100:103], v[28:31], v[68:71], v[100:103]
	s_waitcnt vmcnt(13)
	v_mfma_f32_16x16x32_bf16 v[96:99], v[40:43], v[68:71], v[96:99]
	s_waitcnt vmcnt(8)
	v_mfma_f32_16x16x32_bf16 v[92:95], v[44:47], v[68:71], v[92:95]
	v_mfma_f32_16x16x32_bf16 v[88:91], v[36:39], v[68:71], v[88:91]
	s_waitcnt lgkmcnt(5)
	v_mfma_f32_16x16x32_bf16 v[84:87], v[28:31], v[60:63], v[84:87]
	v_mfma_f32_16x16x32_bf16 v[80:83], v[40:43], v[60:63], v[80:83]
	v_mfma_f32_16x16x32_bf16 v[76:79], v[44:47], v[60:63], v[76:79]
	v_mfma_f32_16x16x32_bf16 v[72:75], v[36:39], v[60:63], v[72:75]
	global_load_dwordx4 v[28:31], v[136:137], off offset:1024
	global_load_dwordx4 v[40:43], v[140:141], off offset:1024
	global_load_dwordx4 v[44:47], v[142:143], off offset:1024
	global_load_dwordx4 v[36:39], v[144:145], off offset:1024
	ds_read_b128 v[68:71], v111 offset:64
	ds_read_b128 v[60:63], v111 offset:16704
	v_mfma_f32_16x16x32_bf16 v[100:103], v[8:11], v[64:67], v[100:103]
	v_mfma_f32_16x16x32_bf16 v[96:99], v[20:23], v[64:67], v[96:99]
	s_waitcnt vmcnt(10)
	v_mfma_f32_16x16x32_bf16 v[92:95], v[32:35], v[64:67], v[92:95]
	v_mfma_f32_16x16x32_bf16 v[88:91], v[24:27], v[64:67], v[88:91]
	s_waitcnt lgkmcnt(5)
	v_mfma_f32_16x16x32_bf16 v[84:87], v[8:11], v[56:59], v[84:87]
	v_mfma_f32_16x16x32_bf16 v[80:83], v[20:23], v[56:59], v[80:83]
	v_mfma_f32_16x16x32_bf16 v[76:79], v[32:35], v[56:59], v[76:79]
	v_mfma_f32_16x16x32_bf16 v[72:75], v[24:27], v[56:59], v[72:75]
	global_load_dwordx4 v[8:11], v[136:137], off offset:2048
	global_load_dwordx4 v[20:23], v[140:141], off offset:2048
	global_load_dwordx4 v[32:35], v[142:143], off offset:2048
	global_load_dwordx4 v[24:27], v[144:145], off offset:2048
	ds_read_b128 v[64:67], v111 offset:128
	ds_read_b128 v[56:59], v111 offset:16768
	v_mfma_f32_16x16x32_bf16 v[100:103], v[0:3], v[52:55], v[100:103]
	v_mfma_f32_16x16x32_bf16 v[96:99], v[4:7], v[52:55], v[96:99]
	s_waitcnt vmcnt(13)
	v_mfma_f32_16x16x32_bf16 v[92:95], v[16:19], v[52:55], v[92:95]
	s_waitcnt vmcnt(12)
	v_mfma_f32_16x16x32_bf16 v[88:91], v[12:15], v[52:55], v[88:91]
	s_waitcnt lgkmcnt(6)
	v_mfma_f32_16x16x32_bf16 v[84:87], v[0:3], v[48:51], v[84:87]
	v_mfma_f32_16x16x32_bf16 v[80:83], v[4:7], v[48:51], v[80:83]
	v_mfma_f32_16x16x32_bf16 v[76:79], v[16:19], v[48:51], v[76:79]
	v_mfma_f32_16x16x32_bf16 v[72:75], v[12:15], v[48:51], v[72:75]
	global_load_dwordx4 v[0:3], v[136:137], off offset:3072
	global_load_dwordx4 v[4:7], v[140:141], off offset:3072
	global_load_dwordx4 v[16:19], v[142:143], off offset:3072
	global_load_dwordx4 v[12:15], v[144:145], off offset:3072
	ds_read_b128 v[52:55], v111 offset:192
	ds_read_b128 v[48:51], v111 offset:16832
	s_waitcnt vmcnt(15) lgkmcnt(7)
	v_mfma_f32_16x16x32_bf16 v[100:103], v[112:115], v[128:131], v[100:103]
	s_waitcnt vmcnt(14)
	v_mfma_f32_16x16x32_bf16 v[96:99], v[116:119], v[128:131], v[96:99]
	s_waitcnt vmcnt(13)
	v_mfma_f32_16x16x32_bf16 v[92:95], v[120:123], v[128:131], v[92:95]
	s_waitcnt vmcnt(12)
	v_mfma_f32_16x16x32_bf16 v[88:91], v[124:127], v[128:131], v[88:91]
	s_waitcnt lgkmcnt(6)
	v_mfma_f32_16x16x32_bf16 v[84:87], v[112:115], v[132:135], v[84:87]
	v_mfma_f32_16x16x32_bf16 v[80:83], v[116:119], v[132:135], v[80:83]
	v_mfma_f32_16x16x32_bf16 v[76:79], v[120:123], v[132:135], v[76:79]
	v_mfma_f32_16x16x32_bf16 v[72:75], v[124:127], v[132:135], v[72:75]
	s_add_i32 s1, s1, 4
	s_add_u32 s6, s6, 0x1000
	s_addc_u32 s7, s7, 0
	s_cmp_lt_u32 s1, 8
	v_add_u32_e32 v111, 0x100, v111
	s_cbranch_scc1 .LBB0_819
	v_add_co_u32_e32 v106, vcc, 0x3000, v104
	s_nop 1
	v_addc_co_u32_e32 v107, vcc, 0, v105, vcc
	v_add_co_u32_e32 v116, vcc, 0x7000, v104
	s_nop 1
	v_addc_co_u32_e32 v117, vcc, 0, v105, vcc
	global_load_dwordx4 v[112:115], v[106:107], off offset:3072
	s_nop 0
	global_load_dwordx4 v[116:119], v[116:117], off offset:3072
	v_add_co_u32_e32 v106, vcc, 0xb000, v104
	s_nop 1
	v_addc_co_u32_e32 v107, vcc, 0, v105, vcc
	v_add_co_u32_e32 v120, vcc, 0xf000, v104
	s_nop 1
	v_addc_co_u32_e32 v121, vcc, 0, v105, vcc
	global_load_dwordx4 v[104:107], v[106:107], off offset:3072
	s_nop 0
	global_load_dwordx4 v[120:123], v[120:121], off offset:3072
	ds_read_b128 v[124:127], v110 offset:960
	ds_read_b128 v[128:131], v110 offset:17600
	s_waitcnt vmcnt(15) lgkmcnt(7)
	v_mfma_f32_16x16x32_bf16 v[100:103], v[28:31], v[68:71], v[100:103]
	s_waitcnt vmcnt(14)
	v_mfma_f32_16x16x32_bf16 v[96:99], v[40:43], v[68:71], v[96:99]
	s_waitcnt vmcnt(13)
	v_mfma_f32_16x16x32_bf16 v[92:95], v[44:47], v[68:71], v[92:95]
	s_waitcnt vmcnt(12)
	v_mfma_f32_16x16x32_bf16 v[68:71], v[36:39], v[68:71], v[88:91]
	s_waitcnt lgkmcnt(6)
	v_mfma_f32_16x16x32_bf16 v[28:31], v[28:31], v[60:63], v[84:87]
	v_mfma_f32_16x16x32_bf16 v[40:43], v[40:43], v[60:63], v[80:83]
	v_mfma_f32_16x16x32_bf16 v[44:47], v[44:47], v[60:63], v[76:79]
	v_mfma_f32_16x16x32_bf16 v[36:39], v[36:39], v[60:63], v[72:75]
	s_waitcnt vmcnt(11) lgkmcnt(5)
	v_mfma_f32_16x16x32_bf16 v[60:63], v[8:11], v[64:67], v[100:103]
	s_waitcnt vmcnt(10)
	v_mfma_f32_16x16x32_bf16 v[72:75], v[20:23], v[64:67], v[96:99]
	s_waitcnt vmcnt(9)
	v_mfma_f32_16x16x32_bf16 v[76:79], v[32:35], v[64:67], v[92:95]
	s_waitcnt vmcnt(8)
	v_mfma_f32_16x16x32_bf16 v[64:67], v[24:27], v[64:67], v[68:71]
	s_waitcnt lgkmcnt(4)
	v_mfma_f32_16x16x32_bf16 v[8:11], v[8:11], v[56:59], v[28:31]
	v_mfma_f32_16x16x32_bf16 v[20:23], v[20:23], v[56:59], v[40:43]
	v_mfma_f32_16x16x32_bf16 v[28:31], v[32:35], v[56:59], v[44:47]
	v_mfma_f32_16x16x32_bf16 v[24:27], v[24:27], v[56:59], v[36:39]
	s_waitcnt vmcnt(7) lgkmcnt(3)
	v_mfma_f32_16x16x32_bf16 v[32:35], v[0:3], v[52:55], v[60:63]
	s_waitcnt vmcnt(6)
	v_mfma_f32_16x16x32_bf16 v[36:39], v[4:7], v[52:55], v[72:75]
	s_waitcnt vmcnt(5)
	v_mfma_f32_16x16x32_bf16 v[40:43], v[16:19], v[52:55], v[76:79]
	s_waitcnt vmcnt(4)
	v_mfma_f32_16x16x32_bf16 v[44:47], v[12:15], v[52:55], v[64:67]
	s_waitcnt lgkmcnt(2)
	v_mfma_f32_16x16x32_bf16 v[0:3], v[0:3], v[48:51], v[8:11]
	v_mfma_f32_16x16x32_bf16 v[4:7], v[4:7], v[48:51], v[20:23]
	v_mfma_f32_16x16x32_bf16 v[8:11], v[16:19], v[48:51], v[28:31]
	v_mfma_f32_16x16x32_bf16 v[12:15], v[12:15], v[48:51], v[24:27]
	s_waitcnt vmcnt(3) lgkmcnt(1)
	v_mfma_f32_16x16x32_bf16 v[16:19], v[112:115], v[124:127], v[32:35]
	v_readlane_b32 s0, v251, 41
	v_readlane_b32 s1, v251, 42
	s_nop 0
	v_lshlrev_b32_e32 v32, 6, v108
	v_and_b32_e32 v32, 0xc0, v32
	v_add_u32_e32 v32, v32, v109
	s_waitcnt vmcnt(2)
	v_mfma_f32_16x16x32_bf16 v[20:23], v[116:119], v[124:127], v[36:39]
	v_lshrrev_b32_e32 v33, 2, v108
	s_nop 1
	v_and_or_b32 v36, v138, 12, v32
	v_ashrrev_i32_e32 v32, 2, v138
	v_and_or_b32 v32, v32, -4, v33
	v_ashrrev_i32_e32 v33, 31, v32
	ds_bpermute_b32 v16, v36, v16
	ds_bpermute_b32 v17, v36, v17
	ds_bpermute_b32 v18, v36, v18
	ds_bpermute_b32 v19, v36, v19
	v_lshl_add_u64 v[32:33], s[0:1], 0, v[32:33]
	v_readlane_b32 s0, v251, 31
	v_lshlrev_b64 v[32:33], 10, v[32:33]
	v_readlane_b32 s1, v251, 32
	v_lshlrev_b32_e32 v37, 4, v138
	v_and_b32_e32 v172, 48, v37
	v_lshl_add_u64 v[34:35], s[0:1], 0, v[32:33]
	v_lshl_add_u64 v[34:35], v[34:35], 0, v[172:173]
	v_readlane_b32 s0, v251, 33
	s_waitcnt lgkmcnt(0)
	global_store_dwordx4 v[34:35], v[16:19], off sc1
	ds_bpermute_b32 v16, v36, v20
	ds_bpermute_b32 v17, v36, v21
	ds_bpermute_b32 v18, v36, v22
	ds_bpermute_b32 v19, v36, v23
	v_readlane_b32 s1, v251, 34
	s_waitcnt vmcnt(2)
	v_mfma_f32_16x16x32_bf16 v[24:27], v[104:107], v[124:127], v[40:43]
	v_lshl_add_u64 v[20:21], s[0:1], 0, v[32:33]
	v_lshl_add_u64 v[20:21], v[20:21], 0, v[172:173]
	s_mov_b32 s0, 0x4b62b000
	v_add_co_u32_e32 v22, vcc, s0, v20
	s_waitcnt vmcnt(1)
	v_mfma_f32_16x16x32_bf16 v[28:31], v[120:123], v[124:127], v[44:47]
	v_addc_co_u32_e32 v23, vcc, 0, v21, vcc
	s_waitcnt lgkmcnt(0)
	global_store_dwordx4 v[22:23], v[16:19], off offset:1600 sc1
	ds_bpermute_b32 v16, v36, v24
	ds_bpermute_b32 v17, v36, v25
	ds_bpermute_b32 v18, v36, v26
	ds_bpermute_b32 v19, v36, v27
	v_mfma_f32_16x16x32_bf16 v[0:3], v[112:115], v[128:131], v[0:3]
	s_mov_b32 s0, 0x4b62f000
	s_waitcnt lgkmcnt(0)
	global_store_dwordx4 v[22:23], v[16:19], off offset:1664 sc1
	ds_bpermute_b32 v16, v36, v28
	ds_bpermute_b32 v17, v36, v29
	ds_bpermute_b32 v18, v36, v30
	ds_bpermute_b32 v19, v36, v31
	s_nop 0
	ds_bpermute_b32 v0, v36, v0
	ds_bpermute_b32 v1, v36, v1
	ds_bpermute_b32 v2, v36, v2
	ds_bpermute_b32 v3, v36, v3
	v_mfma_f32_16x16x32_bf16 v[4:7], v[116:119], v[128:131], v[4:7]
	s_waitcnt lgkmcnt(4)
	global_store_dwordx4 v[22:23], v[16:19], off offset:1728 sc1
	s_nop 1
	v_add_co_u32_e32 v16, vcc, s2, v34
	v_mfma_f32_16x16x32_bf16 v[8:11], v[104:107], v[128:131], v[8:11]
	s_nop 0
	v_addc_co_u32_e32 v17, vcc, 0, v35, vcc
	s_waitcnt lgkmcnt(0)
	global_store_dwordx4 v[16:17], v[0:3], off sc1
	ds_bpermute_b32 v0, v36, v4
	ds_bpermute_b32 v1, v36, v5
	ds_bpermute_b32 v2, v36, v6
	ds_bpermute_b32 v3, v36, v7
	v_add_co_u32_e32 v4, vcc, s0, v20
	v_mfma_f32_16x16x32_bf16 v[12:15], v[120:123], v[128:131], v[12:15]
	s_nop 0
	v_addc_co_u32_e32 v5, vcc, 0, v21, vcc
	s_waitcnt lgkmcnt(0)
	global_store_dwordx4 v[4:5], v[0:3], off offset:1600 sc1
	ds_bpermute_b32 v0, v36, v8
	ds_bpermute_b32 v1, v36, v9
	ds_bpermute_b32 v2, v36, v10
	ds_bpermute_b32 v3, v36, v11
	s_waitcnt lgkmcnt(0)
	global_store_dwordx4 v[4:5], v[0:3], off offset:1664 sc1
	ds_bpermute_b32 v0, v36, v12
	ds_bpermute_b32 v1, v36, v13
	ds_bpermute_b32 v2, v36, v14
	ds_bpermute_b32 v3, v36, v15
	s_waitcnt lgkmcnt(0)
	global_store_dwordx4 v[4:5], v[0:3], off offset:1728 sc1
	s_waitcnt lgkmcnt(0)
	s_barrier

.LBB0_1102:
	s_or_b64 exec, exec, s[2:3]
	s_waitcnt vmcnt(11)
	v_fmac_f32_e32 v105, v104, v152
	v_fmac_f32_e32 v55, v108, v152
	v_fmac_f32_e32 v53, v114, v152
	v_fmac_f32_e32 v51, v118, v152
	v_fmac_f32_e32 v49, v120, v152
	v_fmac_f32_e32 v47, v122, v152
	v_fmac_f32_e32 v45, v124, v152
	v_fmac_f32_e32 v31, v128, v152
	v_fmac_f32_e32 v29, v130, v152
	v_fmac_f32_e32 v107, v134, v152
	v_fmac_f32_e32 v111, v136, v152
	v_fmac_f32_e32 v113, v140, v152
	v_fmac_f32_e32 v117, v142, v152
	v_fmac_f32_e32 v127, v144, v152
	v_fmac_f32_e32 v139, v146, v152
	v_fmac_f32_e32 v149, v150, v152
	ds_write_b32 v75, v105
	ds_write_b32 v77, v55
	ds_write_b32 v79, v53
	ds_write_b32 v81, v51
	ds_write_b32 v83, v49
	ds_write_b32 v85, v47
	ds_write_b32 v87, v45
	ds_write_b32 v89, v31
	ds_write_b32 v91, v29
	ds_write_b32 v93, v107
	ds_write_b32 v95, v111
	ds_write_b32 v97, v113
	ds_write_b32 v99, v117
	ds_write_b32 v101, v127
	ds_write_b32 v153, v139
	ds_write_b32 v154, v149
	s_waitcnt lgkmcnt(0)
	s_barrier
	ds_read_b128 v[28:31], v71 offset:16384
	ds_read_b128 v[44:47], v71
	ds_read_b128 v[48:51], v71 offset:16
	ds_read_b128 v[52:55], v71 offset:16400
	s_mov_b32 s0, 0x800000
	s_and_b32 s2, s10, 0xffff
	s_waitcnt lgkmcnt(2)
	v_pk_add_f32 v[28:29], v[44:45], v[28:29]
	v_pk_add_f32 v[30:31], v[46:47], v[30:31]
	v_pk_mul_f32 v[44:45], v[28:29], v[28:29]
	v_pk_mul_f32 v[46:47], v[30:31], v[30:31]
	v_add_f32_e32 v44, v44, v45
	s_waitcnt lgkmcnt(0)
	v_pk_add_f32 v[48:49], v[48:49], v[52:53]
	v_add_f32_e32 v44, v44, v46
	v_pk_mul_f32 v[52:53], v[48:49], v[48:49]
	v_add_f32_e32 v44, v44, v47
	v_pk_add_f32 v[50:51], v[50:51], v[54:55]
	v_add_f32_e32 v44, v44, v52
	v_pk_mul_f32 v[54:55], v[50:51], v[50:51]
	v_add_f32_e32 v44, v44, v53
	v_add_f32_e32 v44, v44, v54
	v_add_f32_e32 v44, v44, v55
	s_mul_i32 s2, s2, 0xaaab
	s_lshr_b32 s2, s2, 18
	v_add_f32_dpp v44, v44, v44 quad_perm:[1,0,3,2] row_mask:0xf bank_mask:0xf bound_ctrl:1
	s_mul_i32 s3, s2, 0xe39
	s_lshr_b32 s3, s3, 17
	v_add_f32_dpp v44, v44, v44 quad_perm:[2,3,0,1] row_mask:0xf bank_mask:0xf bound_ctrl:1
	s_mul_i32 s3, s3, 36
	s_bfe_u32 s12, s10, 0xd0003
	v_add_f32_dpp v44, v44, v44 row_half_mirror row_mask:0xf bank_mask:0xf bound_ctrl:1
	v_fmamk_f32 v44, v44, 0x3c800000, v198
	v_mul_f32_e32 v45, 0x4b800000, v44
	v_cmp_gt_f32_e32 vcc, s0, v44
	s_sub_i32 s3, s2, s3
	s_mulk_i32 s12, 0x12f7
	v_cndmask_b32_e32 v44, v44, v45, vcc
	v_rsq_f32_e32 v44, v44
	s_and_b32 s11, s3, 0xffff
	s_lshr_b32 s12, s12, 17
	s_lshl_b32 s3, s3, 6
	v_mul_f32_e32 v45, 0x45800000, v44
	v_cndmask_b32_e32 v44, v44, v45, vcc
	s_waitcnt vmcnt(10)
	v_lshlrev_b32_e32 v45, 16, v0
	v_and_b32_e32 v0, 0xffff0000, v0
	v_mul_f32_e32 v28, v28, v45
	v_mul_f32_e32 v0, v29, v0
	v_mul_f32_e32 v28, v28, v44
	v_mul_f32_e32 v0, v0, v44
	s_waitcnt vmcnt(8)
	v_mul_f32_e32 v8, v8, v28
	v_mul_f32_e32 v0, v9, v0
	v_cvt_pk_bf16_f32 v0, v8, v0
	v_lshlrev_b32_e32 v8, 16, v1
	v_and_b32_e32 v1, 0xffff0000, v1
	v_mul_f32_e32 v8, v30, v8
	v_mul_f32_e32 v1, v31, v1
	v_mul_f32_e32 v8, v8, v44
	v_mul_f32_e32 v1, v1, v44
	v_mul_f32_e32 v8, v10, v8
	v_mul_f32_e32 v1, v11, v1
	v_cvt_pk_bf16_f32 v1, v8, v1
	v_lshlrev_b32_e32 v8, 16, v2
	v_and_b32_e32 v2, 0xffff0000, v2
	v_mul_f32_e32 v8, v48, v8
	v_mul_f32_e32 v2, v49, v2
	v_mul_f32_e32 v8, v8, v44
	v_mul_f32_e32 v2, v2, v44
	v_mul_f32_e32 v4, v4, v8
	v_mul_f32_e32 v2, v5, v2
	s_lshl_b32 s13, s12, 8
	s_lshl_b32 s12, s12, 11
	s_and_b32 s3, s3, 0xffc0
	v_cvt_pk_bf16_f32 v2, v4, v2
	v_lshlrev_b32_e32 v4, 16, v3
	v_and_b32_e32 v3, 0xffff0000, v3
	s_addk_i32 s12, 0x800
	s_add_i32 s14, s3, 0xffffff00
	v_mul_f32_e32 v4, v50, v4
	v_mul_f32_e32 v3, v51, v3
	s_cmp_lt_u32 s11, 4
	v_mul_f32_e32 v4, v4, v44
	v_mul_f32_e32 v3, v3, v44
	s_cselect_b32 s11, s13, s12
	s_cselect_b32 s3, s3, s14
	v_mul_f32_e32 v4, v6, v4
	v_mul_f32_e32 v3, v7, v3
	s_add_i32 s3, s3, s11
	v_cvt_pk_bf16_f32 v3, v4, v3
	s_mul_i32 s2, s2, 6
	v_add_u32_e32 v4, s3, v65
	s_sub_i32 s2, s10, s2
	v_ashrrev_i32_e32 v5, 31, v4
	v_lshlrev_b64 v[4:5], 11, v[4:5]
	s_lshl_b32 s2, s2, 7
	v_lshl_add_u64 v[4:5], s[60:61], 0, v[4:5]
	s_and_b32 s44, s2, 0x1ff80
	v_lshl_add_u64 v[4:5], v[4:5], 0, s[44:45]
	v_lshl_add_u64 v[4:5], v[4:5], 0, v[172:173]
	v_add_co_u32_e32 v4, vcc, 0x4ccab000, v4
	s_waitcnt vmcnt(0)
	v_mov_b64_e32 v[8:9], v[40:41]
	v_addc_co_u32_e32 v5, vcc, 0, v5, vcc
	global_store_dwordx4 v[4:5], v[0:3], off offset:2304 sc1
	s_waitcnt lgkmcnt(0)
	s_barrier
	v_mov_b64_e32 v[4:5], v[36:37]
	v_mov_b64_e32 v[0:1], v[32:33]
	v_mov_b64_e32 v[30:31], v[26:27]
	v_mov_b64_e32 v[46:47], v[22:23]
	v_mov_b64_e32 v[50:51], v[18:19]
	v_mov_b64_e32 v[54:55], v[14:15]
	s_cmp_lt_i32 s1, 0
	s_mov_b32 s10, s1
	v_mov_b64_e32 v[6:7], v[38:39]
	v_mov_b64_e32 v[10:11], v[42:43]
	v_mov_b64_e32 v[2:3], v[34:35]
	v_mov_b32_e32 v152, v103
	v_mov_b64_e32 v[28:29], v[24:25]
	v_mov_b64_e32 v[44:45], v[20:21]
	v_mov_b64_e32 v[48:49], v[16:17]
	v_mov_b64_e32 v[52:53], v[12:13]
	s_cbranch_scc1 .LBB0_1113

.LBB0_1303:
	v_lshl_add_u32 v128, s24, 8, v189
	v_lshl_or_b32 v168, s22, 8, v191
	v_ashrrev_i32_e32 v169, 31, v168
	v_readlane_b32 s28, v250, 7
	v_or_b32_e32 v134, 16, v128
	v_lshlrev_b64 v[162:163], 1, v[168:169]
	v_readlane_b32 s29, v250, 8
	v_ashrrev_i32_e32 v129, 31, v128
	v_ashrrev_i32_e32 v135, 31, v134
	v_lshl_add_u64 v[130:131], s[28:29], 0, v[162:163]
	v_lshlrev_b64 v[174:175], 11, v[128:129]
	v_lshlrev_b64 v[176:177], 11, v[134:135]
	v_lshl_add_u64 v[132:133], v[130:131], 0, v[174:175]
	v_lshl_add_u64 v[134:135], v[130:131], 0, v[176:177]
	global_load_dwordx4 v[204:207], v[132:133], off
	global_load_dwordx4 v[208:211], v[134:135], off
	v_or_b32_e32 v132, 32, v128
	v_or_b32_e32 v134, 48, v128
	v_ashrrev_i32_e32 v133, 31, v132
	v_ashrrev_i32_e32 v135, 31, v134
	v_lshlrev_b64 v[178:179], 11, v[132:133]
	v_lshlrev_b64 v[180:181], 11, v[134:135]
	v_lshl_add_u64 v[132:133], v[130:131], 0, v[178:179]
	v_lshl_add_u64 v[134:135], v[130:131], 0, v[180:181]
	global_load_dwordx4 v[214:217], v[132:133], off
	global_load_dwordx4 v[152:155], v[134:135], off
	s_mov_b64 s[26:27], 0x40000
	v_add_u32_e32 v134, 0x90, v128
	v_lshl_add_u64 v[182:183], v[174:175], 0, s[26:27]
	v_ashrrev_i32_e32 v135, 31, v134
	v_lshl_add_u64 v[132:133], v[130:131], 0, v[182:183]
	v_lshlrev_b64 v[170:171], 11, v[134:135]
	v_lshl_add_u64 v[134:135], v[130:131], 0, v[170:171]
	global_load_dwordx4 v[148:151], v[132:133], off
	global_load_dwordx4 v[144:147], v[134:135], off
	v_add_u32_e32 v132, 0xa0, v128
	v_add_u32_e32 v128, 0xb0, v128
	v_ashrrev_i32_e32 v133, 31, v132
	v_ashrrev_i32_e32 v129, 31, v128
	v_lshlrev_b64 v[166:167], 11, v[132:133]
	v_lshlrev_b64 v[164:165], 11, v[128:129]
	v_lshl_add_u64 v[132:133], v[130:131], 0, v[166:167]
	v_lshl_add_u64 v[128:129], v[130:131], 0, v[164:165]
	global_load_dwordx4 v[140:143], v[132:133], off
	s_nop 0
	global_load_dwordx4 v[128:131], v[128:129], off
	s_mul_hi_u32 s9, s91, 0xaaaaaaab
	s_lshr_b32 s9, s9, 1
	s_mul_i32 s9, s9, 3
	s_sub_i32 s9, s91, s9
	v_lshl_add_u32 v169, s9, 10, v190
	ds_read_b128 v[136:139], v169
	ds_read_b128 v[132:135], v169 offset:16
	s_waitcnt lgkmcnt(0)
	v_pk_mul_f32 v[124:125], v[124:125], v[136:137]
	v_pk_mul_f32 v[126:127], v[126:127], v[138:139]
	v_pk_mul_f32 v[120:121], v[120:121], v[132:133]
	ds_bpermute_b32 v124, v188, v124
	ds_bpermute_b32 v125, v188, v125
	v_pk_mul_f32 v[122:123], v[122:123], v[134:135]
	ds_bpermute_b32 v126, v188, v126
	ds_bpermute_b32 v127, v188, v127
	ds_bpermute_b32 v120, v188, v120
	ds_bpermute_b32 v121, v188, v121
	ds_bpermute_b32 v122, v188, v122
	ds_bpermute_b32 v123, v188, v123
	s_waitcnt vmcnt(0)
	v_lshlrev_b32_e32 v196, 16, v204
	v_and_b32_e32 v197, 0xffff0000, v204
	v_pk_mul_f32 v[116:117], v[116:117], v[136:137]
	v_lshlrev_b32_e32 v204, 16, v205
	v_and_b32_e32 v205, 0xffff0000, v205
	s_waitcnt lgkmcnt(6)
	v_pk_add_f32 v[124:125], v[196:197], v[124:125]
	v_lshlrev_b32_e32 v196, 16, v206
	v_and_b32_e32 v197, 0xffff0000, v206
	v_readlane_b32 s26, v250, 5
	v_pk_mul_f32 v[118:119], v[118:119], v[138:139]
	v_pk_mul_f32 v[112:113], v[112:113], v[132:133]
	ds_bpermute_b32 v116, v188, v116
	ds_bpermute_b32 v117, v188, v117
	s_waitcnt lgkmcnt(6)
	v_pk_add_f32 v[126:127], v[204:205], v[126:127]
	v_lshlrev_b32_e32 v204, 16, v207
	v_and_b32_e32 v205, 0xffff0000, v207
	s_waitcnt lgkmcnt(4)
	v_pk_add_f32 v[120:121], v[196:197], v[120:121]
	v_readlane_b32 s27, v250, 6
	v_pk_mul_f32 v[114:115], v[114:115], v[134:135]
	ds_bpermute_b32 v118, v188, v118
	ds_bpermute_b32 v119, v188, v119
	ds_bpermute_b32 v112, v188, v112
	ds_bpermute_b32 v113, v188, v113
	s_waitcnt lgkmcnt(6)
	v_pk_add_f32 v[204:205], v[204:205], v[122:123]
	v_cvt_pk_bf16_f32 v122, v124, v125
	v_cvt_pk_bf16_f32 v124, v120, v121
	v_lshl_add_u64 v[120:121], s[26:27], 0, v[174:175]
	ds_bpermute_b32 v114, v188, v114
	ds_bpermute_b32 v115, v188, v115
	v_cvt_pk_bf16_f32 v123, v126, v127
	v_lshl_add_u64 v[120:121], v[120:121], 0, v[162:163]
	v_cvt_pk_bf16_f32 v125, v204, v205
	global_store_dwordx4 v[120:121], v[122:125], off sc1
	v_pk_mul_f32 v[108:109], v[108:109], v[136:137]
	v_pk_mul_f32 v[110:111], v[110:111], v[138:139]
	v_lshlrev_b32_e32 v122, 16, v208
	v_and_b32_e32 v123, 0xffff0000, v208
	v_lshlrev_b32_e32 v124, 16, v209
	v_and_b32_e32 v125, 0xffff0000, v209
	s_waitcnt lgkmcnt(6)
	v_pk_add_f32 v[116:117], v[122:123], v[116:117]
	v_lshlrev_b32_e32 v122, 16, v210
	v_and_b32_e32 v123, 0xffff0000, v210
	v_pk_mul_f32 v[104:105], v[104:105], v[132:133]
	ds_bpermute_b32 v108, v188, v108
	ds_bpermute_b32 v109, v188, v109
	s_waitcnt lgkmcnt(6)
	v_pk_add_f32 v[118:119], v[124:125], v[118:119]
	v_lshlrev_b32_e32 v124, 16, v211
	v_and_b32_e32 v125, 0xffff0000, v211
	s_waitcnt lgkmcnt(4)
	v_pk_add_f32 v[112:113], v[122:123], v[112:113]
	v_pk_mul_f32 v[106:107], v[106:107], v[134:135]
	ds_bpermute_b32 v110, v188, v110
	ds_bpermute_b32 v111, v188, v111
	ds_bpermute_b32 v104, v188, v104
	ds_bpermute_b32 v105, v188, v105
	s_waitcnt lgkmcnt(6)
	v_pk_add_f32 v[124:125], v[124:125], v[114:115]
	v_cvt_pk_bf16_f32 v114, v116, v117
	v_cvt_pk_bf16_f32 v116, v112, v113
	v_lshl_add_u64 v[112:113], s[26:27], 0, v[176:177]
	ds_bpermute_b32 v106, v188, v106
	ds_bpermute_b32 v107, v188, v107
	v_cvt_pk_bf16_f32 v115, v118, v119
	v_lshl_add_u64 v[112:113], v[112:113], 0, v[162:163]
	v_cvt_pk_bf16_f32 v117, v124, v125
	global_store_dwordx4 v[112:113], v[114:117], off sc1
	v_pk_mul_f32 v[102:103], v[102:103], v[138:139]
	v_pk_mul_f32 v[100:101], v[100:101], v[136:137]
	v_lshlrev_b32_e32 v114, 16, v214
	v_and_b32_e32 v115, 0xffff0000, v214
	v_lshlrev_b32_e32 v116, 16, v215
	v_and_b32_e32 v117, 0xffff0000, v215
	s_waitcnt lgkmcnt(6)
	v_pk_add_f32 v[108:109], v[114:115], v[108:109]
	v_lshlrev_b32_e32 v114, 16, v216
	v_and_b32_e32 v115, 0xffff0000, v216
	v_pk_mul_f32 v[98:99], v[98:99], v[134:135]
	v_pk_mul_f32 v[96:97], v[96:97], v[132:133]
	ds_bpermute_b32 v100, v188, v100
	ds_bpermute_b32 v101, v188, v101
	ds_bpermute_b32 v102, v188, v102
	ds_bpermute_b32 v103, v188, v103
	s_waitcnt lgkmcnt(8)
	v_pk_add_f32 v[110:111], v[116:117], v[110:111]
	v_lshlrev_b32_e32 v116, 16, v217
	v_and_b32_e32 v117, 0xffff0000, v217
	s_waitcnt lgkmcnt(6)
	v_pk_add_f32 v[104:105], v[114:115], v[104:105]
	ds_bpermute_b32 v96, v188, v96
	ds_bpermute_b32 v97, v188, v97
	ds_bpermute_b32 v98, v188, v98
	ds_bpermute_b32 v99, v188, v99
	s_waitcnt lgkmcnt(8)
	v_pk_add_f32 v[116:117], v[116:117], v[106:107]
	v_cvt_pk_bf16_f32 v106, v108, v109
	v_cvt_pk_bf16_f32 v108, v104, v105
	v_lshl_add_u64 v[104:105], s[26:27], 0, v[178:179]
	v_cvt_pk_bf16_f32 v107, v110, v111
	v_cvt_pk_bf16_f32 v109, v116, v117
	v_lshl_add_u64 v[104:105], v[104:105], 0, v[162:163]
	v_pk_mul_f32 v[94:95], v[94:95], v[138:139]
	v_pk_mul_f32 v[92:93], v[92:93], v[136:137]
	global_store_dwordx4 v[104:105], v[106:109], off sc1
	v_pk_mul_f32 v[90:91], v[90:91], v[134:135]
	v_pk_mul_f32 v[88:89], v[88:89], v[132:133]
	v_lshlrev_b32_e32 v106, 16, v152
	v_and_b32_e32 v107, 0xffff0000, v152
	v_lshlrev_b32_e32 v108, 16, v153
	v_and_b32_e32 v109, 0xffff0000, v153
	ds_bpermute_b32 v92, v188, v92
	ds_bpermute_b32 v93, v188, v93
	ds_bpermute_b32 v94, v188, v94
	ds_bpermute_b32 v95, v188, v95
	s_waitcnt lgkmcnt(8)
	v_pk_add_f32 v[102:103], v[108:109], v[102:103]
	v_pk_add_f32 v[100:101], v[106:107], v[100:101]
	v_lshlrev_b32_e32 v106, 16, v154
	v_and_b32_e32 v107, 0xffff0000, v154
	v_lshlrev_b32_e32 v108, 16, v155
	v_and_b32_e32 v109, 0xffff0000, v155
	ds_bpermute_b32 v88, v188, v88
	ds_bpermute_b32 v89, v188, v89
	ds_bpermute_b32 v90, v188, v90
	ds_bpermute_b32 v91, v188, v91
	s_waitcnt lgkmcnt(8)
	v_pk_add_f32 v[108:109], v[108:109], v[98:99]
	v_pk_add_f32 v[98:99], v[106:107], v[96:97]
	v_cvt_pk_bf16_f32 v96, v100, v101
	v_lshl_add_u64 v[100:101], s[26:27], 0, v[180:181]
	v_cvt_pk_bf16_f32 v97, v102, v103
	v_cvt_pk_bf16_f32 v98, v98, v99
	v_cvt_pk_bf16_f32 v99, v108, v109
	v_lshl_add_u64 v[106:107], v[100:101], 0, v[162:163]
	global_store_dwordx4 v[106:107], v[96:99], off sc1
	v_pk_mul_f32 v[80:81], v[80:81], v[132:133]
	ds_bpermute_b32 v126, v188, v80
	v_lshlrev_b32_e32 v96, 16, v148
	v_and_b32_e32 v97, 0xffff0000, v148
	v_lshlrev_b32_e32 v98, 16, v149
	v_and_b32_e32 v99, 0xffff0000, v149
	s_waitcnt lgkmcnt(5)
	v_pk_add_f32 v[94:95], v[98:99], v[94:95]
	v_pk_add_f32 v[92:93], v[96:97], v[92:93]
	v_lshlrev_b32_e32 v96, 16, v150
	v_and_b32_e32 v97, 0xffff0000, v150
	v_lshlrev_b32_e32 v98, 16, v151
	v_and_b32_e32 v99, 0xffff0000, v151
	v_or_b32_e32 v80, 0x80, v168
	s_waitcnt lgkmcnt(1)
	v_pk_add_f32 v[98:99], v[98:99], v[90:91]
	v_pk_add_f32 v[90:91], v[96:97], v[88:89]
	v_cvt_pk_bf16_f32 v88, v92, v93
	v_lshl_add_u64 v[92:93], s[26:27], 0, v[182:183]
	v_pk_mul_f32 v[84:85], v[84:85], v[136:137]
	v_pk_mul_f32 v[82:83], v[82:83], v[134:135]
	ds_bpermute_b32 v127, v188, v81
	v_ashrrev_i32_e32 v81, 31, v80
	v_lshl_add_u64 v[108:109], v[92:93], 0, v[162:163]
	ds_bpermute_b32 v110, v188, v84
	ds_bpermute_b32 v111, v188, v85
	ds_bpermute_b32 v148, v188, v82
	ds_bpermute_b32 v149, v188, v83
	v_lshl_add_u64 v[82:83], s[28:29], 0, v[174:175]
	v_lshlrev_b64 v[80:81], 1, v[80:81]
	v_lshl_add_u64 v[84:85], s[28:29], 0, v[176:177]
	v_cvt_pk_bf16_f32 v89, v94, v95
	v_cvt_pk_bf16_f32 v90, v90, v91
	v_cvt_pk_bf16_f32 v91, v98, v99
	global_store_dwordx4 v[108:109], v[88:91], off sc1
	v_lshl_add_u64 v[82:83], v[82:83], 0, v[80:81]
	v_lshl_add_u64 v[84:85], v[84:85], 0, v[80:81]
	global_load_dwordx4 v[114:117], v[82:83], off
	global_load_dwordx4 v[122:125], v[84:85], off
	v_lshl_add_u64 v[82:83], s[28:29], 0, v[178:179]
	v_lshl_add_u64 v[84:85], s[28:29], 0, v[180:181]
	v_lshl_add_u64 v[82:83], v[82:83], 0, v[80:81]
	v_lshl_add_u64 v[84:85], v[84:85], 0, v[80:81]
	global_load_dwordx4 v[100:103], v[82:83], off
	global_load_dwordx4 v[96:99], v[84:85], off
	v_lshl_add_u64 v[82:83], s[28:29], 0, v[182:183]
	v_lshl_add_u64 v[84:85], s[28:29], 0, v[170:171]
	v_lshl_add_u64 v[82:83], v[82:83], 0, v[80:81]
	v_lshl_add_u64 v[84:85], v[84:85], 0, v[80:81]
	global_load_dwordx4 v[92:95], v[82:83], off
	global_load_dwordx4 v[88:91], v[84:85], off
	v_lshl_add_u64 v[82:83], s[28:29], 0, v[166:167]
	v_lshl_add_u64 v[84:85], s[28:29], 0, v[164:165]
	v_pk_mul_f32 v[86:87], v[86:87], v[138:139]
	v_lshl_add_u64 v[82:83], v[82:83], 0, v[80:81]
	v_lshl_add_u64 v[80:81], v[84:85], 0, v[80:81]
	ds_bpermute_b32 v118, v188, v86
	ds_bpermute_b32 v119, v188, v87
	global_load_dwordx4 v[84:87], v[82:83], off
	s_nop 0
	global_load_dwordx4 v[80:83], v[80:81], off
	v_pk_mul_f32 v[76:77], v[76:77], v[136:137]
	v_pk_mul_f32 v[78:79], v[78:79], v[138:139]
	v_pk_mul_f32 v[72:73], v[72:73], v[132:133]
	ds_bpermute_b32 v76, v188, v76
	ds_bpermute_b32 v77, v188, v77
	v_pk_mul_f32 v[74:75], v[74:75], v[134:135]
	ds_bpermute_b32 v78, v188, v78
	ds_bpermute_b32 v79, v188, v79
	ds_bpermute_b32 v72, v188, v72
	ds_bpermute_b32 v73, v188, v73
	v_lshlrev_b32_e32 v150, 16, v144
	v_and_b32_e32 v151, 0xffff0000, v144
	v_lshlrev_b32_e32 v144, 16, v145
	v_and_b32_e32 v145, 0xffff0000, v145
	ds_bpermute_b32 v74, v188, v74
	ds_bpermute_b32 v75, v188, v75
	s_waitcnt lgkmcnt(8)
	v_pk_add_f32 v[118:119], v[144:145], v[118:119]
	v_lshlrev_b32_e32 v144, 16, v146
	v_and_b32_e32 v145, 0xffff0000, v146
	v_pk_mul_f32 v[60:61], v[60:61], v[136:137]
	v_lshlrev_b32_e32 v146, 16, v147
	v_and_b32_e32 v147, 0xffff0000, v147
	v_pk_add_f32 v[126:127], v[144:145], v[126:127]
	v_cvt_pk_bf16_f32 v145, v118, v119
	v_lshlrev_b32_e32 v118, 16, v140
	v_and_b32_e32 v119, 0xffff0000, v140
	v_pk_mul_f32 v[62:63], v[62:63], v[138:139]
	v_pk_mul_f32 v[56:57], v[56:57], v[132:133]
	ds_bpermute_b32 v60, v188, v60
	ds_bpermute_b32 v61, v188, v61
	v_pk_add_f32 v[148:149], v[146:147], v[148:149]
	v_cvt_pk_bf16_f32 v146, v126, v127
	v_lshlrev_b32_e32 v126, 16, v141
	v_and_b32_e32 v127, 0xffff0000, v141
	s_waitcnt lgkmcnt(8)
	v_pk_add_f32 v[76:77], v[118:119], v[76:77]
	v_lshlrev_b32_e32 v118, 16, v142
	v_and_b32_e32 v119, 0xffff0000, v142
	v_pk_mul_f32 v[58:59], v[58:59], v[134:135]
	ds_bpermute_b32 v62, v188, v62
	ds_bpermute_b32 v63, v188, v63
	ds_bpermute_b32 v56, v188, v56
	ds_bpermute_b32 v57, v188, v57
	s_waitcnt lgkmcnt(10)
	v_pk_add_f32 v[78:79], v[126:127], v[78:79]
	v_lshlrev_b32_e32 v126, 16, v143
	v_and_b32_e32 v127, 0xffff0000, v143
	s_waitcnt lgkmcnt(8)
	v_pk_add_f32 v[72:73], v[118:119], v[72:73]
	ds_bpermute_b32 v58, v188, v58
	ds_bpermute_b32 v59, v188, v59
	v_pk_add_f32 v[110:111], v[150:151], v[110:111]
	s_waitcnt lgkmcnt(8)
	v_pk_add_f32 v[74:75], v[126:127], v[74:75]
	v_cvt_pk_bf16_f32 v76, v76, v77
	v_cvt_pk_bf16_f32 v77, v78, v79
	v_cvt_pk_bf16_f32 v78, v72, v73
	v_lshl_add_u64 v[72:73], s[26:27], 0, v[166:167]
	v_cvt_pk_bf16_f32 v144, v110, v111
	v_lshl_add_u64 v[110:111], s[26:27], 0, v[170:171]
	v_cvt_pk_bf16_f32 v79, v74, v75
	v_lshl_add_u64 v[74:75], v[72:73], 0, v[162:163]
	v_lshlrev_b32_e32 v72, 16, v128
	v_and_b32_e32 v73, 0xffff0000, v128
	v_lshl_add_u64 v[110:111], v[110:111], 0, v[162:163]
	global_store_dwordx4 v[74:75], v[76:79], off sc1
	s_waitcnt lgkmcnt(6)
	v_pk_add_f32 v[60:61], v[72:73], v[60:61]
	v_lshlrev_b32_e32 v72, 16, v130
	v_lshlrev_b32_e32 v76, 16, v129
	v_and_b32_e32 v77, 0xffff0000, v129
	v_and_b32_e32 v73, 0xffff0000, v130
	v_cvt_pk_bf16_f32 v147, v148, v149
	global_store_dwordx4 v[110:111], v[144:147], off sc1
	s_waitcnt lgkmcnt(4)
	v_pk_add_f32 v[62:63], v[76:77], v[62:63]
	v_lshlrev_b32_e32 v76, 16, v131
	v_and_b32_e32 v77, 0xffff0000, v131
	s_waitcnt lgkmcnt(2)
	v_pk_add_f32 v[56:57], v[72:73], v[56:57]
	s_waitcnt lgkmcnt(0)
	v_pk_add_f32 v[118:119], v[76:77], v[58:59]
	v_cvt_pk_bf16_f32 v76, v60, v61
	v_cvt_pk_bf16_f32 v77, v62, v63
	v_cvt_pk_bf16_f32 v78, v56, v57
	ds_read_b128 v[60:63], v169 offset:512
	ds_read_b128 v[56:59], v169 offset:528
	v_lshl_add_u64 v[72:73], s[26:27], 0, v[164:165]
	v_lshl_add_u64 v[72:73], v[72:73], 0, v[162:163]
	v_cvt_pk_bf16_f32 v79, v118, v119
	global_store_dwordx4 v[72:73], v[76:79], off sc1
	s_waitcnt lgkmcnt(1)
	v_pk_mul_f32 v[70:71], v[70:71], v[62:63]
	v_pk_mul_f32 v[68:69], v[68:69], v[60:61]
	s_waitcnt lgkmcnt(0)
	v_pk_mul_f32 v[66:67], v[66:67], v[58:59]
	v_pk_mul_f32 v[64:65], v[64:65], v[56:57]
	ds_bpermute_b32 v68, v188, v68
	ds_bpermute_b32 v69, v188, v69
	ds_bpermute_b32 v70, v188, v70
	ds_bpermute_b32 v71, v188, v71
	ds_bpermute_b32 v64, v188, v64
	ds_bpermute_b32 v65, v188, v65
	ds_bpermute_b32 v66, v188, v66
	ds_bpermute_b32 v67, v188, v67
	v_pk_mul_f32 v[54:55], v[54:55], v[62:63]
	v_pk_mul_f32 v[52:53], v[52:53], v[60:61]
	s_waitcnt vmcnt(10)
	v_lshlrev_b32_e32 v76, 16, v114
	v_and_b32_e32 v77, 0xffff0000, v114
	v_lshlrev_b32_e32 v78, 16, v115
	v_and_b32_e32 v79, 0xffff0000, v115
	v_pk_mul_f32 v[50:51], v[50:51], v[58:59]
	v_pk_mul_f32 v[48:49], v[48:49], v[56:57]
	ds_bpermute_b32 v52, v188, v52
	ds_bpermute_b32 v53, v188, v53
	ds_bpermute_b32 v54, v188, v54
	ds_bpermute_b32 v55, v188, v55
	s_waitcnt lgkmcnt(8)
	v_pk_add_f32 v[70:71], v[78:79], v[70:71]
	v_pk_add_f32 v[68:69], v[76:77], v[68:69]
	v_lshlrev_b32_e32 v76, 16, v116
	v_and_b32_e32 v77, 0xffff0000, v116
	v_lshlrev_b32_e32 v78, 16, v117
	v_and_b32_e32 v79, 0xffff0000, v117
	ds_bpermute_b32 v48, v188, v48
	ds_bpermute_b32 v49, v188, v49
	ds_bpermute_b32 v50, v188, v50
	ds_bpermute_b32 v51, v188, v51
	s_waitcnt lgkmcnt(8)
	v_pk_add_f32 v[78:79], v[78:79], v[66:67]
	v_pk_add_f32 v[66:67], v[76:77], v[64:65]
	v_cvt_pk_bf16_f32 v64, v68, v69
	v_cvt_pk_bf16_f32 v65, v70, v71
	v_pk_mul_f32 v[46:47], v[46:47], v[62:63]
	v_cvt_pk_bf16_f32 v66, v66, v67
	v_cvt_pk_bf16_f32 v67, v78, v79
	v_pk_mul_f32 v[44:45], v[44:45], v[60:61]
	global_store_dwordx4 v[120:121], v[64:67], off offset:256 sc1
	v_pk_mul_f32 v[42:43], v[42:43], v[58:59]
	v_pk_mul_f32 v[40:41], v[40:41], v[56:57]
	s_waitcnt vmcnt(10)
	v_lshlrev_b32_e32 v64, 16, v122
	v_and_b32_e32 v65, 0xffff0000, v122
	v_lshlrev_b32_e32 v66, 16, v123
	v_and_b32_e32 v67, 0xffff0000, v123
	ds_bpermute_b32 v44, v188, v44
	ds_bpermute_b32 v45, v188, v45
	ds_bpermute_b32 v46, v188, v46
	ds_bpermute_b32 v47, v188, v47
	s_waitcnt lgkmcnt(8)
	v_pk_add_f32 v[54:55], v[66:67], v[54:55]
	v_pk_add_f32 v[52:53], v[64:65], v[52:53]
	v_lshlrev_b32_e32 v64, 16, v124
	v_and_b32_e32 v65, 0xffff0000, v124
	v_lshlrev_b32_e32 v66, 16, v125
	v_and_b32_e32 v67, 0xffff0000, v125
	ds_bpermute_b32 v40, v188, v40
	ds_bpermute_b32 v41, v188, v41
	ds_bpermute_b32 v42, v188, v42
	ds_bpermute_b32 v43, v188, v43
	s_waitcnt lgkmcnt(8)
	v_pk_add_f32 v[66:67], v[66:67], v[50:51]
	v_pk_add_f32 v[50:51], v[64:65], v[48:49]
	v_cvt_pk_bf16_f32 v48, v52, v53
	v_cvt_pk_bf16_f32 v49, v54, v55
	v_pk_mul_f32 v[38:39], v[38:39], v[62:63]
	v_cvt_pk_bf16_f32 v50, v50, v51
	v_cvt_pk_bf16_f32 v51, v66, v67
	v_pk_mul_f32 v[36:37], v[36:37], v[60:61]
	global_store_dwordx4 v[112:113], v[48:51], off offset:256 sc1
	v_pk_mul_f32 v[34:35], v[34:35], v[58:59]
	v_pk_mul_f32 v[32:33], v[32:33], v[56:57]
	s_waitcnt vmcnt(10)
	v_lshlrev_b32_e32 v48, 16, v100
	v_and_b32_e32 v49, 0xffff0000, v100
	v_lshlrev_b32_e32 v50, 16, v101
	v_and_b32_e32 v51, 0xffff0000, v101
	ds_bpermute_b32 v36, v188, v36
	ds_bpermute_b32 v37, v188, v37
	ds_bpermute_b32 v38, v188, v38
	ds_bpermute_b32 v39, v188, v39
	s_waitcnt lgkmcnt(8)
	v_pk_add_f32 v[46:47], v[50:51], v[46:47]
	v_pk_add_f32 v[44:45], v[48:49], v[44:45]
	v_lshlrev_b32_e32 v48, 16, v102
	v_and_b32_e32 v49, 0xffff0000, v102
	v_lshlrev_b32_e32 v50, 16, v103
	v_and_b32_e32 v51, 0xffff0000, v103
	ds_bpermute_b32 v32, v188, v32
	ds_bpermute_b32 v33, v188, v33
	ds_bpermute_b32 v34, v188, v34
	ds_bpermute_b32 v35, v188, v35
	s_waitcnt lgkmcnt(8)
	v_pk_add_f32 v[50:51], v[50:51], v[42:43]
	v_pk_add_f32 v[42:43], v[48:49], v[40:41]
	v_cvt_pk_bf16_f32 v40, v44, v45
	v_cvt_pk_bf16_f32 v41, v46, v47
	v_pk_mul_f32 v[30:31], v[30:31], v[62:63]
	v_cvt_pk_bf16_f32 v42, v42, v43
	v_cvt_pk_bf16_f32 v43, v50, v51
	v_pk_mul_f32 v[28:29], v[28:29], v[60:61]
	global_store_dwordx4 v[104:105], v[40:43], off offset:256 sc1
	v_pk_mul_f32 v[26:27], v[26:27], v[58:59]
	v_pk_mul_f32 v[24:25], v[24:25], v[56:57]
	s_waitcnt vmcnt(10)
	v_lshlrev_b32_e32 v40, 16, v96
	v_and_b32_e32 v41, 0xffff0000, v96
	v_lshlrev_b32_e32 v42, 16, v97
	v_and_b32_e32 v43, 0xffff0000, v97
	ds_bpermute_b32 v28, v188, v28
	ds_bpermute_b32 v29, v188, v29
	ds_bpermute_b32 v30, v188, v30
	ds_bpermute_b32 v31, v188, v31
	s_waitcnt lgkmcnt(8)
	v_pk_add_f32 v[38:39], v[42:43], v[38:39]
	v_pk_add_f32 v[36:37], v[40:41], v[36:37]
	v_lshlrev_b32_e32 v40, 16, v98
	v_and_b32_e32 v41, 0xffff0000, v98
	v_lshlrev_b32_e32 v42, 16, v99
	v_and_b32_e32 v43, 0xffff0000, v99
	ds_bpermute_b32 v24, v188, v24
	ds_bpermute_b32 v25, v188, v25
	ds_bpermute_b32 v26, v188, v26
	ds_bpermute_b32 v27, v188, v27
	s_waitcnt lgkmcnt(8)
	v_pk_add_f32 v[42:43], v[42:43], v[34:35]
	v_pk_add_f32 v[34:35], v[40:41], v[32:33]
	v_cvt_pk_bf16_f32 v32, v36, v37
	v_cvt_pk_bf16_f32 v33, v38, v39
	v_pk_mul_f32 v[22:23], v[22:23], v[62:63]
	v_cvt_pk_bf16_f32 v34, v34, v35
	v_cvt_pk_bf16_f32 v35, v42, v43
	v_pk_mul_f32 v[20:21], v[20:21], v[60:61]
	global_store_dwordx4 v[106:107], v[32:35], off offset:256 sc1
	v_pk_mul_f32 v[18:19], v[18:19], v[58:59]
	v_pk_mul_f32 v[16:17], v[16:17], v[56:57]
	s_waitcnt vmcnt(10)
	v_lshlrev_b32_e32 v32, 16, v92
	v_and_b32_e32 v33, 0xffff0000, v92
	v_lshlrev_b32_e32 v34, 16, v93
	v_and_b32_e32 v35, 0xffff0000, v93
	ds_bpermute_b32 v20, v188, v20
	ds_bpermute_b32 v21, v188, v21
	ds_bpermute_b32 v22, v188, v22
	ds_bpermute_b32 v23, v188, v23
	s_waitcnt lgkmcnt(8)
	v_pk_add_f32 v[30:31], v[34:35], v[30:31]
	v_pk_add_f32 v[28:29], v[32:33], v[28:29]
	v_lshlrev_b32_e32 v32, 16, v94
	v_and_b32_e32 v33, 0xffff0000, v94
	v_lshlrev_b32_e32 v34, 16, v95
	v_and_b32_e32 v35, 0xffff0000, v95
	ds_bpermute_b32 v16, v188, v16
	ds_bpermute_b32 v17, v188, v17
	ds_bpermute_b32 v18, v188, v18
	ds_bpermute_b32 v19, v188, v19
	s_waitcnt lgkmcnt(8)
	v_pk_add_f32 v[34:35], v[34:35], v[26:27]
	v_pk_add_f32 v[26:27], v[32:33], v[24:25]
	v_cvt_pk_bf16_f32 v24, v28, v29
	v_cvt_pk_bf16_f32 v25, v30, v31
	v_pk_mul_f32 v[14:15], v[14:15], v[62:63]
	v_cvt_pk_bf16_f32 v26, v26, v27
	v_cvt_pk_bf16_f32 v27, v34, v35
	v_pk_mul_f32 v[12:13], v[12:13], v[60:61]
	global_store_dwordx4 v[108:109], v[24:27], off offset:256 sc1
	v_pk_mul_f32 v[10:11], v[10:11], v[58:59]
	v_pk_mul_f32 v[8:9], v[8:9], v[56:57]
	s_waitcnt vmcnt(10)
	v_lshlrev_b32_e32 v24, 16, v88
	v_and_b32_e32 v25, 0xffff0000, v88
	v_lshlrev_b32_e32 v26, 16, v89
	v_and_b32_e32 v27, 0xffff0000, v89
	ds_bpermute_b32 v12, v188, v12
	ds_bpermute_b32 v13, v188, v13
	ds_bpermute_b32 v14, v188, v14
	ds_bpermute_b32 v15, v188, v15
	s_waitcnt lgkmcnt(8)
	v_pk_add_f32 v[22:23], v[26:27], v[22:23]
	v_pk_add_f32 v[20:21], v[24:25], v[20:21]
	v_lshlrev_b32_e32 v24, 16, v90
	v_and_b32_e32 v25, 0xffff0000, v90
	v_lshlrev_b32_e32 v26, 16, v91
	v_and_b32_e32 v27, 0xffff0000, v91
	ds_bpermute_b32 v8, v188, v8
	ds_bpermute_b32 v9, v188, v9
	ds_bpermute_b32 v10, v188, v10
	ds_bpermute_b32 v11, v188, v11
	s_waitcnt lgkmcnt(8)
	v_pk_add_f32 v[26:27], v[26:27], v[18:19]
	v_pk_add_f32 v[18:19], v[24:25], v[16:17]
	v_cvt_pk_bf16_f32 v16, v20, v21
	v_cvt_pk_bf16_f32 v17, v22, v23
	v_pk_mul_f32 v[6:7], v[6:7], v[62:63]
	v_cvt_pk_bf16_f32 v18, v18, v19
	v_cvt_pk_bf16_f32 v19, v26, v27
	v_pk_mul_f32 v[4:5], v[4:5], v[60:61]
	global_store_dwordx4 v[110:111], v[16:19], off offset:256 sc1
	v_pk_mul_f32 v[2:3], v[2:3], v[58:59]
	v_pk_mul_f32 v[0:1], v[0:1], v[56:57]
	s_waitcnt vmcnt(10)
	v_lshlrev_b32_e32 v16, 16, v84
	v_and_b32_e32 v17, 0xffff0000, v84
	v_lshlrev_b32_e32 v18, 16, v85
	v_and_b32_e32 v19, 0xffff0000, v85
	ds_bpermute_b32 v4, v188, v4
	ds_bpermute_b32 v5, v188, v5
	ds_bpermute_b32 v6, v188, v6
	ds_bpermute_b32 v7, v188, v7
	s_waitcnt lgkmcnt(8)
	v_pk_add_f32 v[14:15], v[18:19], v[14:15]
	v_pk_add_f32 v[12:13], v[16:17], v[12:13]
	v_lshlrev_b32_e32 v16, 16, v86
	v_and_b32_e32 v17, 0xffff0000, v86
	v_lshlrev_b32_e32 v18, 16, v87
	v_and_b32_e32 v19, 0xffff0000, v87
	ds_bpermute_b32 v0, v188, v0
	ds_bpermute_b32 v1, v188, v1
	ds_bpermute_b32 v2, v188, v2
	ds_bpermute_b32 v3, v188, v3
	s_waitcnt lgkmcnt(8)
	v_pk_add_f32 v[18:19], v[18:19], v[10:11]
	v_pk_add_f32 v[10:11], v[16:17], v[8:9]
	v_cvt_pk_bf16_f32 v8, v12, v13
	v_cvt_pk_bf16_f32 v9, v14, v15
	s_and_b64 vcc, exec, s[20:21]
	v_cvt_pk_bf16_f32 v10, v10, v11
	v_cvt_pk_bf16_f32 v11, v18, v19
	global_store_dwordx4 v[74:75], v[8:11], off offset:256 sc1
	v_mov_b32_e32 v132, v195
	v_mov_b32_e32 v128, v193
	s_waitcnt vmcnt(10)
	v_lshlrev_b32_e32 v8, 16, v80
	v_and_b32_e32 v9, 0xffff0000, v80
	v_lshlrev_b32_e32 v10, 16, v81
	v_and_b32_e32 v11, 0xffff0000, v81
	s_waitcnt lgkmcnt(4)
	v_pk_add_f32 v[6:7], v[10:11], v[6:7]
	v_pk_add_f32 v[4:5], v[8:9], v[4:5]
	v_lshlrev_b32_e32 v8, 16, v82
	v_and_b32_e32 v9, 0xffff0000, v82
	v_lshlrev_b32_e32 v10, 16, v83
	v_and_b32_e32 v11, 0xffff0000, v83
	s_waitcnt lgkmcnt(0)
	v_pk_add_f32 v[10:11], v[10:11], v[2:3]
	v_pk_add_f32 v[2:3], v[8:9], v[0:1]
	v_mov_b32_e32 v134, v194
	v_mov_b32_e32 v130, v192
	s_mov_b32 s24, s8
	s_mov_b32 s22, s14
	s_mov_b64 s[28:29], s[16:17]
	s_mov_b64 s[26:27], s[18:19]
	s_mov_b32 s91, s90
	s_mov_b32 s94, s84
	s_mov_b32 s84, s86
	s_mov_b32 s86, s0
	s_mov_b32 s95, s97
	s_mov_b32 s97, s33
	s_mov_b32 s33, s64
	v_readlane_b32 s64, v255, 32
	v_cvt_pk_bf16_f32 v0, v4, v5
	v_cvt_pk_bf16_f32 v1, v6, v7
	v_cvt_pk_bf16_f32 v2, v2, v3
	v_cvt_pk_bf16_f32 v3, v10, v11
	global_store_dwordx4 v[72:73], v[0:3], off offset:256 sc1
	s_cbranch_vccnz .LBB0_1322

.LBB0_1328:
	v_add_u32_e32 v12, s12, v88
	v_add_u32_e32 v4, 0x45, v12
	v_ashrrev_i32_e32 v13, 31, v12
	v_ashrrev_i32_e32 v5, 31, v4
	v_lshlrev_b64 v[0:1], 13, v[12:13]
	v_lshlrev_b64 v[4:5], 13, v[4:5]
	v_lshl_add_u64 v[0:1], v[64:65], 0, v[0:1]
	v_lshl_add_u64 v[4:5], v[64:65], 0, v[4:5]
	global_load_dwordx4 v[48:51], v[0:1], off nt
	v_add_u32_e32 v8, 0x46, v12
	global_load_dwordx4 v[4:7], v[4:5], off nt
	v_or_b32_e32 v0, 1, v12
	v_ashrrev_i32_e32 v1, 31, v0
	v_ashrrev_i32_e32 v9, 31, v8
	v_lshlrev_b64 v[0:1], 13, v[0:1]
	v_lshlrev_b64 v[8:9], 13, v[8:9]
	v_lshl_add_u64 v[0:1], v[64:65], 0, v[0:1]
	v_lshl_add_u64 v[8:9], v[64:65], 0, v[8:9]
	global_load_dwordx4 v[52:55], v[0:1], off nt
	v_mov_b32_e32 v67, v173
	global_load_dwordx4 v[8:11], v[8:9], off nt
	v_or_b32_e32 v0, 2, v12
	v_ashrrev_i32_e32 v1, 31, v0
	v_lshlrev_b64 v[0:1], 13, v[0:1]
	v_lshl_add_u64 v[0:1], v[64:65], 0, v[0:1]
	global_load_dwordx4 v[56:59], v[0:1], off nt
	v_or_b32_e32 v0, 3, v12
	v_ashrrev_i32_e32 v1, 31, v0
	v_lshlrev_b64 v[0:1], 13, v[0:1]
	v_lshl_add_u64 v[0:1], v[64:65], 0, v[0:1]
	global_load_dwordx4 v[60:63], v[0:1], off nt
	v_or_b32_e32 v0, 4, v12
	v_ashrrev_i32_e32 v1, 31, v0
	v_lshlrev_b64 v[0:1], 13, v[0:1]
	v_lshl_add_u64 v[0:1], v[64:65], 0, v[0:1]
	global_load_dwordx4 v[32:35], v[0:1], off nt
	v_or_b32_e32 v0, 5, v12
	v_ashrrev_i32_e32 v1, 31, v0
	v_lshlrev_b64 v[0:1], 13, v[0:1]
	v_lshl_add_u64 v[0:1], v[64:65], 0, v[0:1]
	global_load_dwordx4 v[36:39], v[0:1], off nt
	v_or_b32_e32 v0, 6, v12
	v_ashrrev_i32_e32 v1, 31, v0
	v_lshlrev_b64 v[0:1], 13, v[0:1]
	v_lshl_add_u64 v[0:1], v[64:65], 0, v[0:1]
	global_load_dwordx4 v[40:43], v[0:1], off nt
	v_or_b32_e32 v0, 7, v12
	v_ashrrev_i32_e32 v1, 31, v0
	v_lshlrev_b64 v[0:1], 13, v[0:1]
	v_lshl_add_u64 v[0:1], v[64:65], 0, v[0:1]
	global_load_dwordx4 v[44:47], v[0:1], off nt
	v_add_u32_e32 v0, 64, v12
	v_ashrrev_i32_e32 v1, 31, v0
	v_lshlrev_b64 v[0:1], 13, v[0:1]
	v_lshl_add_u64 v[0:1], v[64:65], 0, v[0:1]
	global_load_dwordx4 v[16:19], v[0:1], off nt
	v_add_u32_e32 v0, 0x41, v12
	v_ashrrev_i32_e32 v1, 31, v0
	v_lshlrev_b64 v[0:1], 13, v[0:1]
	v_lshl_add_u64 v[0:1], v[64:65], 0, v[0:1]
	global_load_dwordx4 v[20:23], v[0:1], off nt
	v_add_u32_e32 v0, 0x42, v12
	v_ashrrev_i32_e32 v1, 31, v0
	v_lshlrev_b64 v[0:1], 13, v[0:1]
	v_lshl_add_u64 v[0:1], v[64:65], 0, v[0:1]
	global_load_dwordx4 v[24:27], v[0:1], off nt
	v_add_u32_e32 v0, 0x43, v12
	v_ashrrev_i32_e32 v1, 31, v0
	v_lshlrev_b64 v[0:1], 13, v[0:1]
	v_lshl_add_u64 v[0:1], v[64:65], 0, v[0:1]
	global_load_dwordx4 v[28:31], v[0:1], off nt
	v_add_u32_e32 v0, 0x44, v12
	v_ashrrev_i32_e32 v1, 31, v0
	v_lshlrev_b64 v[0:1], 13, v[0:1]
	v_lshl_add_u64 v[0:1], v[64:65], 0, v[0:1]
	global_load_dwordx4 v[0:3], v[0:1], off nt
	v_add_u32_e32 v12, 0x47, v12
	v_ashrrev_i32_e32 v13, 31, v12
	v_lshlrev_b64 v[12:13], 13, v[12:13]
	v_lshl_add_u64 v[12:13], v[64:65], 0, v[12:13]
	global_load_dwordx4 v[12:15], v[12:13], off nt
	v_mov_b32_e32 v66, v173
	s_and_b64 vcc, exec, s[10:11]
	s_mov_b64 s[10:11], 0
	s_waitcnt vmcnt(15)
	v_mul_f32_e32 v48, 0x42000000, v48
	s_waitcnt vmcnt(14)
	v_mul_f32_e32 v4, 0x42000000, v4
	v_mul_f32_e32 v5, 0x42000000, v5
	s_waitcnt vmcnt(13)
	v_mul_f32_e32 v52, 0x42000000, v52
	v_cvt_pk_fp8_f32 v66, v48, v52
	s_waitcnt vmcnt(12)
	v_mul_f32_e32 v8, 0x42000000, v8
	s_waitcnt vmcnt(11)
	v_mul_f32_e32 v48, 0x42000000, v57
	v_mul_f32_e32 v56, 0x42000000, v56
	s_waitcnt vmcnt(10)
	v_mul_f32_e32 v60, 0x42000000, v60
	v_cvt_pk_fp8_f32 v66, v56, v60 op_sel:[0,0,1]
	s_waitcnt vmcnt(9)
	v_mul_f32_e32 v32, 0x42000000, v32
	s_waitcnt vmcnt(8)
	v_mul_f32_e32 v36, 0x42000000, v36
	v_cvt_pk_fp8_f32 v67, v32, v36
	v_mul_f32_e32 v32, 0x42000000, v49
	v_mul_f32_e32 v36, 0x42000000, v53
	v_mul_f32_e32 v49, 0x42000000, v61
	s_waitcnt vmcnt(7)
	v_mul_f32_e32 v40, 0x42000000, v40
	s_waitcnt vmcnt(6)
	v_mul_f32_e32 v44, 0x42000000, v44
	v_cvt_pk_fp8_f32 v67, v40, v44 op_sel:[0,0,1]
	v_mov_b32_e32 v40, v173
	v_cvt_pk_fp8_f32 v40, v32, v36
	v_mul_f32_e32 v32, 0x42000000, v33
	v_mul_f32_e32 v33, 0x42000000, v37
	v_mul_f32_e32 v36, 0x42000000, v41
	v_mov_b32_e32 v41, v173
	v_cvt_pk_fp8_f32 v41, v32, v33
	v_mul_f32_e32 v37, 0x42000000, v45
	v_mul_f32_e32 v32, 0x42000000, v50
	v_mul_f32_e32 v33, 0x42000000, v54
	v_cvt_pk_fp8_f32 v41, v36, v37 op_sel:[0,0,1]
	v_mov_b32_e32 v36, v173
	v_cvt_pk_fp8_f32 v36, v32, v33
	v_mul_f32_e32 v37, 0x42000000, v58
	v_mul_f32_e32 v45, 0x42000000, v62
	v_mul_f32_e32 v32, 0x42000000, v34
	v_cvt_pk_fp8_f32 v36, v37, v45 op_sel:[0,0,1]
	v_mul_f32_e32 v33, 0x42000000, v38
	v_mov_b32_e32 v37, v173
	v_cvt_pk_fp8_f32 v37, v32, v33
	v_mul_f32_e32 v34, 0x42000000, v42
	v_mul_f32_e32 v38, 0x42000000, v46
	v_mul_f32_e32 v33, 0x42000000, v51
	v_cvt_pk_fp8_f32 v37, v34, v38 op_sel:[0,0,1]
	v_mul_f32_e32 v34, 0x42000000, v55
	v_mov_b32_e32 v32, v173
	v_cvt_pk_fp8_f32 v32, v33, v34
	v_mul_f32_e32 v34, 0x42000000, v35
	v_mul_f32_e32 v35, 0x42000000, v39
	v_mov_b32_e32 v33, v173
	v_cvt_pk_fp8_f32 v33, v34, v35
	s_waitcnt vmcnt(1)
	v_mul_f32_e32 v0, 0x42000000, v0
	v_mov_b32_e32 v35, v173
	v_cvt_pk_fp8_f32 v35, v0, v4
	s_waitcnt vmcnt(0)
	v_mul_f32_e32 v12, 0x42000000, v12
	v_mul_f32_e32 v4, 0x42000000, v17
	v_mov_b32_e32 v0, v173
	v_cvt_pk_fp8_f32 v35, v8, v12 op_sel:[0,0,1]
	v_mul_f32_e32 v8, 0x42000000, v21
	v_cvt_pk_fp8_f32 v0, v4, v8
	v_mul_f32_e32 v4, 0x42000000, v1
	v_mov_b32_e32 v1, v173
	v_cvt_pk_fp8_f32 v1, v4, v5
	v_mul_f32_e32 v16, 0x42000000, v16
	v_mul_f32_e32 v20, 0x42000000, v20
	v_mov_b32_e32 v34, v173
	v_cvt_pk_fp8_f32 v34, v16, v20
	v_mul_f32_e32 v12, 0x42000000, v25
	v_mul_f32_e32 v16, 0x42000000, v29
	v_mul_f32_e32 v8, 0x42000000, v9
	v_mul_f32_e32 v9, 0x42000000, v13
	v_cvt_pk_fp8_f32 v40, v48, v49 op_sel:[0,0,1]
	v_cvt_pk_fp8_f32 v0, v12, v16 op_sel:[0,0,1]
	v_cvt_pk_fp8_f32 v1, v8, v9 op_sel:[0,0,1]
	v_add_u32_e32 v44, s12, v79
	v_mul_f32_e32 v4, 0x42000000, v22
	v_mul_f32_e32 v2, 0x42000000, v2
	ds_write2_b64 v44, v[40:41], v[0:1] offset0:34 offset1:42
	v_mul_f32_e32 v1, 0x42000000, v18
	v_mov_b32_e32 v0, v173
	v_cvt_pk_fp8_f32 v0, v1, v4
	v_mul_f32_e32 v4, 0x42000000, v6
	v_mov_b32_e32 v1, v173
	v_cvt_pk_fp8_f32 v1, v2, v4
	v_mul_f32_e32 v5, 0x42000000, v26
	v_mul_f32_e32 v8, 0x42000000, v30
	v_cvt_pk_fp8_f32 v0, v5, v8 op_sel:[0,0,1]
	v_mul_f32_e32 v5, 0x42000000, v10
	v_mul_f32_e32 v6, 0x42000000, v14
	v_cvt_pk_fp8_f32 v1, v5, v6 op_sel:[0,0,1]
	v_mul_f32_e32 v2, 0x42000000, v23
	v_mul_f32_e32 v38, 0x42000000, v59
	v_mul_f32_e32 v42, 0x42000000, v63
	ds_write2_b64 v44, v[36:37], v[0:1] offset0:68 offset1:76
	v_mul_f32_e32 v1, 0x42000000, v19
	v_mov_b32_e32 v0, v173
	v_cvt_pk_fp8_f32 v0, v1, v2
	v_mul_f32_e32 v2, 0x42000000, v3
	v_mul_f32_e32 v3, 0x42000000, v7
	v_mov_b32_e32 v1, v173
	v_cvt_pk_fp8_f32 v1, v2, v3
	v_mul_f32_e32 v4, 0x42000000, v27
	v_mul_f32_e32 v5, 0x42000000, v31
	v_cvt_pk_fp8_f32 v32, v38, v42 op_sel:[0,0,1]
	v_mul_f32_e32 v38, 0x42000000, v43
	v_mul_f32_e32 v39, 0x42000000, v47
	v_mul_f32_e32 v24, 0x42000000, v24
	v_mul_f32_e32 v28, 0x42000000, v28
	v_cvt_pk_fp8_f32 v0, v4, v5 op_sel:[0,0,1]
	v_mul_f32_e32 v4, 0x42000000, v11
	v_mul_f32_e32 v5, 0x42000000, v15
	v_cvt_pk_fp8_f32 v33, v38, v39 op_sel:[0,0,1]
	v_cvt_pk_fp8_f32 v34, v24, v28 op_sel:[0,0,1]
	v_cvt_pk_fp8_f32 v1, v4, v5 op_sel:[0,0,1]
	s_movk_i32 s12, 0x80
	ds_write2_b64 v44, v[66:67], v[34:35] offset1:8
	ds_write2_b64 v44, v[32:33], v[0:1] offset0:102 offset1:110
	s_cbranch_vccnz .LBB0_1328
	s_lshl_b64 s[8:9], s[8:9], 21
	s_add_u32 s8, s95, s8
	s_addc_u32 s9, s97, s9
	s_lshl_b32 s10, s2, 8
	s_waitcnt lgkmcnt(0)
	s_barrier
	s_ashr_i32 s11, s3, 31
	ds_read_b128 v[0:3], v80
	v_add_u32_e32 v4, s10, v71
	s_add_u32 s2, s8, s3
	v_ashrrev_i32_e32 v5, 31, v4
	s_addc_u32 s3, s9, s11
	v_lshlrev_b64 v[4:5], 10, v[4:5]
	v_lshl_add_u64 v[4:5], s[2:3], 0, v[4:5]
	v_lshl_add_u64 v[4:5], v[4:5], 0, v[172:173]
	s_waitcnt lgkmcnt(0)
	global_store_dwordx4 v[4:5], v[0:3], off sc1
	ds_read_b128 v[0:3], v81
	v_add_u32_e32 v4, s10, v72
	v_ashrrev_i32_e32 v5, 31, v4
	v_lshlrev_b64 v[4:5], 10, v[4:5]
	v_lshl_add_u64 v[4:5], s[2:3], 0, v[4:5]
	v_lshl_add_u64 v[4:5], v[4:5], 0, v[172:173]
	s_waitcnt lgkmcnt(0)
	global_store_dwordx4 v[4:5], v[0:3], off sc1
	ds_read_b128 v[0:3], v82
	v_add_u32_e32 v4, s10, v73
	v_ashrrev_i32_e32 v5, 31, v4
	v_lshlrev_b64 v[4:5], 10, v[4:5]
	v_lshl_add_u64 v[4:5], s[2:3], 0, v[4:5]
	v_lshl_add_u64 v[4:5], v[4:5], 0, v[172:173]
	s_waitcnt lgkmcnt(0)
	global_store_dwordx4 v[4:5], v[0:3], off sc1
	ds_read_b128 v[0:3], v83
	v_add_u32_e32 v4, s10, v74
	v_ashrrev_i32_e32 v5, 31, v4
	v_lshlrev_b64 v[4:5], 10, v[4:5]
	v_lshl_add_u64 v[4:5], s[2:3], 0, v[4:5]
	v_lshl_add_u64 v[4:5], v[4:5], 0, v[172:173]
	s_waitcnt lgkmcnt(0)
	global_store_dwordx4 v[4:5], v[0:3], off sc1
	ds_read_b128 v[0:3], v84
	v_add_u32_e32 v4, s10, v75
	v_ashrrev_i32_e32 v5, 31, v4
	v_lshlrev_b64 v[4:5], 10, v[4:5]
	v_lshl_add_u64 v[4:5], s[2:3], 0, v[4:5]
	v_lshl_add_u64 v[4:5], v[4:5], 0, v[172:173]
	s_waitcnt lgkmcnt(0)
	global_store_dwordx4 v[4:5], v[0:3], off sc1
	ds_read_b128 v[0:3], v85
	v_add_u32_e32 v4, s10, v76
	v_ashrrev_i32_e32 v5, 31, v4
	v_lshlrev_b64 v[4:5], 10, v[4:5]
	v_lshl_add_u64 v[4:5], s[2:3], 0, v[4:5]
	v_lshl_add_u64 v[4:5], v[4:5], 0, v[172:173]
	s_waitcnt lgkmcnt(0)
	global_store_dwordx4 v[4:5], v[0:3], off sc1
	ds_read_b128 v[0:3], v86
	v_add_u32_e32 v4, s10, v77
	v_ashrrev_i32_e32 v5, 31, v4
	v_lshlrev_b64 v[4:5], 10, v[4:5]
	v_lshl_add_u64 v[4:5], s[2:3], 0, v[4:5]
	v_lshl_add_u64 v[4:5], v[4:5], 0, v[172:173]
	s_waitcnt lgkmcnt(0)
	global_store_dwordx4 v[4:5], v[0:3], off sc1
	ds_read_b128 v[0:3], v87
	v_add_u32_e32 v4, s10, v78
	v_ashrrev_i32_e32 v5, 31, v4
	v_lshlrev_b64 v[4:5], 10, v[4:5]
	v_lshl_add_u64 v[4:5], s[2:3], 0, v[4:5]
	v_lshl_add_u64 v[4:5], v[4:5], 0, v[172:173]
	s_waitcnt lgkmcnt(0)
	global_store_dwordx4 v[4:5], v[0:3], off sc1
	s_waitcnt lgkmcnt(0)
	s_barrier
	s_movk_i32 s8, 0xc0
	s_mov_b64 s[2:3], 0
	s_andn2_b64 vcc, exec, s[6:7]
	s_cbranch_vccnz .LBB0_1327

.LBB0_1770:
	s_waitcnt vmcnt(1)
	v_lshlrev_b32_e32 v94, 16, v98
	v_and_b32_e32 v95, 0xffff0000, v98
	v_lshlrev_b32_e32 v142, 16, v99
	v_and_b32_e32 v143, 0xffff0000, v99
	v_cvt_f32_fp8_e32 v98, v137
	v_cvt_f32_fp8_sdwa v99, v137 src0_sel:BYTE_1
	v_cvt_f32_fp8_sdwa v144, v137 src0_sel:BYTE_2
	v_cvt_f32_fp8_sdwa v145, v137 src0_sel:BYTE_3
	v_cvt_f32_fp8_e32 v146, v138
	v_cvt_f32_fp8_sdwa v147, v138 src0_sel:BYTE_1
	v_cvt_f32_fp8_sdwa v148, v138 src0_sel:BYTE_2
	v_cvt_f32_fp8_sdwa v149, v138 src0_sel:BYTE_3
	v_cvt_f32_fp8_e32 v150, v139
	v_cvt_f32_fp8_sdwa v151, v139 src0_sel:BYTE_1
	v_cvt_f32_fp8_sdwa v138, v139 src0_sel:BYTE_2
	v_cvt_f32_fp8_sdwa v139, v139 src0_sel:BYTE_3
	v_cvt_f32_fp8_e32 v152, v140
	v_cvt_f32_fp8_sdwa v153, v140 src0_sel:BYTE_1
	v_cvt_f32_fp8_sdwa v154, v140 src0_sel:BYTE_2
	v_cvt_f32_fp8_sdwa v155, v140 src0_sel:BYTE_3
	v_pk_fma_f32 v[98:99], v[40:41], v[98:99], 0 op_sel_hi:[0,1,0]
	v_pk_fma_f32 v[140:141], v[40:41], v[144:145], 0 op_sel_hi:[0,1,0]
	v_pk_fma_f32 v[140:141], v[40:41], v[148:149], v[140:141] op_sel:[1,0,0]
	v_pk_fma_f32 v[98:99], v[40:41], v[146:147], v[98:99] op_sel:[1,0,0]
	v_pk_fma_f32 v[138:139], v[42:43], v[138:139], v[140:141] op_sel_hi:[0,1,1]
	v_pk_fma_f32 v[144:145], v[42:43], v[150:151], v[98:99] op_sel_hi:[0,1,1]
	v_mov_b32_e32 v98, v43
	v_pk_fma_f32 v[138:139], v[98:99], v[154:155], v[138:139] op_sel_hi:[0,1,1]
	v_pk_fma_f32 v[140:141], v[98:99], v[152:153], v[144:145] op_sel_hi:[0,1,1]
	v_pk_mul_f32 v[140:141], v[140:141], s[20:21] op_sel_hi:[1,0]
	v_pk_mul_f32 v[138:139], v[138:139], s[20:21] op_sel_hi:[1,0]
	v_pk_fma_f32 v[76:77], v[140:141], v[76:77], v[94:95]
	v_pk_fma_f32 v[78:79], v[138:139], v[78:79], v[142:143]
	v_cvt_f32_fp8_e32 v140, v133
	v_cvt_f32_fp8_sdwa v141, v133 src0_sel:BYTE_1
	v_cvt_f32_fp8_sdwa v142, v133 src0_sel:BYTE_2
	v_cvt_f32_fp8_sdwa v143, v133 src0_sel:BYTE_3
	v_cvt_f32_fp8_sdwa v146, v134 src0_sel:BYTE_2
	v_cvt_f32_fp8_sdwa v147, v134 src0_sel:BYTE_3
	v_cvt_f32_fp8_e32 v144, v134
	v_cvt_f32_fp8_sdwa v145, v134 src0_sel:BYTE_1
	v_cvt_f32_fp8_e32 v148, v135
	v_cvt_f32_fp8_sdwa v149, v135 src0_sel:BYTE_1
	v_cvt_f32_fp8_sdwa v134, v135 src0_sel:BYTE_2
	v_cvt_f32_fp8_sdwa v135, v135 src0_sel:BYTE_3
	v_cvt_f32_fp8_sdwa v152, v136 src0_sel:BYTE_2
	v_cvt_f32_fp8_sdwa v153, v136 src0_sel:BYTE_3
	v_cvt_f32_fp8_e32 v150, v136
	v_cvt_f32_fp8_sdwa v151, v136 src0_sel:BYTE_1
	v_pk_fma_f32 v[136:137], v[40:41], v[140:141], 0 op_sel_hi:[0,1,0]
	v_pk_fma_f32 v[140:141], v[40:41], v[142:143], 0 op_sel_hi:[0,1,0]
	v_pk_fma_f32 v[140:141], v[40:41], v[146:147], v[140:141] op_sel:[1,0,0]
	v_pk_fma_f32 v[136:137], v[40:41], v[144:145], v[136:137] op_sel:[1,0,0]
	v_pk_fma_f32 v[134:135], v[42:43], v[134:135], v[140:141] op_sel_hi:[0,1,1]
	v_pk_fma_f32 v[136:137], v[42:43], v[148:149], v[136:137] op_sel_hi:[0,1,1]
	v_pk_fma_f32 v[134:135], v[98:99], v[152:153], v[134:135] op_sel_hi:[0,1,1]
	v_lshlrev_b32_e32 v138, 16, v104
	v_and_b32_e32 v139, 0xffff0000, v104
	v_lshlrev_b32_e32 v104, 16, v105
	v_and_b32_e32 v105, 0xffff0000, v105
	v_pk_fma_f32 v[136:137], v[98:99], v[150:151], v[136:137] op_sel_hi:[0,1,1]
	v_pk_mul_f32 v[134:135], v[134:135], s[20:21] op_sel_hi:[1,0]
	v_pk_mul_f32 v[136:137], v[136:137], s[20:21] op_sel_hi:[1,0]
	v_pk_fma_f32 v[74:75], v[134:135], v[74:75], v[104:105]
	v_cvt_f32_fp8_e32 v104, v129
	v_cvt_f32_fp8_sdwa v105, v129 src0_sel:BYTE_1
	v_pk_fma_f32 v[72:73], v[136:137], v[72:73], v[138:139]
	v_cvt_f32_fp8_sdwa v134, v129 src0_sel:BYTE_2
	v_cvt_f32_fp8_sdwa v135, v129 src0_sel:BYTE_3
	v_cvt_f32_fp8_e32 v136, v130
	v_cvt_f32_fp8_sdwa v137, v130 src0_sel:BYTE_1
	v_cvt_f32_fp8_sdwa v138, v130 src0_sel:BYTE_2
	v_cvt_f32_fp8_sdwa v139, v130 src0_sel:BYTE_3
	v_cvt_f32_fp8_e32 v140, v131
	v_cvt_f32_fp8_sdwa v141, v131 src0_sel:BYTE_1
	v_cvt_f32_fp8_sdwa v130, v131 src0_sel:BYTE_2
	v_cvt_f32_fp8_sdwa v131, v131 src0_sel:BYTE_3
	v_cvt_f32_fp8_e32 v142, v132
	v_cvt_f32_fp8_sdwa v143, v132 src0_sel:BYTE_1
	v_cvt_f32_fp8_sdwa v144, v132 src0_sel:BYTE_2
	v_cvt_f32_fp8_sdwa v145, v132 src0_sel:BYTE_3
	v_pk_fma_f32 v[104:105], v[40:41], v[104:105], 0 op_sel_hi:[0,1,0]
	v_pk_fma_f32 v[134:135], v[40:41], v[134:135], 0 op_sel_hi:[0,1,0]
	v_pk_fma_f32 v[104:105], v[40:41], v[136:137], v[104:105] op_sel:[1,0,0]
	v_pk_fma_f32 v[134:135], v[40:41], v[138:139], v[134:135] op_sel:[1,0,0]
	v_pk_fma_f32 v[104:105], v[42:43], v[140:141], v[104:105] op_sel_hi:[0,1,1]
	v_pk_fma_f32 v[130:131], v[42:43], v[130:131], v[134:135] op_sel_hi:[0,1,1]
	v_pk_fma_f32 v[104:105], v[98:99], v[142:143], v[104:105] op_sel_hi:[0,1,1]
	v_lshlrev_b32_e32 v132, 16, v102
	v_and_b32_e32 v133, 0xffff0000, v102
	v_pk_fma_f32 v[130:131], v[98:99], v[144:145], v[130:131] op_sel_hi:[0,1,1]
	v_pk_mul_f32 v[104:105], v[104:105], s[20:21] op_sel_hi:[1,0]
	v_lshlrev_b32_e32 v102, 16, v103
	v_and_b32_e32 v103, 0xffff0000, v103
	v_pk_mul_f32 v[130:131], v[130:131], s[20:21] op_sel_hi:[1,0]
	v_pk_fma_f32 v[68:69], v[104:105], v[68:69], v[132:133]
	v_cvt_f32_fp8_e32 v104, v121
	v_cvt_f32_fp8_sdwa v105, v121 src0_sel:BYTE_1
	v_pk_fma_f32 v[70:71], v[130:131], v[70:71], v[102:103]
	v_cvt_f32_fp8_sdwa v130, v121 src0_sel:BYTE_2
	v_cvt_f32_fp8_sdwa v131, v121 src0_sel:BYTE_3
	v_cvt_f32_fp8_e32 v132, v122
	v_cvt_f32_fp8_sdwa v133, v122 src0_sel:BYTE_1
	v_cvt_f32_fp8_sdwa v134, v122 src0_sel:BYTE_2
	v_cvt_f32_fp8_sdwa v135, v122 src0_sel:BYTE_3
	v_cvt_f32_fp8_e32 v136, v123
	v_cvt_f32_fp8_sdwa v137, v123 src0_sel:BYTE_1
	v_cvt_f32_fp8_sdwa v122, v123 src0_sel:BYTE_2
	v_cvt_f32_fp8_sdwa v123, v123 src0_sel:BYTE_3
	v_cvt_f32_fp8_e32 v138, v124
	v_cvt_f32_fp8_sdwa v139, v124 src0_sel:BYTE_1
	v_cvt_f32_fp8_sdwa v140, v124 src0_sel:BYTE_2
	v_cvt_f32_fp8_sdwa v141, v124 src0_sel:BYTE_3
	v_pk_fma_f32 v[104:105], v[44:45], v[104:105], 0 op_sel_hi:[0,1,0]
	v_pk_fma_f32 v[130:131], v[44:45], v[130:131], 0 op_sel_hi:[0,1,0]
	v_pk_fma_f32 v[104:105], v[44:45], v[132:133], v[104:105] op_sel:[1,0,0]
	v_pk_fma_f32 v[130:131], v[44:45], v[134:135], v[130:131] op_sel:[1,0,0]
	v_pk_fma_f32 v[104:105], v[46:47], v[136:137], v[104:105] op_sel_hi:[0,1,1]
	v_mov_b32_e32 v124, v47
	v_pk_fma_f32 v[122:123], v[46:47], v[122:123], v[130:131] op_sel_hi:[0,1,1]
	v_pk_fma_f32 v[104:105], v[124:125], v[138:139], v[104:105] op_sel_hi:[0,1,1]
	v_cvt_f32_fp8_e32 v136, v117
	v_cvt_f32_fp8_sdwa v137, v117 src0_sel:BYTE_1
	v_cvt_f32_fp8_sdwa v138, v117 src0_sel:BYTE_2
	v_cvt_f32_fp8_sdwa v139, v117 src0_sel:BYTE_3
	v_pk_fma_f32 v[122:123], v[124:125], v[140:141], v[122:123] op_sel_hi:[0,1,1]
	v_cvt_f32_fp8_e32 v140, v118
	v_cvt_f32_fp8_sdwa v141, v118 src0_sel:BYTE_1
	v_cvt_f32_fp8_sdwa v142, v118 src0_sel:BYTE_2
	v_cvt_f32_fp8_sdwa v143, v118 src0_sel:BYTE_3
	v_cvt_f32_fp8_e32 v144, v119
	v_cvt_f32_fp8_sdwa v145, v119 src0_sel:BYTE_1
	v_cvt_f32_fp8_sdwa v118, v119 src0_sel:BYTE_2
	v_cvt_f32_fp8_sdwa v119, v119 src0_sel:BYTE_3
	v_cvt_f32_fp8_e32 v146, v120
	v_cvt_f32_fp8_sdwa v147, v120 src0_sel:BYTE_1
	v_cvt_f32_fp8_sdwa v148, v120 src0_sel:BYTE_2
	v_cvt_f32_fp8_sdwa v149, v120 src0_sel:BYTE_3
	v_pk_fma_f32 v[120:121], v[44:45], v[136:137], 0 op_sel_hi:[0,1,0]
	v_pk_fma_f32 v[136:137], v[44:45], v[138:139], 0 op_sel_hi:[0,1,0]
	v_pk_fma_f32 v[136:137], v[44:45], v[142:143], v[136:137] op_sel:[1,0,0]
	v_pk_fma_f32 v[120:121], v[44:45], v[140:141], v[120:121] op_sel:[1,0,0]
	v_pk_fma_f32 v[118:119], v[46:47], v[118:119], v[136:137] op_sel_hi:[0,1,1]
	v_pk_fma_f32 v[120:121], v[46:47], v[144:145], v[120:121] op_sel_hi:[0,1,1]
	v_pk_fma_f32 v[118:119], v[124:125], v[148:149], v[118:119] op_sel_hi:[0,1,1]
	v_pk_fma_f32 v[120:121], v[124:125], v[146:147], v[120:121] op_sel_hi:[0,1,1]
	v_cvt_f32_fp8_e32 v132, v128
	v_cvt_f32_fp8_sdwa v133, v128 src0_sel:BYTE_1
	v_cvt_f32_fp8_sdwa v134, v128 src0_sel:BYTE_2
	v_cvt_f32_fp8_sdwa v135, v128 src0_sel:BYTE_3
	v_lshlrev_b32_e32 v128, 16, v92
	v_and_b32_e32 v129, 0xffff0000, v92
	v_lshlrev_b32_e32 v92, 16, v93
	v_and_b32_e32 v93, 0xffff0000, v93
	v_pk_mul_f32 v[120:121], v[120:121], s[20:21] op_sel_hi:[1,0]
	v_pk_mul_f32 v[118:119], v[118:119], s[20:21] op_sel_hi:[1,0]
	v_pk_fma_f32 v[60:61], v[120:121], v[60:61], v[128:129]
	v_pk_fma_f32 v[62:63], v[118:119], v[62:63], v[92:93]
	v_cvt_f32_fp8_e32 v118, v113
	v_cvt_f32_fp8_sdwa v119, v113 src0_sel:BYTE_1
	v_cvt_f32_fp8_sdwa v120, v113 src0_sel:BYTE_2
	v_cvt_f32_fp8_sdwa v121, v113 src0_sel:BYTE_3
	v_cvt_f32_fp8_e32 v128, v114
	v_cvt_f32_fp8_sdwa v129, v114 src0_sel:BYTE_1
	v_cvt_f32_fp8_sdwa v136, v114 src0_sel:BYTE_2
	v_cvt_f32_fp8_sdwa v137, v114 src0_sel:BYTE_3
	v_cvt_f32_fp8_e32 v138, v115
	v_cvt_f32_fp8_sdwa v139, v115 src0_sel:BYTE_1
	v_cvt_f32_fp8_sdwa v114, v115 src0_sel:BYTE_2
	v_cvt_f32_fp8_sdwa v115, v115 src0_sel:BYTE_3
	v_cvt_f32_fp8_e32 v140, v116
	v_cvt_f32_fp8_sdwa v141, v116 src0_sel:BYTE_1
	v_cvt_f32_fp8_sdwa v142, v116 src0_sel:BYTE_2
	v_cvt_f32_fp8_sdwa v143, v116 src0_sel:BYTE_3
	v_pk_fma_f32 v[116:117], v[44:45], v[120:121], 0 op_sel_hi:[0,1,0]
	v_pk_fma_f32 v[118:119], v[44:45], v[118:119], 0 op_sel_hi:[0,1,0]
	v_pk_fma_f32 v[118:119], v[44:45], v[128:129], v[118:119] op_sel:[1,0,0]
	v_pk_fma_f32 v[116:117], v[44:45], v[136:137], v[116:117] op_sel:[1,0,0]
	v_lshlrev_b32_e32 v92, 16, v90
	v_pk_fma_f32 v[114:115], v[46:47], v[114:115], v[116:117] op_sel_hi:[0,1,1]
	v_pk_fma_f32 v[116:117], v[46:47], v[138:139], v[118:119] op_sel_hi:[0,1,1]
	v_pk_fma_f32 v[116:117], v[124:125], v[140:141], v[116:117] op_sel_hi:[0,1,1]
	v_pk_fma_f32 v[114:115], v[124:125], v[142:143], v[114:115] op_sel_hi:[0,1,1]
	v_and_b32_e32 v93, 0xffff0000, v90
	v_lshlrev_b32_e32 v90, 16, v91
	v_and_b32_e32 v91, 0xffff0000, v91
	v_pk_mul_f32 v[114:115], v[114:115], s[20:21] op_sel_hi:[1,0]
	v_pk_mul_f32 v[116:117], v[116:117], s[20:21] op_sel_hi:[1,0]
	v_pk_fma_f32 v[54:55], v[114:115], v[54:55], v[90:91]
	v_pk_fma_f32 v[52:53], v[116:117], v[52:53], v[92:93]
	v_cvt_f32_fp8_e32 v90, v109
	v_cvt_f32_fp8_sdwa v91, v109 src0_sel:BYTE_1
	v_cvt_f32_fp8_sdwa v92, v109 src0_sel:BYTE_2
	v_cvt_f32_fp8_sdwa v93, v109 src0_sel:BYTE_3
	v_cvt_f32_fp8_e32 v114, v110
	v_cvt_f32_fp8_sdwa v115, v110 src0_sel:BYTE_1
	v_cvt_f32_fp8_sdwa v116, v110 src0_sel:BYTE_2
	v_cvt_f32_fp8_sdwa v117, v110 src0_sel:BYTE_3
	v_cvt_f32_fp8_e32 v118, v111
	v_cvt_f32_fp8_sdwa v119, v111 src0_sel:BYTE_1
	v_cvt_f32_fp8_sdwa v110, v111 src0_sel:BYTE_2
	v_cvt_f32_fp8_sdwa v111, v111 src0_sel:BYTE_3
	v_cvt_f32_fp8_e32 v120, v112
	v_cvt_f32_fp8_sdwa v121, v112 src0_sel:BYTE_1
	v_cvt_f32_fp8_sdwa v128, v112 src0_sel:BYTE_2
	v_cvt_f32_fp8_sdwa v129, v112 src0_sel:BYTE_3
	v_lshlrev_b32_e32 v102, 16, v100
	v_and_b32_e32 v103, 0xffff0000, v100
	v_lshlrev_b32_e32 v100, 16, v101
	v_and_b32_e32 v101, 0xffff0000, v101
	v_pk_mul_f32 v[104:105], v[104:105], s[20:21] op_sel_hi:[1,0]
	v_pk_mul_f32 v[122:123], v[122:123], s[20:21] op_sel_hi:[1,0]
	v_pk_fma_f32 v[92:93], v[44:45], v[92:93], 0 op_sel_hi:[0,1,0]
	v_pk_fma_f32 v[90:91], v[44:45], v[90:91], 0 op_sel_hi:[0,1,0]
	v_pk_fma_f32 v[66:67], v[122:123], v[66:67], v[100:101]
	v_pk_fma_f32 v[64:65], v[104:105], v[64:65], v[102:103]
	v_cvt_f32_fp8_e32 v100, v125
	v_cvt_f32_fp8_sdwa v101, v125 src0_sel:BYTE_1
	v_cvt_f32_fp8_sdwa v102, v125 src0_sel:BYTE_2
	v_cvt_f32_fp8_sdwa v103, v125 src0_sel:BYTE_3
	v_pk_fma_f32 v[90:91], v[44:45], v[114:115], v[90:91] op_sel:[1,0,0]
	v_pk_fma_f32 v[44:45], v[44:45], v[116:117], v[92:93] op_sel:[1,0,0]
	v_cvt_f32_fp8_e32 v104, v126
	v_cvt_f32_fp8_sdwa v105, v126 src0_sel:BYTE_1
	v_cvt_f32_fp8_sdwa v122, v126 src0_sel:BYTE_2
	v_cvt_f32_fp8_sdwa v123, v126 src0_sel:BYTE_3
	v_pk_fma_f32 v[44:45], v[46:47], v[110:111], v[44:45] op_sel_hi:[0,1,1]
	v_pk_fma_f32 v[46:47], v[46:47], v[118:119], v[90:91] op_sel_hi:[0,1,1]
	v_cvt_f32_fp8_e32 v130, v127
	v_cvt_f32_fp8_sdwa v131, v127 src0_sel:BYTE_1
	v_pk_fma_f32 v[46:47], v[124:125], v[120:121], v[46:47] op_sel_hi:[0,1,1]
	v_pk_fma_f32 v[44:45], v[124:125], v[128:129], v[44:45] op_sel_hi:[0,1,1]
	v_lshlrev_b32_e32 v112, 16, v88
	v_and_b32_e32 v113, 0xffff0000, v88
	v_lshlrev_b32_e32 v88, 16, v89
	v_and_b32_e32 v89, 0xffff0000, v89
	v_pk_mul_f32 v[44:45], v[44:45], s[20:21] op_sel_hi:[1,0]
	v_pk_mul_f32 v[46:47], v[46:47], s[20:21] op_sel_hi:[1,0]
	v_cvt_f32_fp8_sdwa v126, v127 src0_sel:BYTE_2
	v_cvt_f32_fp8_sdwa v127, v127 src0_sel:BYTE_3
	v_pk_fma_f32 v[46:47], v[46:47], v[48:49], v[112:113]
	v_pk_fma_f32 v[44:45], v[44:45], v[50:51], v[88:89]
	v_pk_fma_f32 v[48:49], v[40:41], v[100:101], 0 op_sel_hi:[0,1,0]
	v_pk_fma_f32 v[50:51], v[40:41], v[102:103], 0 op_sel_hi:[0,1,0]
	v_pk_fma_f32 v[50:51], v[40:41], v[122:123], v[50:51] op_sel:[1,0,0]
	v_pk_fma_f32 v[40:41], v[40:41], v[104:105], v[48:49] op_sel:[1,0,0]
	s_waitcnt vmcnt(0)
	v_lshlrev_b32_e32 v94, 16, v96
	v_pk_fma_f32 v[40:41], v[42:43], v[130:131], v[40:41] op_sel_hi:[0,1,1]
	v_pk_fma_f32 v[40:41], v[98:99], v[132:133], v[40:41] op_sel_hi:[0,1,1]
	v_pk_fma_f32 v[42:43], v[42:43], v[126:127], v[50:51] op_sel_hi:[0,1,1]
	v_pk_mul_f32 v[48:49], v[40:41], s[20:21] op_sel_hi:[1,0]
	v_pk_mul_f32 v[40:41], v[44:45], v[44:45]
	v_pk_mul_f32 v[50:51], v[46:47], v[46:47]
	v_and_b32_e32 v95, 0xffff0000, v96
	v_pk_mov_b32 v[88:89], v[50:51], v[40:41] op_sel:[1,0]
	v_mov_b32_e32 v51, v41
	v_pk_add_f32 v[40:41], v[88:89], v[50:51]
	v_pk_mul_f32 v[50:51], v[54:55], v[54:55]
	v_pk_mul_f32 v[88:89], v[52:53], v[52:53]
	v_pk_add_f32 v[40:41], v[40:41], v[40:41] op_sel:[0,1] op_sel_hi:[1,0]
	v_pk_mov_b32 v[90:91], v[88:89], v[50:51] op_sel:[1,0]
	v_mov_b32_e32 v89, v51
	v_pk_add_f32 v[50:51], v[90:91], v[88:89]
	v_mul_f32_e32 v88, v64, v64
	v_mul_f32_e32 v89, v65, v65
	v_pk_add_f32 v[50:51], v[50:51], v[50:51] op_sel:[0,1] op_sel_hi:[1,0]
	v_mov_b32_e32 v41, v88
	v_mov_b32_e32 v51, v89
	v_pk_add_f32 v[40:41], v[40:41], v[50:51]
	v_mul_f32_e32 v50, v61, v61
	v_mul_f32_e32 v88, v63, v63
	v_mul_f32_e32 v90, v66, v66
	v_mul_f32_e32 v91, v67, v67
	v_pk_fma_f32 v[50:51], v[60:61], v[60:61], v[50:51] op_sel_hi:[1,1,0]
	v_pk_fma_f32 v[88:89], v[62:63], v[62:63], v[88:89] op_sel_hi:[1,1,0]
	v_mov_b32_e32 v51, v90
	v_mov_b32_e32 v89, v91
	v_pk_add_f32 v[50:51], v[50:51], v[88:89]
	v_pk_fma_f32 v[42:43], v[98:99], v[134:135], v[42:43] op_sel_hi:[0,1,1]
	v_pk_add_f32 v[40:41], v[40:41], v[50:51]
	s_ashr_i32 s25, s24, 31
	v_add_f32_e32 v40, v40, v41
	v_mov_b32_e32 v41, 0
	v_lshlrev_b32_e32 v96, 16, v97
	v_add_f32_dpp v40, v40, v40 quad_perm:[1,0,3,2] row_mask:0xf bank_mask:0xf bound_ctrl:1
	v_and_b32_e32 v97, 0xffff0000, v97
	s_nop 0
	v_add_f32_dpp v40, v40, v40 quad_perm:[2,3,0,1] row_mask:0xf bank_mask:0xf bound_ctrl:1
	s_nop 1
	v_add_f32_dpp v40, v40, v40 row_half_mirror row_mask:0xf bank_mask:0xf bound_ctrl:1
	s_nop 1
	v_add_f32_dpp v40, v40, v40 row_mirror row_mask:0xf bank_mask:0xf bound_ctrl:1
	s_nop 1
	v_mov_b32_dpp v41, v40 row_bcast:15 row_mask:0xa bank_mask:0xf
	v_add_f32_e32 v40, v40, v41
	v_mov_b32_e32 v41, 0
	s_nop 1
	v_mov_b32_dpp v41, v40 row_bcast:31 row_mask:0xc bank_mask:0xf
	v_add_f32_e32 v40, v40, v41
	s_nop 0
	v_readlane_b32 s0, v40, 63
	s_nop 1
	v_fma_f32 v40, s0, v108, v107
	v_mul_f32_e32 v41, 0x4b800000, v40
	v_cmp_gt_f32_e32 vcc, s34, v40
	s_lshl_b64 s[0:1], s[24:25], 12
	s_nop 0
	v_cndmask_b32_e32 v40, v40, v41, vcc
	v_rsq_f32_e32 v50, v40
	v_pk_mul_f32 v[40:41], v[42:43], s[20:21] op_sel_hi:[1,0]
	v_pk_fma_f32 v[42:43], v[48:49], v[56:57], v[94:95]
	v_pk_fma_f32 v[40:41], v[40:41], v[58:59], v[96:97]
	v_mul_f32_e32 v48, 0x45800000, v50
	v_cndmask_b32_e32 v48, v50, v48, vcc
	v_pk_mul_f32 v[56:57], v[46:47], v[48:49] op_sel_hi:[1,0]
	v_pk_mul_f32 v[44:45], v[44:45], v[48:49] op_sel_hi:[1,0]
	v_lshl_add_u64 v[50:51], v[84:85], 0, s[0:1]
	v_pk_mul_f32 v[46:47], v[2:3], v[44:45]
	v_pk_mul_f32 v[44:45], v[0:1], v[56:57]
	global_store_dwordx4 v[50:51], v[44:47], off sc1
	s_andn2_b64 vcc, exec, s[26:27]
	s_nop 0
	v_pk_mul_f32 v[44:45], v[52:53], v[48:49] op_sel_hi:[1,0]
	v_pk_mul_f32 v[46:47], v[54:55], v[48:49] op_sel_hi:[1,0]
	v_pk_mul_f32 v[44:45], v[4:5], v[44:45]
	v_pk_mul_f32 v[46:47], v[6:7], v[46:47]
	global_store_dwordx4 v[50:51], v[44:47], off offset:1024 sc1
	s_nop 1
	v_pk_mul_f32 v[44:45], v[60:61], v[48:49] op_sel_hi:[1,0]
	v_pk_mul_f32 v[46:47], v[62:63], v[48:49] op_sel_hi:[1,0]
	v_pk_mul_f32 v[44:45], v[8:9], v[44:45]
	v_pk_mul_f32 v[46:47], v[10:11], v[46:47]
	global_store_dwordx4 v[50:51], v[44:47], off offset:2048 sc1
	s_nop 1
	v_pk_mul_f32 v[44:45], v[64:65], v[48:49] op_sel_hi:[1,0]
	v_pk_mul_f32 v[46:47], v[66:67], v[48:49] op_sel_hi:[1,0]
	v_pk_mul_f32 v[44:45], v[12:13], v[44:45]
	v_pk_mul_f32 v[46:47], v[14:15], v[46:47]
	global_store_dwordx4 v[50:51], v[44:47], off offset:3072 sc1
	s_nop 1
	v_mul_f32_e32 v44, v69, v69
	v_mul_f32_e32 v45, v71, v71
	v_fmac_f32_e32 v44, v68, v68
	v_fmac_f32_e32 v45, v70, v70
	v_add_f32_e32 v44, v44, v45
	v_mul_f32_e32 v45, v73, v73
	v_mul_f32_e32 v46, v75, v75
	v_fmac_f32_e32 v45, v72, v72
	v_fmac_f32_e32 v46, v74, v74
	v_add_f32_e32 v45, v45, v46
	v_add_f32_e32 v44, v44, v45
	v_mul_f32_e32 v45, v77, v77
	v_mul_f32_e32 v46, v79, v79
	v_fmac_f32_e32 v45, v76, v76
	v_fmac_f32_e32 v46, v78, v78
	v_add_f32_e32 v45, v45, v46
	v_add_f32_e32 v44, v44, v45
	v_mul_f32_e32 v45, v43, v43
	v_mul_f32_e32 v46, v41, v41
	v_fmac_f32_e32 v45, v42, v42
	v_fmac_f32_e32 v46, v40, v40
	v_add_f32_e32 v45, v45, v46
	v_add_f32_e32 v44, v44, v45
	v_mov_b32_e32 v45, 0
	s_nop 0
	v_add_f32_dpp v44, v44, v44 quad_perm:[1,0,3,2] row_mask:0xf bank_mask:0xf bound_ctrl:1
	s_nop 1
	v_add_f32_dpp v44, v44, v44 quad_perm:[2,3,0,1] row_mask:0xf bank_mask:0xf bound_ctrl:1
	s_nop 1
	v_add_f32_dpp v44, v44, v44 row_half_mirror row_mask:0xf bank_mask:0xf bound_ctrl:1
	s_nop 1
	v_add_f32_dpp v44, v44, v44 row_mirror row_mask:0xf bank_mask:0xf bound_ctrl:1
	s_nop 1
	v_mov_b32_dpp v45, v44 row_bcast:15 row_mask:0xa bank_mask:0xf
	v_add_f32_e32 v44, v44, v45
	v_mov_b32_e32 v45, 0
	s_nop 1
	v_mov_b32_dpp v45, v44 row_bcast:31 row_mask:0xc bank_mask:0xf
	v_add_f32_e32 v44, v44, v45
	s_nop 0
	v_readlane_b32 s0, v44, 63
	s_cbranch_vccnz .LBB0_1753
	s_nop 0
	v_fma_f32 v44, s0, v108, v107
	v_mul_f32_e32 v45, 0x4b800000, v44
	v_cmp_gt_f32_e32 vcc, s34, v44
	s_add_i32 s0, s24, 8
	s_ashr_i32 s1, s0, 31
	v_cndmask_b32_e32 v44, v44, v45, vcc
	v_rsq_f32_e32 v44, v44
	s_lshl_b64 s[0:1], s[0:1], 12
	v_lshl_add_u64 v[50:51], v[84:85], 0, s[0:1]
	v_mul_f32_e32 v45, 0x45800000, v44
	v_cndmask_b32_e32 v48, v44, v45, vcc
	v_pk_mul_f32 v[44:45], v[68:69], v[48:49] op_sel_hi:[1,0]
	v_pk_mul_f32 v[46:47], v[70:71], v[48:49] op_sel_hi:[1,0]
	v_pk_mul_f32 v[44:45], v[0:1], v[44:45]
	v_pk_mul_f32 v[46:47], v[2:3], v[46:47]
	global_store_dwordx4 v[50:51], v[44:47], off sc1
	v_pk_mul_f32 v[40:41], v[40:41], v[48:49] op_sel_hi:[1,0]
	s_nop 0
	v_pk_mul_f32 v[44:45], v[72:73], v[48:49] op_sel_hi:[1,0]
	v_pk_mul_f32 v[46:47], v[74:75], v[48:49] op_sel_hi:[1,0]
	v_pk_mul_f32 v[44:45], v[4:5], v[44:45]
	v_pk_mul_f32 v[46:47], v[6:7], v[46:47]
	global_store_dwordx4 v[50:51], v[44:47], off offset:1024 sc1
	s_nop 1
	v_pk_mul_f32 v[44:45], v[76:77], v[48:49] op_sel_hi:[1,0]
	v_pk_mul_f32 v[46:47], v[78:79], v[48:49] op_sel_hi:[1,0]
	v_pk_mul_f32 v[44:45], v[8:9], v[44:45]
	v_pk_mul_f32 v[46:47], v[10:11], v[46:47]
	global_store_dwordx4 v[50:51], v[44:47], off offset:2048 sc1
	s_nop 1
	v_pk_mul_f32 v[44:45], v[42:43], v[48:49] op_sel_hi:[1,0]
	v_pk_mul_f32 v[42:43], v[14:15], v[40:41]
	v_pk_mul_f32 v[40:41], v[12:13], v[44:45]
	global_store_dwordx4 v[50:51], v[40:43], off offset:3072 sc1
	s_branch .LBB0_1753
